# GEMM unit loops: accumulators start from C=0 MFMAs of a peeled first K-tile instead of 128 v_mov; wait-state pads after the fp8 K-loops removed
# speedup vs baseline: 1.0338x; 1.0074x over previous
.LBB0_185:
	s_ashr_i32 s23, s22, 31
	s_lshl_b64 s[24:25], s[22:23], 19
	s_add_u32 s24, s19, s24
	s_addc_u32 s25, s33, s25
	s_and_b64 s[26:27], s[4:5], exec
	s_cselect_b32 s7, s25, s35
	s_cselect_b32 s9, s24, s34
	s_ashr_i32 s21, s20, 31
	s_lshl_b64 s[26:27], s[20:21], 19
	s_add_u32 s26, s38, s26
	s_addc_u32 s27, s39, s27
	s_and_b64 s[36:37], s[4:5], exec
	s_cselect_b32 s21, s27, s31
	s_cselect_b32 s23, s26, s30
	s_add_u32 s53, s30, 0x4000
	s_addc_u32 s54, s31, 0
	s_add_u32 s30, s34, 0x40080
	s_addc_u32 s31, s35, 0
	s_mov_b32 s55, -2
	ds_read_b128 v[26:29], v191
	ds_read_b128 v[30:33], v191 offset:1024
	ds_read_b128 v[18:21], v191 offset:2048
	ds_read_b128 v[22:25], v191 offset:3072
	ds_read_b128 v[10:13], v192
	ds_read_b128 v[14:17], v192 offset:1024
	ds_read_b128 v[2:5], v192 offset:2048
	ds_read_b128 v[6:9], v192 offset:3072
	s_add_u32 s0, s30, 0xfffc0080
	s_addc_u32 s1, s31, -1
	s_cmp_eq_u32 s55, 12
	s_cselect_b32 s37, s7, s1
	s_cselect_b32 s36, s9, s0
	s_cselect_b32 s35, s21, s54
	s_cselect_b32 s34, s23, s53
	v_lshl_add_u64 v[184:185], s[30:31], 0, v[176:177]
	s_add_i32 m0, s29, 0xc000
	ds_read_b128 v[196:199], v193
	ds_read_b128 v[200:203], v193 offset:1024
	ds_read_b128 v[204:207], v193 offset:2048
	ds_read_b128 v[208:211], v193 offset:3072
	ds_read_b128 v[212:215], v193 offset:4096
	ds_read_b128 v[216:219], v193 offset:5120
	ds_read_b128 v[220:223], v193 offset:6144
	ds_read_b128 v[224:227], v193 offset:7168
	global_load_lds_dwordx4 v[184:185], off
	v_lshl_add_u64 v[184:185], s[30:31], 0, v[178:179]
	s_add_i32 m0, s29, 0xe000
	s_nop 0
	global_load_lds_dwordx4 v[184:185], off
	s_waitcnt vmcnt(8)
	s_waitcnt lgkmcnt(0)
	s_barrier
	s_setprio 1
	s_waitcnt lgkmcnt(0)
	v_mfma_scale_f32_16x16x128_f8f6f4 v[158:161], v[26:33], v[196:203], 0, v194, v194 op_sel_hi:[0,0,0]
	v_mfma_scale_f32_16x16x128_f8f6f4 v[154:157], v[18:25], v[196:203], 0, v194, v194 op_sel_hi:[0,0,0]
	v_mfma_scale_f32_16x16x128_f8f6f4 v[142:145], v[26:33], v[204:211], 0, v194, v194 op_sel_hi:[0,0,0]
	v_mfma_scale_f32_16x16x128_f8f6f4 v[138:141], v[18:25], v[204:211], 0, v194, v194 op_sel_hi:[0,0,0]
	v_mfma_scale_f32_16x16x128_f8f6f4 v[126:129], v[26:33], v[212:219], 0, v194, v194 op_sel_hi:[0,0,0]
	v_mfma_scale_f32_16x16x128_f8f6f4 v[122:125], v[18:25], v[212:219], 0, v194, v194 op_sel_hi:[0,0,0]
	v_mfma_scale_f32_16x16x128_f8f6f4 v[110:113], v[26:33], v[220:227], 0, v194, v194 op_sel_hi:[0,0,0]
	v_mfma_scale_f32_16x16x128_f8f6f4 v[106:109], v[18:25], v[220:227], 0, v194, v194 op_sel_hi:[0,0,0]
	s_setprio 0
	s_setprio 1
	v_mfma_scale_f32_16x16x128_f8f6f4 v[150:153], v[10:17], v[196:203], 0, v194, v194 op_sel_hi:[0,0,0]
	v_mfma_scale_f32_16x16x128_f8f6f4 v[146:149], v[2:9], v[196:203], 0, v194, v194 op_sel_hi:[0,0,0]
	v_mfma_scale_f32_16x16x128_f8f6f4 v[134:137], v[10:17], v[204:211], 0, v194, v194 op_sel_hi:[0,0,0]
	v_mfma_scale_f32_16x16x128_f8f6f4 v[130:133], v[2:9], v[204:211], 0, v194, v194 op_sel_hi:[0,0,0]
	v_mfma_scale_f32_16x16x128_f8f6f4 v[118:121], v[10:17], v[212:219], 0, v194, v194 op_sel_hi:[0,0,0]
	v_mfma_scale_f32_16x16x128_f8f6f4 v[114:117], v[2:9], v[212:219], 0, v194, v194 op_sel_hi:[0,0,0]
	v_mfma_scale_f32_16x16x128_f8f6f4 v[102:105], v[10:17], v[220:227], 0, v194, v194 op_sel_hi:[0,0,0]
	v_mfma_scale_f32_16x16x128_f8f6f4 v[98:101], v[2:9], v[220:227], 0, v194, v194 op_sel_hi:[0,0,0]
	s_setprio 0
	s_barrier
	s_add_i32 s0, s49, s40
	v_lshl_add_u64 v[184:185], s[34:35], 0, v[164:165]
	s_mov_b32 m0, s0
	ds_read_b128 v[196:199], v193 offset:16384
	ds_read_b128 v[200:203], v193 offset:17408
	ds_read_b128 v[204:207], v193 offset:18432
	ds_read_b128 v[208:211], v193 offset:19456
	ds_read_b128 v[212:215], v193 offset:20480
	ds_read_b128 v[216:219], v193 offset:21504
	ds_read_b128 v[220:223], v193 offset:22528
	ds_read_b128 v[224:227], v193 offset:23552
	global_load_lds_dwordx4 v[184:185], off
	s_add_i32 m0, s0, 0x2000
	s_add_u32 s56, s34, 0x40000
	v_lshl_add_u64 v[184:185], s[34:35], 0, v[168:169]
	s_addc_u32 s57, s35, 0
	s_add_i32 s0, s50, s40
	global_load_lds_dwordx4 v[184:185], off
	v_lshl_add_u64 v[184:185], s[56:57], 0, v[164:165]
	s_mov_b32 m0, s0
	v_lshl_add_u64 v[186:187], s[36:37], 0, v[166:167]
	global_load_lds_dwordx4 v[184:185], off
	v_lshl_add_u64 v[184:185], s[56:57], 0, v[168:169]
	s_add_i32 m0, s0, 0x2000
	s_nop 0
	global_load_lds_dwordx4 v[184:185], off
	v_lshl_add_u64 v[184:185], s[36:37], 0, v[162:163]
	s_mov_b32 m0, s29
	s_nop 0
	global_load_lds_dwordx4 v[184:185], off
	s_mov_b32 m0, s41
	s_nop 0
	global_load_lds_dwordx4 v[186:187], off
	s_waitcnt vmcnt(8)
	s_waitcnt lgkmcnt(0)
	s_barrier
	s_setprio 1
	s_waitcnt lgkmcnt(0)
	v_mfma_scale_f32_16x16x128_f8f6f4 v[94:97], v[26:33], v[196:203], 0, v194, v194 op_sel_hi:[0,0,0]
	v_mfma_scale_f32_16x16x128_f8f6f4 v[90:93], v[18:25], v[196:203], 0, v194, v194 op_sel_hi:[0,0,0]
	v_mfma_scale_f32_16x16x128_f8f6f4 v[78:81], v[26:33], v[204:211], 0, v194, v194 op_sel_hi:[0,0,0]
	v_mfma_scale_f32_16x16x128_f8f6f4 v[74:77], v[18:25], v[204:211], 0, v194, v194 op_sel_hi:[0,0,0]
	v_mfma_scale_f32_16x16x128_f8f6f4 v[62:65], v[26:33], v[212:219], 0, v194, v194 op_sel_hi:[0,0,0]
	v_mfma_scale_f32_16x16x128_f8f6f4 v[58:61], v[18:25], v[212:219], 0, v194, v194 op_sel_hi:[0,0,0]
	v_mfma_scale_f32_16x16x128_f8f6f4 v[46:49], v[26:33], v[220:227], 0, v194, v194 op_sel_hi:[0,0,0]
	v_mfma_scale_f32_16x16x128_f8f6f4 v[42:45], v[18:25], v[220:227], 0, v194, v194 op_sel_hi:[0,0,0]
	s_setprio 0
	s_setprio 1
	v_mfma_scale_f32_16x16x128_f8f6f4 v[86:89], v[10:17], v[196:203], 0, v194, v194 op_sel_hi:[0,0,0]
	v_mfma_scale_f32_16x16x128_f8f6f4 v[82:85], v[2:9], v[196:203], 0, v194, v194 op_sel_hi:[0,0,0]
	v_mfma_scale_f32_16x16x128_f8f6f4 v[70:73], v[10:17], v[204:211], 0, v194, v194 op_sel_hi:[0,0,0]
	v_mfma_scale_f32_16x16x128_f8f6f4 v[66:69], v[2:9], v[204:211], 0, v194, v194 op_sel_hi:[0,0,0]
	v_mfma_scale_f32_16x16x128_f8f6f4 v[54:57], v[10:17], v[212:219], 0, v194, v194 op_sel_hi:[0,0,0]
	v_mfma_scale_f32_16x16x128_f8f6f4 v[50:53], v[2:9], v[212:219], 0, v194, v194 op_sel_hi:[0,0,0]
	v_mfma_scale_f32_16x16x128_f8f6f4 v[38:41], v[10:17], v[220:227], 0, v194, v194 op_sel_hi:[0,0,0]
	v_mfma_scale_f32_16x16x128_f8f6f4 v[34:37], v[2:9], v[220:227], 0, v194, v194 op_sel_hi:[0,0,0]
	s_setprio 0
	s_barrier
	s_branch .Lmid_186

.Lmid_186:
	s_add_i32 s0, 0, 0x18000
	v_add_u32_e32 v0, s0, v189
	s_add_i32 s1, 0, 0x1c000
	ds_read_b128 v[2:5], v0
	ds_read_b128 v[6:9], v0 offset:1024
	ds_read_b128 v[10:13], v0 offset:2048
	ds_read_b128 v[14:17], v0 offset:3072
	v_add_u32_e32 v0, s1, v189
	ds_read_b128 v[18:21], v0
	ds_read_b128 v[22:25], v0 offset:1024
	ds_read_b128 v[26:29], v0 offset:2048
	ds_read_b128 v[30:33], v0 offset:3072
	s_add_u32 s36, s36, 0x40000
	s_addc_u32 s37, s37, 0
	s_mov_b32 m0, s42
	v_lshl_add_u64 v[228:229], s[36:37], 0, v[162:163]
	ds_read_b128 v[196:199], v193 offset:32768
	ds_read_b128 v[200:203], v193 offset:33792
	ds_read_b128 v[204:207], v193 offset:34816
	ds_read_b128 v[208:211], v193 offset:35840
	ds_read_b128 v[212:215], v193 offset:36864
	ds_read_b128 v[216:219], v193 offset:37888
	ds_read_b128 v[220:223], v193 offset:38912
	ds_read_b128 v[224:227], v193 offset:39936
	global_load_lds_dwordx4 v[228:229], off
	v_lshl_add_u64 v[228:229], s[36:37], 0, v[166:167]
	s_mov_b32 m0, s43
	s_nop 0
	global_load_lds_dwordx4 v[228:229], off
	s_waitcnt vmcnt(8)
	s_waitcnt lgkmcnt(0)
	s_barrier
	s_setprio 1
	s_waitcnt lgkmcnt(0)
	v_mfma_scale_f32_16x16x128_f8f6f4 v[158:161], v[2:9], v[196:203], v[158:161], v194, v194 op_sel_hi:[0,0,0]
	v_mfma_scale_f32_16x16x128_f8f6f4 v[154:157], v[10:17], v[196:203], v[154:157], v194, v194 op_sel_hi:[0,0,0]
	v_mfma_scale_f32_16x16x128_f8f6f4 v[142:145], v[2:9], v[204:211], v[142:145], v194, v194 op_sel_hi:[0,0,0]
	v_mfma_scale_f32_16x16x128_f8f6f4 v[138:141], v[10:17], v[204:211], v[138:141], v194, v194 op_sel_hi:[0,0,0]
	v_mfma_scale_f32_16x16x128_f8f6f4 v[126:129], v[2:9], v[212:219], v[126:129], v194, v194 op_sel_hi:[0,0,0]
	v_mfma_scale_f32_16x16x128_f8f6f4 v[122:125], v[10:17], v[212:219], v[122:125], v194, v194 op_sel_hi:[0,0,0]
	v_mfma_scale_f32_16x16x128_f8f6f4 v[110:113], v[2:9], v[220:227], v[110:113], v194, v194 op_sel_hi:[0,0,0]
	v_mfma_scale_f32_16x16x128_f8f6f4 v[106:109], v[10:17], v[220:227], v[106:109], v194, v194 op_sel_hi:[0,0,0]
	s_setprio 0
	s_setprio 1
	v_mfma_scale_f32_16x16x128_f8f6f4 v[150:153], v[18:25], v[196:203], v[150:153], v194, v194 op_sel_hi:[0,0,0]
	v_mfma_scale_f32_16x16x128_f8f6f4 v[146:149], v[26:33], v[196:203], v[146:149], v194, v194 op_sel_hi:[0,0,0]
	v_mfma_scale_f32_16x16x128_f8f6f4 v[134:137], v[18:25], v[204:211], v[134:137], v194, v194 op_sel_hi:[0,0,0]
	v_mfma_scale_f32_16x16x128_f8f6f4 v[130:133], v[26:33], v[204:211], v[130:133], v194, v194 op_sel_hi:[0,0,0]
	v_mfma_scale_f32_16x16x128_f8f6f4 v[118:121], v[18:25], v[212:219], v[118:121], v194, v194 op_sel_hi:[0,0,0]
	v_mfma_scale_f32_16x16x128_f8f6f4 v[114:117], v[26:33], v[212:219], v[114:117], v194, v194 op_sel_hi:[0,0,0]
	v_mfma_scale_f32_16x16x128_f8f6f4 v[102:105], v[18:25], v[220:227], v[102:105], v194, v194 op_sel_hi:[0,0,0]
	v_mfma_scale_f32_16x16x128_f8f6f4 v[98:101], v[26:33], v[220:227], v[98:101], v194, v194 op_sel_hi:[0,0,0]
	s_setprio 0
	s_barrier
	s_add_u32 s36, s34, 0x2000
	s_addc_u32 s37, s35, 0
	s_add_i32 s0, s0, s40
	v_lshl_add_u64 v[228:229], s[36:37], 0, v[164:165]
	s_mov_b32 m0, s0
	ds_read_b128 v[196:199], v193 offset:49152
	ds_read_b128 v[200:203], v193 offset:50176
	ds_read_b128 v[204:207], v193 offset:51200
	ds_read_b128 v[208:211], v193 offset:52224
	ds_read_b128 v[212:215], v193 offset:53248
	ds_read_b128 v[216:219], v193 offset:54272
	ds_read_b128 v[220:223], v193 offset:55296
	ds_read_b128 v[224:227], v193 offset:56320
	global_load_lds_dwordx4 v[228:229], off
	s_add_i32 m0, s0, 0x2000
	s_add_u32 s34, s34, 0x42000
	v_lshl_add_u64 v[228:229], s[36:37], 0, v[168:169]
	s_addc_u32 s35, s35, 0
	s_add_i32 s0, s1, s40
	global_load_lds_dwordx4 v[228:229], off
	v_lshl_add_u64 v[228:229], s[34:35], 0, v[164:165]
	s_mov_b32 m0, s0
	v_lshl_add_u64 v[184:185], v[184:185], 0, s[12:13]
	global_load_lds_dwordx4 v[228:229], off
	v_lshl_add_u64 v[228:229], s[34:35], 0, v[168:169]
	s_add_i32 m0, s0, 0x2000
	s_nop 0
	global_load_lds_dwordx4 v[228:229], off
	s_mov_b32 m0, s44
	s_nop 0
	global_load_lds_dwordx4 v[184:185], off
	v_lshl_add_u64 v[184:185], v[186:187], 0, s[12:13]
	s_mov_b32 m0, s45
	s_nop 0
	global_load_lds_dwordx4 v[184:185], off
	s_waitcnt vmcnt(8)
	s_waitcnt lgkmcnt(0)
	s_barrier
	s_setprio 1
	s_waitcnt lgkmcnt(0)
	v_mfma_scale_f32_16x16x128_f8f6f4 v[94:97], v[2:9], v[196:203], v[94:97], v194, v194 op_sel_hi:[0,0,0]
	v_mfma_scale_f32_16x16x128_f8f6f4 v[90:93], v[10:17], v[196:203], v[90:93], v194, v194 op_sel_hi:[0,0,0]
	v_mfma_scale_f32_16x16x128_f8f6f4 v[78:81], v[2:9], v[204:211], v[78:81], v194, v194 op_sel_hi:[0,0,0]
	v_mfma_scale_f32_16x16x128_f8f6f4 v[74:77], v[10:17], v[204:211], v[74:77], v194, v194 op_sel_hi:[0,0,0]
	v_mfma_scale_f32_16x16x128_f8f6f4 v[62:65], v[2:9], v[212:219], v[62:65], v194, v194 op_sel_hi:[0,0,0]
	v_mfma_scale_f32_16x16x128_f8f6f4 v[58:61], v[10:17], v[212:219], v[58:61], v194, v194 op_sel_hi:[0,0,0]
	v_mfma_scale_f32_16x16x128_f8f6f4 v[46:49], v[2:9], v[220:227], v[46:49], v194, v194 op_sel_hi:[0,0,0]
	v_mfma_scale_f32_16x16x128_f8f6f4 v[42:45], v[10:17], v[220:227], v[42:45], v194, v194 op_sel_hi:[0,0,0]
	s_setprio 0
	s_setprio 1
	v_mfma_scale_f32_16x16x128_f8f6f4 v[86:89], v[18:25], v[196:203], v[86:89], v194, v194 op_sel_hi:[0,0,0]
	v_mfma_scale_f32_16x16x128_f8f6f4 v[82:85], v[26:33], v[196:203], v[82:85], v194, v194 op_sel_hi:[0,0,0]
	v_mfma_scale_f32_16x16x128_f8f6f4 v[70:73], v[18:25], v[204:211], v[70:73], v194, v194 op_sel_hi:[0,0,0]
	v_mfma_scale_f32_16x16x128_f8f6f4 v[66:69], v[26:33], v[204:211], v[66:69], v194, v194 op_sel_hi:[0,0,0]
	v_mfma_scale_f32_16x16x128_f8f6f4 v[54:57], v[18:25], v[212:219], v[54:57], v194, v194 op_sel_hi:[0,0,0]
	v_mfma_scale_f32_16x16x128_f8f6f4 v[50:53], v[26:33], v[212:219], v[50:53], v194, v194 op_sel_hi:[0,0,0]
	v_mfma_scale_f32_16x16x128_f8f6f4 v[38:41], v[18:25], v[220:227], v[38:41], v194, v194 op_sel_hi:[0,0,0]
	v_mfma_scale_f32_16x16x128_f8f6f4 v[34:37], v[26:33], v[220:227], v[34:37], v194, v194 op_sel_hi:[0,0,0]
	s_setprio 0
	s_barrier
	s_add_i32 s55, s55, 2
	s_add_u32 s53, s53, 0x4000
	s_addc_u32 s54, s54, 0
	s_add_u32 s30, s30, 0x100
	s_addc_u32 s31, s31, 0
	s_cmp_gt_u32 s55, 13
	s_cbranch_scc0 .LBB0_186
	s_and_b64 vcc, exec, s[14:15]
	s_cbranch_vccz .LBB0_189
	s_barrier
.LBB0_189:
	s_cmp_lt_i32 s28, 64
	v_lshl_add_u32 v18, s6, 8, v188
	s_cselect_b64 s[6:7], -1, 0
	s_lshl_b64 s[30:31], 1, s28
	s_and_b32 s9, s31, 0x333ff
	s_cmp_lg_u64 s[8:9], 0
	s_cselect_b64 s[30:31], -1, 0
	s_and_b64 s[30:31], s[16:17], s[30:31]
	s_and_b64 s[30:31], s[6:7], s[30:31]
	v_cndmask_b32_e64 v0, 0, 1, s[30:31]
	v_cmp_ne_u32_e64 s[6:7], 1, v0
	s_andn2_b64 vcc, exec, s[30:31]
	v_ashrrev_i32_e32 v19, 31, v18
	s_cbranch_vccnz .LBB0_191
	v_lshlrev_b64 v[2:3], 6, v[18:19]
	v_lshl_add_u64 v[6:7], v[172:173], 0, v[2:3]
	v_lshl_add_u64 v[8:9], v[174:175], 0, v[2:3]
	global_load_dwordx4 v[2:5], v[6:7], off offset:16
	global_load_dwordx4 v[14:17], v[6:7], off
	global_load_dwordx4 v[10:13], v[8:9], off
	s_nop 0
	global_load_dwordx4 v[6:9], v[8:9], off offset:16
	s_branch .LBB0_192

.LBB0_1128:
	s_ashr_i32 s21, s20, 31
	s_lshl_b64 s[0:1], s[20:21], 20
	s_add_u32 s22, s36, s0
	s_addc_u32 s23, s37, s1
	s_and_b64 s[0:1], s[4:5], exec
	s_cselect_b32 s21, s23, s31
	s_cselect_b32 s52, s22, s30
	s_ashr_i32 s19, s18, 31
	s_lshl_b64 s[0:1], s[18:19], 20
	s_add_u32 s24, s38, s0
	s_addc_u32 s25, s39, s1
	s_and_b64 s[0:1], s[4:5], exec
	s_cselect_b32 s19, s25, s29
	s_cselect_b32 s53, s24, s28
	s_add_u32 s54, s28, 0x4000
	s_addc_u32 s55, s29, 0
	s_add_u32 s28, s30, 0x80080
	s_addc_u32 s29, s31, 0
	s_mov_b32 s56, -2
	ds_read_b128 v[146:149], v164
	ds_read_b128 v[150:153], v164 offset:1024
	ds_read_b128 v[168:171], v164 offset:2048
	ds_read_b128 v[172:175], v164 offset:3072
	ds_read_b128 v[176:179], v165
	ds_read_b128 v[180:183], v165 offset:1024
	ds_read_b128 v[184:187], v165 offset:2048
	ds_read_b128 v[188:191], v165 offset:3072
	s_add_u32 s0, s28, 0xfff80080
	s_addc_u32 s1, s29, -1
	s_cmp_eq_u32 s56, 28
	s_cselect_b32 s35, s21, s1
	s_cselect_b32 s34, s52, s0
	s_cselect_b32 s31, s19, s55
	s_cselect_b32 s30, s53, s54
	v_lshl_add_u64 v[224:225], s[28:29], 0, v[138:139]
	s_add_i32 m0, s27, 0xc000
	ds_read_b128 v[192:195], v166
	ds_read_b128 v[196:199], v166 offset:1024
	ds_read_b128 v[200:203], v166 offset:2048
	ds_read_b128 v[204:207], v166 offset:3072
	ds_read_b128 v[208:211], v166 offset:4096
	ds_read_b128 v[212:215], v166 offset:5120
	ds_read_b128 v[216:219], v166 offset:6144
	ds_read_b128 v[220:223], v166 offset:7168
	global_load_lds_dwordx4 v[224:225], off
	v_lshl_add_u64 v[224:225], s[28:29], 0, v[140:141]
	s_add_i32 m0, s27, 0xe000
	s_nop 0
	global_load_lds_dwordx4 v[224:225], off
	s_waitcnt vmcnt(8)
	s_waitcnt lgkmcnt(0)
	s_barrier
	s_setprio 1
	s_waitcnt lgkmcnt(0)
	v_mfma_f32_16x16x32_bf16 v[126:129], v[146:149], v[192:195], 0
	v_mfma_f32_16x16x32_bf16 v[122:125], v[168:171], v[192:195], 0
	v_mfma_f32_16x16x32_bf16 v[110:113], v[146:149], v[200:203], 0
	v_mfma_f32_16x16x32_bf16 v[106:109], v[168:171], v[200:203], 0
	v_mfma_f32_16x16x32_bf16 v[94:97], v[146:149], v[208:211], 0
	v_mfma_f32_16x16x32_bf16 v[90:93], v[168:171], v[208:211], 0
	v_mfma_f32_16x16x32_bf16 v[78:81], v[146:149], v[216:219], 0
	v_mfma_f32_16x16x32_bf16 v[74:77], v[168:171], v[216:219], 0
	v_mfma_f32_16x16x32_bf16 v[126:129], v[150:153], v[196:199], v[126:129]
	v_mfma_f32_16x16x32_bf16 v[122:125], v[172:175], v[196:199], v[122:125]
	v_mfma_f32_16x16x32_bf16 v[110:113], v[150:153], v[204:207], v[110:113]
	v_mfma_f32_16x16x32_bf16 v[106:109], v[172:175], v[204:207], v[106:109]
	v_mfma_f32_16x16x32_bf16 v[94:97], v[150:153], v[212:215], v[94:97]
	v_mfma_f32_16x16x32_bf16 v[90:93], v[172:175], v[212:215], v[90:93]
	v_mfma_f32_16x16x32_bf16 v[78:81], v[150:153], v[220:223], v[78:81]
	v_mfma_f32_16x16x32_bf16 v[74:77], v[172:175], v[220:223], v[74:77]
	s_setprio 0
	s_setprio 1
	v_mfma_f32_16x16x32_bf16 v[118:121], v[176:179], v[192:195], 0
	v_mfma_f32_16x16x32_bf16 v[114:117], v[184:187], v[192:195], 0
	v_mfma_f32_16x16x32_bf16 v[102:105], v[176:179], v[200:203], 0
	v_mfma_f32_16x16x32_bf16 v[98:101], v[184:187], v[200:203], 0
	v_mfma_f32_16x16x32_bf16 v[86:89], v[176:179], v[208:211], 0
	v_mfma_f32_16x16x32_bf16 v[82:85], v[184:187], v[208:211], 0
	v_mfma_f32_16x16x32_bf16 v[70:73], v[176:179], v[216:219], 0
	v_mfma_f32_16x16x32_bf16 v[66:69], v[184:187], v[216:219], 0
	v_mfma_f32_16x16x32_bf16 v[118:121], v[180:183], v[196:199], v[118:121]
	v_mfma_f32_16x16x32_bf16 v[114:117], v[188:191], v[196:199], v[114:117]
	v_mfma_f32_16x16x32_bf16 v[102:105], v[180:183], v[204:207], v[102:105]
	v_mfma_f32_16x16x32_bf16 v[98:101], v[188:191], v[204:207], v[98:101]
	v_mfma_f32_16x16x32_bf16 v[86:89], v[180:183], v[212:215], v[86:89]
	v_mfma_f32_16x16x32_bf16 v[82:85], v[188:191], v[212:215], v[82:85]
	v_mfma_f32_16x16x32_bf16 v[70:73], v[180:183], v[220:223], v[70:73]
	v_mfma_f32_16x16x32_bf16 v[66:69], v[188:191], v[220:223], v[66:69]
	s_setprio 0
	s_barrier
	s_add_i32 s0, s48, s40
	v_lshl_add_u64 v[224:225], s[30:31], 0, v[132:133]
	s_mov_b32 m0, s0
	ds_read_b128 v[192:195], v166 offset:16384
	ds_read_b128 v[196:199], v166 offset:17408
	ds_read_b128 v[200:203], v166 offset:18432
	ds_read_b128 v[204:207], v166 offset:19456
	ds_read_b128 v[208:211], v166 offset:20480
	ds_read_b128 v[212:215], v166 offset:21504
	ds_read_b128 v[216:219], v166 offset:22528
	ds_read_b128 v[220:223], v166 offset:23552
	global_load_lds_dwordx4 v[224:225], off
	s_add_i32 m0, s0, 0x2000
	s_add_u32 s0, s30, 0x80000
	v_lshl_add_u64 v[224:225], s[30:31], 0, v[136:137]
	s_addc_u32 s1, s31, 0
	s_add_i32 s2, s49, s40
	global_load_lds_dwordx4 v[224:225], off
	v_lshl_add_u64 v[224:225], s[0:1], 0, v[132:133]
	s_mov_b32 m0, s2
	v_lshl_add_u64 v[226:227], s[34:35], 0, v[134:135]
	global_load_lds_dwordx4 v[224:225], off
	v_lshl_add_u64 v[224:225], s[0:1], 0, v[136:137]
	s_add_i32 m0, s2, 0x2000
	s_nop 0
	global_load_lds_dwordx4 v[224:225], off
	v_lshl_add_u64 v[224:225], s[34:35], 0, v[130:131]
	s_mov_b32 m0, s27
	s_nop 0
	global_load_lds_dwordx4 v[224:225], off
	s_mov_b32 m0, s41
	s_nop 0
	global_load_lds_dwordx4 v[226:227], off
	s_waitcnt vmcnt(8)
	s_waitcnt lgkmcnt(0)
	s_barrier
	s_setprio 1
	s_waitcnt lgkmcnt(0)
	v_mfma_f32_16x16x32_bf16 v[62:65], v[146:149], v[192:195], 0
	v_mfma_f32_16x16x32_bf16 v[58:61], v[168:171], v[192:195], 0
	v_mfma_f32_16x16x32_bf16 v[46:49], v[146:149], v[200:203], 0
	v_mfma_f32_16x16x32_bf16 v[42:45], v[168:171], v[200:203], 0
	v_mfma_f32_16x16x32_bf16 v[30:33], v[146:149], v[208:211], 0
	v_mfma_f32_16x16x32_bf16 v[26:29], v[168:171], v[208:211], 0
	v_mfma_f32_16x16x32_bf16 v[14:17], v[146:149], v[216:219], 0
	v_mfma_f32_16x16x32_bf16 v[10:13], v[168:171], v[216:219], 0
	v_mfma_f32_16x16x32_bf16 v[62:65], v[150:153], v[196:199], v[62:65]
	v_mfma_f32_16x16x32_bf16 v[58:61], v[172:175], v[196:199], v[58:61]
	v_mfma_f32_16x16x32_bf16 v[46:49], v[150:153], v[204:207], v[46:49]
	v_mfma_f32_16x16x32_bf16 v[42:45], v[172:175], v[204:207], v[42:45]
	v_mfma_f32_16x16x32_bf16 v[30:33], v[150:153], v[212:215], v[30:33]
	v_mfma_f32_16x16x32_bf16 v[26:29], v[172:175], v[212:215], v[26:29]
	v_mfma_f32_16x16x32_bf16 v[14:17], v[150:153], v[220:223], v[14:17]
	v_mfma_f32_16x16x32_bf16 v[10:13], v[172:175], v[220:223], v[10:13]
	s_setprio 0
	s_setprio 1
	v_mfma_f32_16x16x32_bf16 v[54:57], v[176:179], v[192:195], 0
	v_mfma_f32_16x16x32_bf16 v[50:53], v[184:187], v[192:195], 0
	v_mfma_f32_16x16x32_bf16 v[38:41], v[176:179], v[200:203], 0
	v_mfma_f32_16x16x32_bf16 v[34:37], v[184:187], v[200:203], 0
	v_mfma_f32_16x16x32_bf16 v[22:25], v[176:179], v[208:211], 0
	v_mfma_f32_16x16x32_bf16 v[18:21], v[184:187], v[208:211], 0
	v_mfma_f32_16x16x32_bf16 v[6:9], v[176:179], v[216:219], 0
	v_mfma_f32_16x16x32_bf16 v[2:5], v[184:187], v[216:219], 0
	v_mfma_f32_16x16x32_bf16 v[54:57], v[180:183], v[196:199], v[54:57]
	v_mfma_f32_16x16x32_bf16 v[50:53], v[188:191], v[196:199], v[50:53]
	v_mfma_f32_16x16x32_bf16 v[38:41], v[180:183], v[204:207], v[38:41]
	v_mfma_f32_16x16x32_bf16 v[34:37], v[188:191], v[204:207], v[34:37]
	v_mfma_f32_16x16x32_bf16 v[22:25], v[180:183], v[212:215], v[22:25]
	v_mfma_f32_16x16x32_bf16 v[18:21], v[188:191], v[212:215], v[18:21]
	v_mfma_f32_16x16x32_bf16 v[6:9], v[180:183], v[220:223], v[6:9]
	v_mfma_f32_16x16x32_bf16 v[2:5], v[188:191], v[220:223], v[2:5]
	s_setprio 0
	s_barrier
	s_branch .Lmid_1129

.Lmid_1129:
	s_add_i32 s2, 0, 0x18000
	v_add_u32_e32 v0, s2, v162
	s_add_i32 s3, 0, 0x1c000
	ds_read_b128 v[146:149], v0
	ds_read_b128 v[150:153], v0 offset:1024
	ds_read_b128 v[168:171], v0 offset:2048
	ds_read_b128 v[172:175], v0 offset:3072
	v_add_u32_e32 v0, s3, v162
	ds_read_b128 v[176:179], v0
	ds_read_b128 v[180:183], v0 offset:1024
	ds_read_b128 v[184:187], v0 offset:2048
	ds_read_b128 v[188:191], v0 offset:3072
	s_add_u32 s0, s34, 0x80000
	s_addc_u32 s1, s35, 0
	s_mov_b32 m0, s42
	v_lshl_add_u64 v[228:229], s[0:1], 0, v[130:131]
	ds_read_b128 v[192:195], v166 offset:32768
	ds_read_b128 v[196:199], v166 offset:33792
	ds_read_b128 v[200:203], v166 offset:34816
	ds_read_b128 v[204:207], v166 offset:35840
	ds_read_b128 v[208:211], v166 offset:36864
	ds_read_b128 v[212:215], v166 offset:37888
	ds_read_b128 v[216:219], v166 offset:38912
	ds_read_b128 v[220:223], v166 offset:39936
	global_load_lds_dwordx4 v[228:229], off
	v_lshl_add_u64 v[228:229], s[0:1], 0, v[134:135]
	s_mov_b32 m0, s43
	s_nop 0
	global_load_lds_dwordx4 v[228:229], off
	s_waitcnt vmcnt(8)
	s_waitcnt lgkmcnt(0)
	s_barrier
	s_setprio 1
	s_waitcnt lgkmcnt(0)
	v_mfma_f32_16x16x32_bf16 v[126:129], v[146:149], v[192:195], v[126:129]
	v_mfma_f32_16x16x32_bf16 v[122:125], v[168:171], v[192:195], v[122:125]
	v_mfma_f32_16x16x32_bf16 v[110:113], v[146:149], v[200:203], v[110:113]
	v_mfma_f32_16x16x32_bf16 v[106:109], v[168:171], v[200:203], v[106:109]
	v_mfma_f32_16x16x32_bf16 v[94:97], v[146:149], v[208:211], v[94:97]
	v_mfma_f32_16x16x32_bf16 v[90:93], v[168:171], v[208:211], v[90:93]
	v_mfma_f32_16x16x32_bf16 v[78:81], v[146:149], v[216:219], v[78:81]
	v_mfma_f32_16x16x32_bf16 v[74:77], v[168:171], v[216:219], v[74:77]
	v_mfma_f32_16x16x32_bf16 v[126:129], v[150:153], v[196:199], v[126:129]
	v_mfma_f32_16x16x32_bf16 v[122:125], v[172:175], v[196:199], v[122:125]
	v_mfma_f32_16x16x32_bf16 v[110:113], v[150:153], v[204:207], v[110:113]
	v_mfma_f32_16x16x32_bf16 v[106:109], v[172:175], v[204:207], v[106:109]
	v_mfma_f32_16x16x32_bf16 v[94:97], v[150:153], v[212:215], v[94:97]
	v_mfma_f32_16x16x32_bf16 v[90:93], v[172:175], v[212:215], v[90:93]
	v_mfma_f32_16x16x32_bf16 v[78:81], v[150:153], v[220:223], v[78:81]
	v_mfma_f32_16x16x32_bf16 v[74:77], v[172:175], v[220:223], v[74:77]
	s_setprio 0
	s_setprio 1
	v_mfma_f32_16x16x32_bf16 v[118:121], v[176:179], v[192:195], v[118:121]
	v_mfma_f32_16x16x32_bf16 v[114:117], v[184:187], v[192:195], v[114:117]
	v_mfma_f32_16x16x32_bf16 v[102:105], v[176:179], v[200:203], v[102:105]
	v_mfma_f32_16x16x32_bf16 v[98:101], v[184:187], v[200:203], v[98:101]
	v_mfma_f32_16x16x32_bf16 v[86:89], v[176:179], v[208:211], v[86:89]
	v_mfma_f32_16x16x32_bf16 v[82:85], v[184:187], v[208:211], v[82:85]
	v_mfma_f32_16x16x32_bf16 v[70:73], v[176:179], v[216:219], v[70:73]
	v_mfma_f32_16x16x32_bf16 v[66:69], v[184:187], v[216:219], v[66:69]
	v_mfma_f32_16x16x32_bf16 v[118:121], v[180:183], v[196:199], v[118:121]
	v_mfma_f32_16x16x32_bf16 v[114:117], v[188:191], v[196:199], v[114:117]
	v_mfma_f32_16x16x32_bf16 v[102:105], v[180:183], v[204:207], v[102:105]
	v_mfma_f32_16x16x32_bf16 v[98:101], v[188:191], v[204:207], v[98:101]
	v_mfma_f32_16x16x32_bf16 v[86:89], v[180:183], v[212:215], v[86:89]
	v_mfma_f32_16x16x32_bf16 v[82:85], v[188:191], v[212:215], v[82:85]
	v_mfma_f32_16x16x32_bf16 v[70:73], v[180:183], v[220:223], v[70:73]
	v_mfma_f32_16x16x32_bf16 v[66:69], v[188:191], v[220:223], v[66:69]
	s_setprio 0
	s_barrier
	s_add_u32 s0, s30, 0x2000
	s_addc_u32 s1, s31, 0
	s_add_i32 s2, s2, s40
	v_lshl_add_u64 v[228:229], s[0:1], 0, v[132:133]
	s_mov_b32 m0, s2
	ds_read_b128 v[192:195], v166 offset:49152
	ds_read_b128 v[196:199], v166 offset:50176
	ds_read_b128 v[200:203], v166 offset:51200
	ds_read_b128 v[204:207], v166 offset:52224
	ds_read_b128 v[208:211], v166 offset:53248
	ds_read_b128 v[212:215], v166 offset:54272
	ds_read_b128 v[216:219], v166 offset:55296
	ds_read_b128 v[220:223], v166 offset:56320
	global_load_lds_dwordx4 v[228:229], off
	s_add_i32 m0, s2, 0x2000
	v_lshl_add_u64 v[228:229], s[0:1], 0, v[136:137]
	s_add_u32 s0, s30, 0x82000
	s_addc_u32 s1, s31, 0
	s_add_i32 s2, s3, s40
	global_load_lds_dwordx4 v[228:229], off
	v_lshl_add_u64 v[228:229], s[0:1], 0, v[132:133]
	s_mov_b32 m0, s2
	v_lshl_add_u64 v[224:225], v[224:225], 0, s[12:13]
	global_load_lds_dwordx4 v[228:229], off
	v_lshl_add_u64 v[228:229], s[0:1], 0, v[136:137]
	s_add_i32 m0, s2, 0x2000
	s_nop 0
	global_load_lds_dwordx4 v[228:229], off
	s_mov_b32 m0, s45
	s_nop 0
	global_load_lds_dwordx4 v[224:225], off
	v_lshl_add_u64 v[224:225], v[226:227], 0, s[12:13]
	s_mov_b32 m0, s46
	s_nop 0
	global_load_lds_dwordx4 v[224:225], off
	s_waitcnt vmcnt(8)
	s_waitcnt lgkmcnt(0)
	s_barrier
	s_setprio 1
	s_waitcnt lgkmcnt(0)
	v_mfma_f32_16x16x32_bf16 v[62:65], v[146:149], v[192:195], v[62:65]
	v_mfma_f32_16x16x32_bf16 v[58:61], v[168:171], v[192:195], v[58:61]
	v_mfma_f32_16x16x32_bf16 v[46:49], v[146:149], v[200:203], v[46:49]
	v_mfma_f32_16x16x32_bf16 v[42:45], v[168:171], v[200:203], v[42:45]
	v_mfma_f32_16x16x32_bf16 v[30:33], v[146:149], v[208:211], v[30:33]
	v_mfma_f32_16x16x32_bf16 v[26:29], v[168:171], v[208:211], v[26:29]
	v_mfma_f32_16x16x32_bf16 v[14:17], v[146:149], v[216:219], v[14:17]
	v_mfma_f32_16x16x32_bf16 v[10:13], v[168:171], v[216:219], v[10:13]
	v_mfma_f32_16x16x32_bf16 v[62:65], v[150:153], v[196:199], v[62:65]
	v_mfma_f32_16x16x32_bf16 v[58:61], v[172:175], v[196:199], v[58:61]
	v_mfma_f32_16x16x32_bf16 v[46:49], v[150:153], v[204:207], v[46:49]
	v_mfma_f32_16x16x32_bf16 v[42:45], v[172:175], v[204:207], v[42:45]
	v_mfma_f32_16x16x32_bf16 v[30:33], v[150:153], v[212:215], v[30:33]
	v_mfma_f32_16x16x32_bf16 v[26:29], v[172:175], v[212:215], v[26:29]
	v_mfma_f32_16x16x32_bf16 v[14:17], v[150:153], v[220:223], v[14:17]
	v_mfma_f32_16x16x32_bf16 v[10:13], v[172:175], v[220:223], v[10:13]
	s_setprio 0
	s_setprio 1
	v_mfma_f32_16x16x32_bf16 v[54:57], v[176:179], v[192:195], v[54:57]
	v_mfma_f32_16x16x32_bf16 v[50:53], v[184:187], v[192:195], v[50:53]
	v_mfma_f32_16x16x32_bf16 v[38:41], v[176:179], v[200:203], v[38:41]
	v_mfma_f32_16x16x32_bf16 v[34:37], v[184:187], v[200:203], v[34:37]
	v_mfma_f32_16x16x32_bf16 v[22:25], v[176:179], v[208:211], v[22:25]
	v_mfma_f32_16x16x32_bf16 v[18:21], v[184:187], v[208:211], v[18:21]
	v_mfma_f32_16x16x32_bf16 v[6:9], v[176:179], v[216:219], v[6:9]
	v_mfma_f32_16x16x32_bf16 v[2:5], v[184:187], v[216:219], v[2:5]
	v_mfma_f32_16x16x32_bf16 v[54:57], v[180:183], v[196:199], v[54:57]
	v_mfma_f32_16x16x32_bf16 v[50:53], v[188:191], v[196:199], v[50:53]
	v_mfma_f32_16x16x32_bf16 v[38:41], v[180:183], v[204:207], v[38:41]
	v_mfma_f32_16x16x32_bf16 v[34:37], v[188:191], v[204:207], v[34:37]
	v_mfma_f32_16x16x32_bf16 v[22:25], v[180:183], v[212:215], v[22:25]
	v_mfma_f32_16x16x32_bf16 v[18:21], v[188:191], v[212:215], v[18:21]
	v_mfma_f32_16x16x32_bf16 v[6:9], v[180:183], v[220:223], v[6:9]
	v_mfma_f32_16x16x32_bf16 v[2:5], v[188:191], v[220:223], v[2:5]
	s_setprio 0
	s_barrier
	s_add_i32 s56, s56, 2
	s_add_u32 s54, s54, 0x4000
	s_addc_u32 s55, s55, 0
	s_add_u32 s28, s28, 0x100
	s_addc_u32 s29, s29, 0
	s_cmp_gt_u32 s56, 29
	s_cbranch_scc0 .LBB0_1129
	s_and_b64 vcc, exec, s[14:15]
	s_cbranch_vccz .LBB0_1132
	s_barrier

.LBB0_1152:
	s_ashr_i32 s21, s20, 31
	s_lshl_b64 s[0:1], s[20:21], 20
	s_add_u32 s22, s36, s0
	s_addc_u32 s23, s37, s1
	s_and_b64 s[0:1], s[4:5], exec
	s_cselect_b32 s21, s23, s31
	s_cselect_b32 s52, s22, s30
	s_ashr_i32 s19, s18, 31
	s_lshl_b64 s[0:1], s[18:19], 20
	s_add_u32 s24, s38, s0
	s_addc_u32 s25, s39, s1
	s_and_b64 s[0:1], s[4:5], exec
	s_cselect_b32 s19, s25, s29
	s_cselect_b32 s53, s24, s28
	s_add_u32 s54, s28, 0x4000
	s_addc_u32 s55, s29, 0
	s_add_u32 s28, s30, 0x80080
	s_addc_u32 s29, s31, 0
	s_mov_b32 s56, -2
	ds_read_b128 v[146:149], v1
	ds_read_b128 v[150:153], v1 offset:1024
	ds_read_b128 v[160:163], v1 offset:2048
	ds_read_b128 v[164:167], v1 offset:3072
	ds_read_b128 v[168:171], v154
	ds_read_b128 v[172:175], v154 offset:1024
	ds_read_b128 v[176:179], v154 offset:2048
	ds_read_b128 v[180:183], v154 offset:3072
	s_add_u32 s0, s28, 0xfff80080
	s_addc_u32 s1, s29, -1
	s_cmp_eq_u32 s56, 28
	s_cselect_b32 s35, s21, s1
	s_cselect_b32 s34, s52, s0
	s_cselect_b32 s31, s19, s55
	s_cselect_b32 s30, s53, s54
	v_lshl_add_u64 v[216:217], s[28:29], 0, v[138:139]
	s_add_i32 m0, s27, 0xc000
	ds_read_b128 v[184:187], v155
	ds_read_b128 v[188:191], v155 offset:1024
	ds_read_b128 v[192:195], v155 offset:2048
	ds_read_b128 v[196:199], v155 offset:3072
	ds_read_b128 v[200:203], v155 offset:4096
	ds_read_b128 v[204:207], v155 offset:5120
	ds_read_b128 v[208:211], v155 offset:6144
	ds_read_b128 v[212:215], v155 offset:7168
	global_load_lds_dwordx4 v[216:217], off
	v_lshl_add_u64 v[216:217], s[28:29], 0, v[140:141]
	s_add_i32 m0, s27, 0xe000
	s_nop 0
	global_load_lds_dwordx4 v[216:217], off
	s_waitcnt vmcnt(8)
	s_waitcnt lgkmcnt(0)
	s_barrier
	s_setprio 1
	s_waitcnt lgkmcnt(0)
	v_mfma_f32_16x16x32_bf16 v[126:129], v[146:149], v[184:187], 0
	v_mfma_f32_16x16x32_bf16 v[122:125], v[160:163], v[184:187], 0
	v_mfma_f32_16x16x32_bf16 v[110:113], v[146:149], v[192:195], 0
	v_mfma_f32_16x16x32_bf16 v[106:109], v[160:163], v[192:195], 0
	v_mfma_f32_16x16x32_bf16 v[94:97], v[146:149], v[200:203], 0
	v_mfma_f32_16x16x32_bf16 v[90:93], v[160:163], v[200:203], 0
	v_mfma_f32_16x16x32_bf16 v[78:81], v[146:149], v[208:211], 0
	v_mfma_f32_16x16x32_bf16 v[74:77], v[160:163], v[208:211], 0
	v_mfma_f32_16x16x32_bf16 v[126:129], v[150:153], v[188:191], v[126:129]
	v_mfma_f32_16x16x32_bf16 v[122:125], v[164:167], v[188:191], v[122:125]
	v_mfma_f32_16x16x32_bf16 v[110:113], v[150:153], v[196:199], v[110:113]
	v_mfma_f32_16x16x32_bf16 v[106:109], v[164:167], v[196:199], v[106:109]
	v_mfma_f32_16x16x32_bf16 v[94:97], v[150:153], v[204:207], v[94:97]
	v_mfma_f32_16x16x32_bf16 v[90:93], v[164:167], v[204:207], v[90:93]
	v_mfma_f32_16x16x32_bf16 v[78:81], v[150:153], v[212:215], v[78:81]
	v_mfma_f32_16x16x32_bf16 v[74:77], v[164:167], v[212:215], v[74:77]
	s_setprio 0
	s_setprio 1
	v_mfma_f32_16x16x32_bf16 v[118:121], v[168:171], v[184:187], 0
	v_mfma_f32_16x16x32_bf16 v[114:117], v[176:179], v[184:187], 0
	v_mfma_f32_16x16x32_bf16 v[102:105], v[168:171], v[192:195], 0
	v_mfma_f32_16x16x32_bf16 v[98:101], v[176:179], v[192:195], 0
	v_mfma_f32_16x16x32_bf16 v[86:89], v[168:171], v[200:203], 0
	v_mfma_f32_16x16x32_bf16 v[82:85], v[176:179], v[200:203], 0
	v_mfma_f32_16x16x32_bf16 v[70:73], v[168:171], v[208:211], 0
	v_mfma_f32_16x16x32_bf16 v[66:69], v[176:179], v[208:211], 0
	v_mfma_f32_16x16x32_bf16 v[118:121], v[172:175], v[188:191], v[118:121]
	v_mfma_f32_16x16x32_bf16 v[114:117], v[180:183], v[188:191], v[114:117]
	v_mfma_f32_16x16x32_bf16 v[102:105], v[172:175], v[196:199], v[102:105]
	v_mfma_f32_16x16x32_bf16 v[98:101], v[180:183], v[196:199], v[98:101]
	v_mfma_f32_16x16x32_bf16 v[86:89], v[172:175], v[204:207], v[86:89]
	v_mfma_f32_16x16x32_bf16 v[82:85], v[180:183], v[204:207], v[82:85]
	v_mfma_f32_16x16x32_bf16 v[70:73], v[172:175], v[212:215], v[70:73]
	v_mfma_f32_16x16x32_bf16 v[66:69], v[180:183], v[212:215], v[66:69]
	s_setprio 0
	s_barrier
	s_add_i32 s0, s48, s40
	v_lshl_add_u64 v[216:217], s[30:31], 0, v[132:133]
	s_mov_b32 m0, s0
	ds_read_b128 v[184:187], v155 offset:16384
	ds_read_b128 v[188:191], v155 offset:17408
	ds_read_b128 v[192:195], v155 offset:18432
	ds_read_b128 v[196:199], v155 offset:19456
	ds_read_b128 v[200:203], v155 offset:20480
	ds_read_b128 v[204:207], v155 offset:21504
	ds_read_b128 v[208:211], v155 offset:22528
	ds_read_b128 v[212:215], v155 offset:23552
	global_load_lds_dwordx4 v[216:217], off
	s_add_i32 m0, s0, 0x2000
	s_add_u32 s0, s30, 0x80000
	v_lshl_add_u64 v[216:217], s[30:31], 0, v[136:137]
	s_addc_u32 s1, s31, 0
	s_add_i32 s2, s49, s40
	global_load_lds_dwordx4 v[216:217], off
	v_lshl_add_u64 v[216:217], s[0:1], 0, v[132:133]
	s_mov_b32 m0, s2
	v_lshl_add_u64 v[218:219], s[34:35], 0, v[134:135]
	global_load_lds_dwordx4 v[216:217], off
	v_lshl_add_u64 v[216:217], s[0:1], 0, v[136:137]
	s_add_i32 m0, s2, 0x2000
	s_nop 0
	global_load_lds_dwordx4 v[216:217], off
	v_lshl_add_u64 v[216:217], s[34:35], 0, v[130:131]
	s_mov_b32 m0, s27
	s_nop 0
	global_load_lds_dwordx4 v[216:217], off
	s_mov_b32 m0, s41
	s_nop 0
	global_load_lds_dwordx4 v[218:219], off
	s_waitcnt vmcnt(8)
	s_waitcnt lgkmcnt(0)
	s_barrier
	s_setprio 1
	s_waitcnt lgkmcnt(0)
	v_mfma_f32_16x16x32_bf16 v[62:65], v[146:149], v[184:187], 0
	v_mfma_f32_16x16x32_bf16 v[58:61], v[160:163], v[184:187], 0
	v_mfma_f32_16x16x32_bf16 v[46:49], v[146:149], v[192:195], 0
	v_mfma_f32_16x16x32_bf16 v[42:45], v[160:163], v[192:195], 0
	v_mfma_f32_16x16x32_bf16 v[30:33], v[146:149], v[200:203], 0
	v_mfma_f32_16x16x32_bf16 v[26:29], v[160:163], v[200:203], 0
	v_mfma_f32_16x16x32_bf16 v[14:17], v[146:149], v[208:211], 0
	v_mfma_f32_16x16x32_bf16 v[10:13], v[160:163], v[208:211], 0
	v_mfma_f32_16x16x32_bf16 v[62:65], v[150:153], v[188:191], v[62:65]
	v_mfma_f32_16x16x32_bf16 v[58:61], v[164:167], v[188:191], v[58:61]
	v_mfma_f32_16x16x32_bf16 v[46:49], v[150:153], v[196:199], v[46:49]
	v_mfma_f32_16x16x32_bf16 v[42:45], v[164:167], v[196:199], v[42:45]
	v_mfma_f32_16x16x32_bf16 v[30:33], v[150:153], v[204:207], v[30:33]
	v_mfma_f32_16x16x32_bf16 v[26:29], v[164:167], v[204:207], v[26:29]
	v_mfma_f32_16x16x32_bf16 v[14:17], v[150:153], v[212:215], v[14:17]
	v_mfma_f32_16x16x32_bf16 v[10:13], v[164:167], v[212:215], v[10:13]
	s_setprio 0
	s_setprio 1
	v_mfma_f32_16x16x32_bf16 v[54:57], v[168:171], v[184:187], 0
	v_mfma_f32_16x16x32_bf16 v[50:53], v[176:179], v[184:187], 0
	v_mfma_f32_16x16x32_bf16 v[38:41], v[168:171], v[192:195], 0
	v_mfma_f32_16x16x32_bf16 v[34:37], v[176:179], v[192:195], 0
	v_mfma_f32_16x16x32_bf16 v[22:25], v[168:171], v[200:203], 0
	v_mfma_f32_16x16x32_bf16 v[18:21], v[176:179], v[200:203], 0
	v_mfma_f32_16x16x32_bf16 v[6:9], v[168:171], v[208:211], 0
	v_mfma_f32_16x16x32_bf16 v[2:5], v[176:179], v[208:211], 0
	v_mfma_f32_16x16x32_bf16 v[54:57], v[172:175], v[188:191], v[54:57]
	v_mfma_f32_16x16x32_bf16 v[50:53], v[180:183], v[188:191], v[50:53]
	v_mfma_f32_16x16x32_bf16 v[38:41], v[172:175], v[196:199], v[38:41]
	v_mfma_f32_16x16x32_bf16 v[34:37], v[180:183], v[196:199], v[34:37]
	v_mfma_f32_16x16x32_bf16 v[22:25], v[172:175], v[204:207], v[22:25]
	v_mfma_f32_16x16x32_bf16 v[18:21], v[180:183], v[204:207], v[18:21]
	v_mfma_f32_16x16x32_bf16 v[6:9], v[172:175], v[212:215], v[6:9]
	v_mfma_f32_16x16x32_bf16 v[2:5], v[180:183], v[212:215], v[2:5]
	s_setprio 0
	s_barrier
	s_branch .Lmid_1153

.Lmid_1153:
	s_add_i32 s2, 0, 0x18000
	v_add_u32_e32 v0, s2, v159
	s_add_i32 s3, 0, 0x1c000
	ds_read_b128 v[146:149], v0
	ds_read_b128 v[150:153], v0 offset:1024
	ds_read_b128 v[160:163], v0 offset:2048
	ds_read_b128 v[164:167], v0 offset:3072
	v_add_u32_e32 v0, s3, v159
	ds_read_b128 v[168:171], v0
	ds_read_b128 v[172:175], v0 offset:1024
	ds_read_b128 v[176:179], v0 offset:2048
	ds_read_b128 v[180:183], v0 offset:3072
	s_add_u32 s0, s34, 0x80000
	s_addc_u32 s1, s35, 0
	s_mov_b32 m0, s42
	v_lshl_add_u64 v[220:221], s[0:1], 0, v[130:131]
	ds_read_b128 v[184:187], v155 offset:32768
	ds_read_b128 v[188:191], v155 offset:33792
	ds_read_b128 v[192:195], v155 offset:34816
	ds_read_b128 v[196:199], v155 offset:35840
	ds_read_b128 v[200:203], v155 offset:36864
	ds_read_b128 v[204:207], v155 offset:37888
	ds_read_b128 v[208:211], v155 offset:38912
	ds_read_b128 v[212:215], v155 offset:39936
	global_load_lds_dwordx4 v[220:221], off
	v_lshl_add_u64 v[220:221], s[0:1], 0, v[134:135]
	s_mov_b32 m0, s43
	s_nop 0
	global_load_lds_dwordx4 v[220:221], off
	s_waitcnt vmcnt(8)
	s_waitcnt lgkmcnt(0)
	s_barrier
	s_setprio 1
	s_waitcnt lgkmcnt(0)
	v_mfma_f32_16x16x32_bf16 v[126:129], v[146:149], v[184:187], v[126:129]
	v_mfma_f32_16x16x32_bf16 v[122:125], v[160:163], v[184:187], v[122:125]
	v_mfma_f32_16x16x32_bf16 v[110:113], v[146:149], v[192:195], v[110:113]
	v_mfma_f32_16x16x32_bf16 v[106:109], v[160:163], v[192:195], v[106:109]
	v_mfma_f32_16x16x32_bf16 v[94:97], v[146:149], v[200:203], v[94:97]
	v_mfma_f32_16x16x32_bf16 v[90:93], v[160:163], v[200:203], v[90:93]
	v_mfma_f32_16x16x32_bf16 v[78:81], v[146:149], v[208:211], v[78:81]
	v_mfma_f32_16x16x32_bf16 v[74:77], v[160:163], v[208:211], v[74:77]
	v_mfma_f32_16x16x32_bf16 v[126:129], v[150:153], v[188:191], v[126:129]
	v_mfma_f32_16x16x32_bf16 v[122:125], v[164:167], v[188:191], v[122:125]
	v_mfma_f32_16x16x32_bf16 v[110:113], v[150:153], v[196:199], v[110:113]
	v_mfma_f32_16x16x32_bf16 v[106:109], v[164:167], v[196:199], v[106:109]
	v_mfma_f32_16x16x32_bf16 v[94:97], v[150:153], v[204:207], v[94:97]
	v_mfma_f32_16x16x32_bf16 v[90:93], v[164:167], v[204:207], v[90:93]
	v_mfma_f32_16x16x32_bf16 v[78:81], v[150:153], v[212:215], v[78:81]
	v_mfma_f32_16x16x32_bf16 v[74:77], v[164:167], v[212:215], v[74:77]
	s_setprio 0
	s_setprio 1
	v_mfma_f32_16x16x32_bf16 v[118:121], v[168:171], v[184:187], v[118:121]
	v_mfma_f32_16x16x32_bf16 v[114:117], v[176:179], v[184:187], v[114:117]
	v_mfma_f32_16x16x32_bf16 v[102:105], v[168:171], v[192:195], v[102:105]
	v_mfma_f32_16x16x32_bf16 v[98:101], v[176:179], v[192:195], v[98:101]
	v_mfma_f32_16x16x32_bf16 v[86:89], v[168:171], v[200:203], v[86:89]
	v_mfma_f32_16x16x32_bf16 v[82:85], v[176:179], v[200:203], v[82:85]
	v_mfma_f32_16x16x32_bf16 v[70:73], v[168:171], v[208:211], v[70:73]
	v_mfma_f32_16x16x32_bf16 v[66:69], v[176:179], v[208:211], v[66:69]
	v_mfma_f32_16x16x32_bf16 v[118:121], v[172:175], v[188:191], v[118:121]
	v_mfma_f32_16x16x32_bf16 v[114:117], v[180:183], v[188:191], v[114:117]
	v_mfma_f32_16x16x32_bf16 v[102:105], v[172:175], v[196:199], v[102:105]
	v_mfma_f32_16x16x32_bf16 v[98:101], v[180:183], v[196:199], v[98:101]
	v_mfma_f32_16x16x32_bf16 v[86:89], v[172:175], v[204:207], v[86:89]
	v_mfma_f32_16x16x32_bf16 v[82:85], v[180:183], v[204:207], v[82:85]
	v_mfma_f32_16x16x32_bf16 v[70:73], v[172:175], v[212:215], v[70:73]
	v_mfma_f32_16x16x32_bf16 v[66:69], v[180:183], v[212:215], v[66:69]
	s_setprio 0
	s_barrier
	s_add_u32 s0, s30, 0x2000
	s_addc_u32 s1, s31, 0
	s_add_i32 s2, s2, s40
	v_lshl_add_u64 v[220:221], s[0:1], 0, v[132:133]
	s_mov_b32 m0, s2
	ds_read_b128 v[184:187], v155 offset:49152
	ds_read_b128 v[188:191], v155 offset:50176
	ds_read_b128 v[192:195], v155 offset:51200
	ds_read_b128 v[196:199], v155 offset:52224
	ds_read_b128 v[200:203], v155 offset:53248
	ds_read_b128 v[204:207], v155 offset:54272
	ds_read_b128 v[208:211], v155 offset:55296
	ds_read_b128 v[212:215], v155 offset:56320
	global_load_lds_dwordx4 v[220:221], off
	s_add_i32 m0, s2, 0x2000
	v_lshl_add_u64 v[220:221], s[0:1], 0, v[136:137]
	s_add_u32 s0, s30, 0x82000
	s_addc_u32 s1, s31, 0
	s_add_i32 s2, s3, s40
	global_load_lds_dwordx4 v[220:221], off
	v_lshl_add_u64 v[220:221], s[0:1], 0, v[132:133]
	s_mov_b32 m0, s2
	v_lshl_add_u64 v[216:217], v[216:217], 0, s[12:13]
	global_load_lds_dwordx4 v[220:221], off
	v_lshl_add_u64 v[220:221], s[0:1], 0, v[136:137]
	s_add_i32 m0, s2, 0x2000
	s_nop 0
	global_load_lds_dwordx4 v[220:221], off
	s_mov_b32 m0, s45
	s_nop 0
	global_load_lds_dwordx4 v[216:217], off
	v_lshl_add_u64 v[216:217], v[218:219], 0, s[12:13]
	s_mov_b32 m0, s46
	s_nop 0
	global_load_lds_dwordx4 v[216:217], off
	s_waitcnt vmcnt(8)
	s_waitcnt lgkmcnt(0)
	s_barrier
	s_setprio 1
	s_waitcnt lgkmcnt(0)
	v_mfma_f32_16x16x32_bf16 v[62:65], v[146:149], v[184:187], v[62:65]
	v_mfma_f32_16x16x32_bf16 v[58:61], v[160:163], v[184:187], v[58:61]
	v_mfma_f32_16x16x32_bf16 v[46:49], v[146:149], v[192:195], v[46:49]
	v_mfma_f32_16x16x32_bf16 v[42:45], v[160:163], v[192:195], v[42:45]
	v_mfma_f32_16x16x32_bf16 v[30:33], v[146:149], v[200:203], v[30:33]
	v_mfma_f32_16x16x32_bf16 v[26:29], v[160:163], v[200:203], v[26:29]
	v_mfma_f32_16x16x32_bf16 v[14:17], v[146:149], v[208:211], v[14:17]
	v_mfma_f32_16x16x32_bf16 v[10:13], v[160:163], v[208:211], v[10:13]
	v_mfma_f32_16x16x32_bf16 v[62:65], v[150:153], v[188:191], v[62:65]
	v_mfma_f32_16x16x32_bf16 v[58:61], v[164:167], v[188:191], v[58:61]
	v_mfma_f32_16x16x32_bf16 v[46:49], v[150:153], v[196:199], v[46:49]
	v_mfma_f32_16x16x32_bf16 v[42:45], v[164:167], v[196:199], v[42:45]
	v_mfma_f32_16x16x32_bf16 v[30:33], v[150:153], v[204:207], v[30:33]
	v_mfma_f32_16x16x32_bf16 v[26:29], v[164:167], v[204:207], v[26:29]
	v_mfma_f32_16x16x32_bf16 v[14:17], v[150:153], v[212:215], v[14:17]
	v_mfma_f32_16x16x32_bf16 v[10:13], v[164:167], v[212:215], v[10:13]
	s_setprio 0
	s_setprio 1
	v_mfma_f32_16x16x32_bf16 v[54:57], v[168:171], v[184:187], v[54:57]
	v_mfma_f32_16x16x32_bf16 v[50:53], v[176:179], v[184:187], v[50:53]
	v_mfma_f32_16x16x32_bf16 v[38:41], v[168:171], v[192:195], v[38:41]
	v_mfma_f32_16x16x32_bf16 v[34:37], v[176:179], v[192:195], v[34:37]
	v_mfma_f32_16x16x32_bf16 v[22:25], v[168:171], v[200:203], v[22:25]
	v_mfma_f32_16x16x32_bf16 v[18:21], v[176:179], v[200:203], v[18:21]
	v_mfma_f32_16x16x32_bf16 v[6:9], v[168:171], v[208:211], v[6:9]
	v_mfma_f32_16x16x32_bf16 v[2:5], v[176:179], v[208:211], v[2:5]
	v_mfma_f32_16x16x32_bf16 v[54:57], v[172:175], v[188:191], v[54:57]
	v_mfma_f32_16x16x32_bf16 v[50:53], v[180:183], v[188:191], v[50:53]
	v_mfma_f32_16x16x32_bf16 v[38:41], v[172:175], v[196:199], v[38:41]
	v_mfma_f32_16x16x32_bf16 v[34:37], v[180:183], v[196:199], v[34:37]
	v_mfma_f32_16x16x32_bf16 v[22:25], v[172:175], v[204:207], v[22:25]
	v_mfma_f32_16x16x32_bf16 v[18:21], v[180:183], v[204:207], v[18:21]
	v_mfma_f32_16x16x32_bf16 v[6:9], v[172:175], v[212:215], v[6:9]
	v_mfma_f32_16x16x32_bf16 v[2:5], v[180:183], v[212:215], v[2:5]
	s_setprio 0
	s_barrier
	s_add_i32 s56, s56, 2
	s_add_u32 s54, s54, 0x4000
	s_addc_u32 s55, s55, 0
	s_add_u32 s28, s28, 0x100
	s_addc_u32 s29, s29, 0
	s_cmp_gt_u32 s56, 29
	s_cbranch_scc0 .LBB0_1153
	s_and_b64 vcc, exec, s[14:15]
	s_cbranch_vccz .LBB0_1156
	s_barrier

.LBB0_1227:
	s_ashr_i32 s27, s26, 31
	s_lshl_b64 s[0:1], s[26:27], 20
	s_add_u32 s28, s42, s0
	s_addc_u32 s29, s43, s1
	s_and_b64 s[0:1], s[4:5], exec
	s_cselect_b32 s27, s29, s39
	s_cselect_b32 s57, s28, s38
	s_ashr_i32 s25, s24, 31
	s_lshl_b64 s[0:1], s[24:25], 20
	s_add_u32 s30, s44, s0
	s_addc_u32 s31, s45, s1
	s_and_b64 s[0:1], s[4:5], exec
	s_cselect_b32 s25, s31, s37
	s_cselect_b32 s58, s30, s36
	s_add_u32 s59, s36, 0x4000
	s_addc_u32 s60, s37, 0
	s_add_u32 s36, s38, 0x80080
	s_addc_u32 s37, s39, 0
	s_mov_b32 s61, -2
	ds_read_b128 v[146:149], v154
	ds_read_b128 v[158:161], v154 offset:1024
	ds_read_b128 v[162:165], v154 offset:2048
	ds_read_b128 v[166:169], v154 offset:3072
	ds_read_b128 v[170:173], v155
	ds_read_b128 v[174:177], v155 offset:1024
	ds_read_b128 v[178:181], v155 offset:2048
	ds_read_b128 v[182:185], v155 offset:3072
	s_add_u32 s0, s36, 0xfff80080
	s_addc_u32 s1, s37, -1
	s_cmp_eq_u32 s61, 28
	s_cselect_b32 s41, s27, s1
	s_cselect_b32 s40, s57, s0
	s_cselect_b32 s39, s25, s60
	s_cselect_b32 s38, s58, s59
	v_lshl_add_u64 v[150:151], s[36:37], 0, v[138:139]
	s_add_i32 m0, s35, 0xc000
	ds_read_b128 v[186:189], v156
	ds_read_b128 v[190:193], v156 offset:1024
	ds_read_b128 v[194:197], v156 offset:2048
	ds_read_b128 v[198:201], v156 offset:3072
	ds_read_b128 v[202:205], v156 offset:4096
	ds_read_b128 v[206:209], v156 offset:5120
	ds_read_b128 v[210:213], v156 offset:6144
	ds_read_b128 v[214:217], v156 offset:7168
	global_load_lds_dwordx4 v[150:151], off
	v_lshl_add_u64 v[150:151], s[36:37], 0, v[140:141]
	s_add_i32 m0, s35, 0xe000
	s_nop 0
	global_load_lds_dwordx4 v[150:151], off
	s_waitcnt vmcnt(8)
	s_waitcnt lgkmcnt(0)
	s_barrier
	s_setprio 1
	s_waitcnt lgkmcnt(0)
	v_mfma_f32_16x16x32_bf16 v[126:129], v[146:149], v[186:189], 0
	v_mfma_f32_16x16x32_bf16 v[122:125], v[162:165], v[186:189], 0
	v_mfma_f32_16x16x32_bf16 v[110:113], v[146:149], v[194:197], 0
	v_mfma_f32_16x16x32_bf16 v[106:109], v[162:165], v[194:197], 0
	v_mfma_f32_16x16x32_bf16 v[94:97], v[146:149], v[202:205], 0
	v_mfma_f32_16x16x32_bf16 v[90:93], v[162:165], v[202:205], 0
	v_mfma_f32_16x16x32_bf16 v[78:81], v[146:149], v[210:213], 0
	v_mfma_f32_16x16x32_bf16 v[74:77], v[162:165], v[210:213], 0
	v_mfma_f32_16x16x32_bf16 v[126:129], v[158:161], v[190:193], v[126:129]
	v_mfma_f32_16x16x32_bf16 v[122:125], v[166:169], v[190:193], v[122:125]
	v_mfma_f32_16x16x32_bf16 v[110:113], v[158:161], v[198:201], v[110:113]
	v_mfma_f32_16x16x32_bf16 v[106:109], v[166:169], v[198:201], v[106:109]
	v_mfma_f32_16x16x32_bf16 v[94:97], v[158:161], v[206:209], v[94:97]
	v_mfma_f32_16x16x32_bf16 v[90:93], v[166:169], v[206:209], v[90:93]
	v_mfma_f32_16x16x32_bf16 v[78:81], v[158:161], v[214:217], v[78:81]
	v_mfma_f32_16x16x32_bf16 v[74:77], v[166:169], v[214:217], v[74:77]
	s_setprio 0
	s_setprio 1
	v_mfma_f32_16x16x32_bf16 v[118:121], v[170:173], v[186:189], 0
	v_mfma_f32_16x16x32_bf16 v[114:117], v[178:181], v[186:189], 0
	v_mfma_f32_16x16x32_bf16 v[102:105], v[170:173], v[194:197], 0
	v_mfma_f32_16x16x32_bf16 v[98:101], v[178:181], v[194:197], 0
	v_mfma_f32_16x16x32_bf16 v[86:89], v[170:173], v[202:205], 0
	v_mfma_f32_16x16x32_bf16 v[82:85], v[178:181], v[202:205], 0
	v_mfma_f32_16x16x32_bf16 v[70:73], v[170:173], v[210:213], 0
	v_mfma_f32_16x16x32_bf16 v[66:69], v[178:181], v[210:213], 0
	v_mfma_f32_16x16x32_bf16 v[118:121], v[174:177], v[190:193], v[118:121]
	v_mfma_f32_16x16x32_bf16 v[114:117], v[182:185], v[190:193], v[114:117]
	v_mfma_f32_16x16x32_bf16 v[102:105], v[174:177], v[198:201], v[102:105]
	v_mfma_f32_16x16x32_bf16 v[98:101], v[182:185], v[198:201], v[98:101]
	v_mfma_f32_16x16x32_bf16 v[86:89], v[174:177], v[206:209], v[86:89]
	v_mfma_f32_16x16x32_bf16 v[82:85], v[182:185], v[206:209], v[82:85]
	v_mfma_f32_16x16x32_bf16 v[70:73], v[174:177], v[214:217], v[70:73]
	v_mfma_f32_16x16x32_bf16 v[66:69], v[182:185], v[214:217], v[66:69]
	s_setprio 0
	s_barrier
	s_add_i32 s0, s54, s46
	v_lshl_add_u64 v[150:151], s[38:39], 0, v[132:133]
	s_mov_b32 m0, s0
	ds_read_b128 v[186:189], v156 offset:16384
	ds_read_b128 v[190:193], v156 offset:17408
	ds_read_b128 v[194:197], v156 offset:18432
	ds_read_b128 v[198:201], v156 offset:19456
	ds_read_b128 v[202:205], v156 offset:20480
	ds_read_b128 v[206:209], v156 offset:21504
	ds_read_b128 v[210:213], v156 offset:22528
	ds_read_b128 v[214:217], v156 offset:23552
	global_load_lds_dwordx4 v[150:151], off
	s_add_i32 m0, s0, 0x2000
	s_add_u32 s0, s38, 0x80000
	v_lshl_add_u64 v[150:151], s[38:39], 0, v[136:137]
	s_addc_u32 s1, s39, 0
	s_add_i32 s2, s55, s46
	global_load_lds_dwordx4 v[150:151], off
	v_lshl_add_u64 v[150:151], s[0:1], 0, v[132:133]
	s_mov_b32 m0, s2
	v_lshl_add_u64 v[218:219], s[40:41], 0, v[134:135]
	global_load_lds_dwordx4 v[150:151], off
	v_lshl_add_u64 v[150:151], s[0:1], 0, v[136:137]
	s_add_i32 m0, s2, 0x2000
	s_nop 0
	global_load_lds_dwordx4 v[150:151], off
	v_lshl_add_u64 v[150:151], s[40:41], 0, v[130:131]
	s_mov_b32 m0, s35
	s_nop 0
	global_load_lds_dwordx4 v[150:151], off
	s_mov_b32 m0, s47
	s_nop 0
	global_load_lds_dwordx4 v[218:219], off
	s_waitcnt vmcnt(8)
	s_waitcnt lgkmcnt(0)
	s_barrier
	s_setprio 1
	s_waitcnt lgkmcnt(0)
	v_mfma_f32_16x16x32_bf16 v[62:65], v[146:149], v[186:189], 0
	v_mfma_f32_16x16x32_bf16 v[58:61], v[162:165], v[186:189], 0
	v_mfma_f32_16x16x32_bf16 v[46:49], v[146:149], v[194:197], 0
	v_mfma_f32_16x16x32_bf16 v[42:45], v[162:165], v[194:197], 0
	v_mfma_f32_16x16x32_bf16 v[30:33], v[146:149], v[202:205], 0
	v_mfma_f32_16x16x32_bf16 v[26:29], v[162:165], v[202:205], 0
	v_mfma_f32_16x16x32_bf16 v[14:17], v[146:149], v[210:213], 0
	v_mfma_f32_16x16x32_bf16 v[10:13], v[162:165], v[210:213], 0
	v_mfma_f32_16x16x32_bf16 v[62:65], v[158:161], v[190:193], v[62:65]
	v_mfma_f32_16x16x32_bf16 v[58:61], v[166:169], v[190:193], v[58:61]
	v_mfma_f32_16x16x32_bf16 v[46:49], v[158:161], v[198:201], v[46:49]
	v_mfma_f32_16x16x32_bf16 v[42:45], v[166:169], v[198:201], v[42:45]
	v_mfma_f32_16x16x32_bf16 v[30:33], v[158:161], v[206:209], v[30:33]
	v_mfma_f32_16x16x32_bf16 v[26:29], v[166:169], v[206:209], v[26:29]
	v_mfma_f32_16x16x32_bf16 v[14:17], v[158:161], v[214:217], v[14:17]
	v_mfma_f32_16x16x32_bf16 v[10:13], v[166:169], v[214:217], v[10:13]
	s_setprio 0
	s_setprio 1
	v_mfma_f32_16x16x32_bf16 v[54:57], v[170:173], v[186:189], 0
	v_mfma_f32_16x16x32_bf16 v[50:53], v[178:181], v[186:189], 0
	v_mfma_f32_16x16x32_bf16 v[38:41], v[170:173], v[194:197], 0
	v_mfma_f32_16x16x32_bf16 v[34:37], v[178:181], v[194:197], 0
	v_mfma_f32_16x16x32_bf16 v[22:25], v[170:173], v[202:205], 0
	v_mfma_f32_16x16x32_bf16 v[18:21], v[178:181], v[202:205], 0
	v_mfma_f32_16x16x32_bf16 v[6:9], v[170:173], v[210:213], 0
	v_mfma_f32_16x16x32_bf16 v[2:5], v[178:181], v[210:213], 0
	v_mfma_f32_16x16x32_bf16 v[54:57], v[174:177], v[190:193], v[54:57]
	v_mfma_f32_16x16x32_bf16 v[50:53], v[182:185], v[190:193], v[50:53]
	v_mfma_f32_16x16x32_bf16 v[38:41], v[174:177], v[198:201], v[38:41]
	v_mfma_f32_16x16x32_bf16 v[34:37], v[182:185], v[198:201], v[34:37]
	v_mfma_f32_16x16x32_bf16 v[22:25], v[174:177], v[206:209], v[22:25]
	v_mfma_f32_16x16x32_bf16 v[18:21], v[182:185], v[206:209], v[18:21]
	v_mfma_f32_16x16x32_bf16 v[6:9], v[174:177], v[214:217], v[6:9]
	v_mfma_f32_16x16x32_bf16 v[2:5], v[182:185], v[214:217], v[2:5]
	s_setprio 0
	s_barrier
	s_branch .Lmid_1228

.Lmid_1228:
	s_add_i32 s2, 0, 0x18000
	v_add_u32_e32 v0, s2, v152
	s_add_i32 s3, 0, 0x1c000
	ds_read_b128 v[146:149], v0
	ds_read_b128 v[158:161], v0 offset:1024
	ds_read_b128 v[162:165], v0 offset:2048
	ds_read_b128 v[166:169], v0 offset:3072
	v_add_u32_e32 v0, s3, v152
	ds_read_b128 v[170:173], v0
	ds_read_b128 v[174:177], v0 offset:1024
	ds_read_b128 v[178:181], v0 offset:2048
	ds_read_b128 v[182:185], v0 offset:3072
	s_add_u32 s0, s40, 0x80000
	s_addc_u32 s1, s41, 0
	s_mov_b32 m0, s48
	v_lshl_add_u64 v[220:221], s[0:1], 0, v[130:131]
	ds_read_b128 v[186:189], v156 offset:32768
	ds_read_b128 v[190:193], v156 offset:33792
	ds_read_b128 v[194:197], v156 offset:34816
	ds_read_b128 v[198:201], v156 offset:35840
	ds_read_b128 v[202:205], v156 offset:36864
	ds_read_b128 v[206:209], v156 offset:37888
	ds_read_b128 v[210:213], v156 offset:38912
	ds_read_b128 v[214:217], v156 offset:39936
	global_load_lds_dwordx4 v[220:221], off
	v_lshl_add_u64 v[220:221], s[0:1], 0, v[134:135]
	s_mov_b32 m0, s49
	s_nop 0
	global_load_lds_dwordx4 v[220:221], off
	s_waitcnt vmcnt(8)
	s_waitcnt lgkmcnt(0)
	s_barrier
	s_setprio 1
	s_waitcnt lgkmcnt(0)
	v_mfma_f32_16x16x32_bf16 v[126:129], v[146:149], v[186:189], v[126:129]
	v_mfma_f32_16x16x32_bf16 v[122:125], v[162:165], v[186:189], v[122:125]
	v_mfma_f32_16x16x32_bf16 v[110:113], v[146:149], v[194:197], v[110:113]
	v_mfma_f32_16x16x32_bf16 v[106:109], v[162:165], v[194:197], v[106:109]
	v_mfma_f32_16x16x32_bf16 v[94:97], v[146:149], v[202:205], v[94:97]
	v_mfma_f32_16x16x32_bf16 v[90:93], v[162:165], v[202:205], v[90:93]
	v_mfma_f32_16x16x32_bf16 v[78:81], v[146:149], v[210:213], v[78:81]
	v_mfma_f32_16x16x32_bf16 v[74:77], v[162:165], v[210:213], v[74:77]
	v_mfma_f32_16x16x32_bf16 v[126:129], v[158:161], v[190:193], v[126:129]
	v_mfma_f32_16x16x32_bf16 v[122:125], v[166:169], v[190:193], v[122:125]
	v_mfma_f32_16x16x32_bf16 v[110:113], v[158:161], v[198:201], v[110:113]
	v_mfma_f32_16x16x32_bf16 v[106:109], v[166:169], v[198:201], v[106:109]
	v_mfma_f32_16x16x32_bf16 v[94:97], v[158:161], v[206:209], v[94:97]
	v_mfma_f32_16x16x32_bf16 v[90:93], v[166:169], v[206:209], v[90:93]
	v_mfma_f32_16x16x32_bf16 v[78:81], v[158:161], v[214:217], v[78:81]
	v_mfma_f32_16x16x32_bf16 v[74:77], v[166:169], v[214:217], v[74:77]
	s_setprio 0
	s_setprio 1
	v_mfma_f32_16x16x32_bf16 v[118:121], v[170:173], v[186:189], v[118:121]
	v_mfma_f32_16x16x32_bf16 v[114:117], v[178:181], v[186:189], v[114:117]
	v_mfma_f32_16x16x32_bf16 v[102:105], v[170:173], v[194:197], v[102:105]
	v_mfma_f32_16x16x32_bf16 v[98:101], v[178:181], v[194:197], v[98:101]
	v_mfma_f32_16x16x32_bf16 v[86:89], v[170:173], v[202:205], v[86:89]
	v_mfma_f32_16x16x32_bf16 v[82:85], v[178:181], v[202:205], v[82:85]
	v_mfma_f32_16x16x32_bf16 v[70:73], v[170:173], v[210:213], v[70:73]
	v_mfma_f32_16x16x32_bf16 v[66:69], v[178:181], v[210:213], v[66:69]
	v_mfma_f32_16x16x32_bf16 v[118:121], v[174:177], v[190:193], v[118:121]
	v_mfma_f32_16x16x32_bf16 v[114:117], v[182:185], v[190:193], v[114:117]
	v_mfma_f32_16x16x32_bf16 v[102:105], v[174:177], v[198:201], v[102:105]
	v_mfma_f32_16x16x32_bf16 v[98:101], v[182:185], v[198:201], v[98:101]
	v_mfma_f32_16x16x32_bf16 v[86:89], v[174:177], v[206:209], v[86:89]
	v_mfma_f32_16x16x32_bf16 v[82:85], v[182:185], v[206:209], v[82:85]
	v_mfma_f32_16x16x32_bf16 v[70:73], v[174:177], v[214:217], v[70:73]
	v_mfma_f32_16x16x32_bf16 v[66:69], v[182:185], v[214:217], v[66:69]
	s_setprio 0
	s_barrier
	s_add_u32 s0, s38, 0x2000
	s_addc_u32 s1, s39, 0
	s_add_i32 s2, s2, s46
	v_lshl_add_u64 v[220:221], s[0:1], 0, v[132:133]
	s_mov_b32 m0, s2
	ds_read_b128 v[186:189], v156 offset:49152
	ds_read_b128 v[190:193], v156 offset:50176
	ds_read_b128 v[194:197], v156 offset:51200
	ds_read_b128 v[198:201], v156 offset:52224
	ds_read_b128 v[202:205], v156 offset:53248
	ds_read_b128 v[206:209], v156 offset:54272
	ds_read_b128 v[210:213], v156 offset:55296
	ds_read_b128 v[214:217], v156 offset:56320
	global_load_lds_dwordx4 v[220:221], off
	s_add_i32 m0, s2, 0x2000
	v_lshl_add_u64 v[220:221], s[0:1], 0, v[136:137]
	s_add_u32 s0, s38, 0x82000
	s_addc_u32 s1, s39, 0
	s_add_i32 s2, s3, s46
	global_load_lds_dwordx4 v[220:221], off
	v_lshl_add_u64 v[220:221], s[0:1], 0, v[132:133]
	s_mov_b32 m0, s2
	v_lshl_add_u64 v[150:151], v[150:151], 0, s[12:13]
	global_load_lds_dwordx4 v[220:221], off
	v_lshl_add_u64 v[220:221], s[0:1], 0, v[136:137]
	s_add_i32 m0, s2, 0x2000
	s_nop 0
	global_load_lds_dwordx4 v[220:221], off
	s_mov_b32 m0, s51
	s_nop 0
	global_load_lds_dwordx4 v[150:151], off
	v_lshl_add_u64 v[150:151], v[218:219], 0, s[12:13]
	s_mov_b32 m0, s52
	s_nop 0
	global_load_lds_dwordx4 v[150:151], off
	s_waitcnt vmcnt(8)
	s_waitcnt lgkmcnt(0)
	s_barrier
	s_setprio 1
	s_waitcnt lgkmcnt(0)
	v_mfma_f32_16x16x32_bf16 v[62:65], v[146:149], v[186:189], v[62:65]
	v_mfma_f32_16x16x32_bf16 v[58:61], v[162:165], v[186:189], v[58:61]
	v_mfma_f32_16x16x32_bf16 v[46:49], v[146:149], v[194:197], v[46:49]
	v_mfma_f32_16x16x32_bf16 v[42:45], v[162:165], v[194:197], v[42:45]
	v_mfma_f32_16x16x32_bf16 v[30:33], v[146:149], v[202:205], v[30:33]
	v_mfma_f32_16x16x32_bf16 v[26:29], v[162:165], v[202:205], v[26:29]
	v_mfma_f32_16x16x32_bf16 v[14:17], v[146:149], v[210:213], v[14:17]
	v_mfma_f32_16x16x32_bf16 v[10:13], v[162:165], v[210:213], v[10:13]
	v_mfma_f32_16x16x32_bf16 v[62:65], v[158:161], v[190:193], v[62:65]
	v_mfma_f32_16x16x32_bf16 v[58:61], v[166:169], v[190:193], v[58:61]
	v_mfma_f32_16x16x32_bf16 v[46:49], v[158:161], v[198:201], v[46:49]
	v_mfma_f32_16x16x32_bf16 v[42:45], v[166:169], v[198:201], v[42:45]
	v_mfma_f32_16x16x32_bf16 v[30:33], v[158:161], v[206:209], v[30:33]
	v_mfma_f32_16x16x32_bf16 v[26:29], v[166:169], v[206:209], v[26:29]
	v_mfma_f32_16x16x32_bf16 v[14:17], v[158:161], v[214:217], v[14:17]
	v_mfma_f32_16x16x32_bf16 v[10:13], v[166:169], v[214:217], v[10:13]
	s_setprio 0
	s_setprio 1
	v_mfma_f32_16x16x32_bf16 v[54:57], v[170:173], v[186:189], v[54:57]
	v_mfma_f32_16x16x32_bf16 v[50:53], v[178:181], v[186:189], v[50:53]
	v_mfma_f32_16x16x32_bf16 v[38:41], v[170:173], v[194:197], v[38:41]
	v_mfma_f32_16x16x32_bf16 v[34:37], v[178:181], v[194:197], v[34:37]
	v_mfma_f32_16x16x32_bf16 v[22:25], v[170:173], v[202:205], v[22:25]
	v_mfma_f32_16x16x32_bf16 v[18:21], v[178:181], v[202:205], v[18:21]
	v_mfma_f32_16x16x32_bf16 v[6:9], v[170:173], v[210:213], v[6:9]
	v_mfma_f32_16x16x32_bf16 v[2:5], v[178:181], v[210:213], v[2:5]
	v_mfma_f32_16x16x32_bf16 v[54:57], v[174:177], v[190:193], v[54:57]
	v_mfma_f32_16x16x32_bf16 v[50:53], v[182:185], v[190:193], v[50:53]
	v_mfma_f32_16x16x32_bf16 v[38:41], v[174:177], v[198:201], v[38:41]
	v_mfma_f32_16x16x32_bf16 v[34:37], v[182:185], v[198:201], v[34:37]
	v_mfma_f32_16x16x32_bf16 v[22:25], v[174:177], v[206:209], v[22:25]
	v_mfma_f32_16x16x32_bf16 v[18:21], v[182:185], v[206:209], v[18:21]
	v_mfma_f32_16x16x32_bf16 v[6:9], v[174:177], v[214:217], v[6:9]
	v_mfma_f32_16x16x32_bf16 v[2:5], v[182:185], v[214:217], v[2:5]
	s_setprio 0
	s_barrier
	s_add_i32 s61, s61, 2
	s_add_u32 s59, s59, 0x4000
	s_addc_u32 s60, s60, 0
	s_add_u32 s36, s36, 0x100
	s_addc_u32 s37, s37, 0
	s_cmp_gt_u32 s61, 29
	s_cbranch_scc0 .LBB0_1228
	s_and_b64 vcc, exec, s[14:15]
	s_cbranch_vccz .LBB0_1231
	s_barrier

.LBB0_1481:
	s_lshl_b32 s1, s30, 7
	s_ashr_i32 s0, s30, 4
	s_and_b32 s1, s1, 0x780
	v_or_b32_e32 v240, s1, v184
	s_ashr_i32 s1, s0, 31
	s_lshl_b64 s[0:1], s[0:1], 13
	s_add_u32 s2, s8, s0
	s_addc_u32 s3, s9, s1
	v_lshlrev_b32_e32 v240, 2, v240
	s_add_u32 s0, s10, s0
	s_addc_u32 s1, s11, s1
	global_load_dwordx4 v[224:227], v240, s[2:3]
	global_load_dwordx4 v[228:231], v240, s[2:3] offset:16
	global_load_dwordx4 v[232:235], v240, s[0:1]
	global_load_dwordx4 v[236:239], v240, s[0:1] offset:16
	s_ashr_i32 s21, s20, 31
	s_lshl_b64 s[0:1], s[20:21], 19
	s_add_u32 s24, s47, s0
	s_addc_u32 s25, s48, s1
	s_and_b64 s[0:1], s[4:5], exec
	s_cselect_b32 s21, s25, s37
	s_cselect_b32 s63, s24, s36
	s_ashr_i32 s23, s22, 31
	s_lshl_b64 s[0:1], s[22:23], 19
	s_add_u32 s26, s45, s0
	s_addc_u32 s27, s46, s1
	s_and_b64 s[0:1], s[4:5], exec
	s_cselect_b32 s23, s27, s35
	s_cselect_b32 s64, s26, s34
	s_add_u32 s65, s34, 0x4000
	s_addc_u32 s66, s35, 0
	s_add_u32 s34, s36, 0x40080
	s_addc_u32 s35, s37, 0
	s_mov_b32 s67, -2
	ds_read_b128 v[26:29], v185
	ds_read_b128 v[30:33], v185 offset:1024
	ds_read_b128 v[18:21], v185 offset:2048
	ds_read_b128 v[22:25], v185 offset:3072
	ds_read_b128 v[10:13], v186
	ds_read_b128 v[14:17], v186 offset:1024
	ds_read_b128 v[2:5], v186 offset:2048
	ds_read_b128 v[6:9], v186 offset:3072
	s_add_u32 s0, s34, 0xfffc0080
	s_addc_u32 s1, s35, -1
	s_cmp_eq_u32 s67, 12
	s_cselect_b32 s39, s21, s1
	s_cselect_b32 s38, s63, s0
	s_cselect_b32 s37, s23, s66
	s_cselect_b32 s36, s64, s65
	v_lshl_add_u64 v[178:179], s[34:35], 0, v[172:173]
	s_add_i32 m0, s29, 0xc000
	ds_read_b128 v[190:193], v187
	ds_read_b128 v[194:197], v187 offset:1024
	ds_read_b128 v[198:201], v187 offset:2048
	ds_read_b128 v[202:205], v187 offset:3072
	ds_read_b128 v[206:209], v187 offset:4096
	ds_read_b128 v[210:213], v187 offset:5120
	ds_read_b128 v[214:217], v187 offset:6144
	ds_read_b128 v[218:221], v187 offset:7168
	global_load_lds_dwordx4 v[178:179], off
	v_lshl_add_u64 v[178:179], s[34:35], 0, v[174:175]
	s_add_i32 m0, s29, 0xe000
	s_nop 0
	global_load_lds_dwordx4 v[178:179], off
	s_waitcnt vmcnt(8)
	s_waitcnt lgkmcnt(0)
	s_barrier
	s_setprio 1
	s_waitcnt lgkmcnt(0)
	v_mfma_scale_f32_16x16x128_f8f6f4 v[158:161], v[26:33], v[190:197], 0, v188, v188 op_sel_hi:[0,0,0]
	v_mfma_scale_f32_16x16x128_f8f6f4 v[154:157], v[18:25], v[190:197], 0, v188, v188 op_sel_hi:[0,0,0]
	v_mfma_scale_f32_16x16x128_f8f6f4 v[142:145], v[26:33], v[198:205], 0, v188, v188 op_sel_hi:[0,0,0]
	v_mfma_scale_f32_16x16x128_f8f6f4 v[138:141], v[18:25], v[198:205], 0, v188, v188 op_sel_hi:[0,0,0]
	v_mfma_scale_f32_16x16x128_f8f6f4 v[126:129], v[26:33], v[206:213], 0, v188, v188 op_sel_hi:[0,0,0]
	v_mfma_scale_f32_16x16x128_f8f6f4 v[122:125], v[18:25], v[206:213], 0, v188, v188 op_sel_hi:[0,0,0]
	v_mfma_scale_f32_16x16x128_f8f6f4 v[110:113], v[26:33], v[214:221], 0, v188, v188 op_sel_hi:[0,0,0]
	v_mfma_scale_f32_16x16x128_f8f6f4 v[106:109], v[18:25], v[214:221], 0, v188, v188 op_sel_hi:[0,0,0]
	s_setprio 0
	s_setprio 1
	v_mfma_scale_f32_16x16x128_f8f6f4 v[150:153], v[10:17], v[190:197], 0, v188, v188 op_sel_hi:[0,0,0]
	v_mfma_scale_f32_16x16x128_f8f6f4 v[146:149], v[2:9], v[190:197], 0, v188, v188 op_sel_hi:[0,0,0]
	v_mfma_scale_f32_16x16x128_f8f6f4 v[134:137], v[10:17], v[198:205], 0, v188, v188 op_sel_hi:[0,0,0]
	v_mfma_scale_f32_16x16x128_f8f6f4 v[130:133], v[2:9], v[198:205], 0, v188, v188 op_sel_hi:[0,0,0]
	v_mfma_scale_f32_16x16x128_f8f6f4 v[118:121], v[10:17], v[206:213], 0, v188, v188 op_sel_hi:[0,0,0]
	v_mfma_scale_f32_16x16x128_f8f6f4 v[114:117], v[2:9], v[206:213], 0, v188, v188 op_sel_hi:[0,0,0]
	v_mfma_scale_f32_16x16x128_f8f6f4 v[102:105], v[10:17], v[214:221], 0, v188, v188 op_sel_hi:[0,0,0]
	v_mfma_scale_f32_16x16x128_f8f6f4 v[98:101], v[2:9], v[214:221], 0, v188, v188 op_sel_hi:[0,0,0]
	s_setprio 0
	s_barrier
	s_add_i32 s0, s57, s49
	v_lshl_add_u64 v[178:179], s[36:37], 0, v[164:165]
	s_mov_b32 m0, s0
	ds_read_b128 v[190:193], v187 offset:16384
	ds_read_b128 v[194:197], v187 offset:17408
	ds_read_b128 v[198:201], v187 offset:18432
	ds_read_b128 v[202:205], v187 offset:19456
	ds_read_b128 v[206:209], v187 offset:20480
	ds_read_b128 v[210:213], v187 offset:21504
	ds_read_b128 v[214:217], v187 offset:22528
	ds_read_b128 v[218:221], v187 offset:23552
	global_load_lds_dwordx4 v[178:179], off
	s_add_i32 m0, s0, 0x2000
	s_add_u32 s0, s36, 0x40000
	v_lshl_add_u64 v[178:179], s[36:37], 0, v[168:169]
	s_addc_u32 s1, s37, 0
	s_add_i32 s2, s58, s49
	global_load_lds_dwordx4 v[178:179], off
	v_lshl_add_u64 v[178:179], s[0:1], 0, v[164:165]
	s_mov_b32 m0, s2
	v_lshl_add_u64 v[180:181], s[38:39], 0, v[166:167]
	global_load_lds_dwordx4 v[178:179], off
	v_lshl_add_u64 v[178:179], s[0:1], 0, v[168:169]
	s_add_i32 m0, s2, 0x2000
	s_nop 0
	global_load_lds_dwordx4 v[178:179], off
	v_lshl_add_u64 v[178:179], s[38:39], 0, v[162:163]
	s_mov_b32 m0, s29
	s_nop 0
	global_load_lds_dwordx4 v[178:179], off
	s_mov_b32 m0, s31
	s_nop 0
	global_load_lds_dwordx4 v[180:181], off
	s_waitcnt vmcnt(8)
	s_waitcnt lgkmcnt(0)
	s_barrier
	s_setprio 1
	s_waitcnt lgkmcnt(0)
	v_mfma_scale_f32_16x16x128_f8f6f4 v[94:97], v[26:33], v[190:197], 0, v188, v188 op_sel_hi:[0,0,0]
	v_mfma_scale_f32_16x16x128_f8f6f4 v[90:93], v[18:25], v[190:197], 0, v188, v188 op_sel_hi:[0,0,0]
	v_mfma_scale_f32_16x16x128_f8f6f4 v[78:81], v[26:33], v[198:205], 0, v188, v188 op_sel_hi:[0,0,0]
	v_mfma_scale_f32_16x16x128_f8f6f4 v[74:77], v[18:25], v[198:205], 0, v188, v188 op_sel_hi:[0,0,0]
	v_mfma_scale_f32_16x16x128_f8f6f4 v[62:65], v[26:33], v[206:213], 0, v188, v188 op_sel_hi:[0,0,0]
	v_mfma_scale_f32_16x16x128_f8f6f4 v[58:61], v[18:25], v[206:213], 0, v188, v188 op_sel_hi:[0,0,0]
	v_mfma_scale_f32_16x16x128_f8f6f4 v[46:49], v[26:33], v[214:221], 0, v188, v188 op_sel_hi:[0,0,0]
	v_mfma_scale_f32_16x16x128_f8f6f4 v[42:45], v[18:25], v[214:221], 0, v188, v188 op_sel_hi:[0,0,0]
	s_setprio 0
	s_setprio 1
	v_mfma_scale_f32_16x16x128_f8f6f4 v[86:89], v[10:17], v[190:197], 0, v188, v188 op_sel_hi:[0,0,0]
	v_mfma_scale_f32_16x16x128_f8f6f4 v[82:85], v[2:9], v[190:197], 0, v188, v188 op_sel_hi:[0,0,0]
	v_mfma_scale_f32_16x16x128_f8f6f4 v[70:73], v[10:17], v[198:205], 0, v188, v188 op_sel_hi:[0,0,0]
	v_mfma_scale_f32_16x16x128_f8f6f4 v[66:69], v[2:9], v[198:205], 0, v188, v188 op_sel_hi:[0,0,0]
	v_mfma_scale_f32_16x16x128_f8f6f4 v[54:57], v[10:17], v[206:213], 0, v188, v188 op_sel_hi:[0,0,0]
	v_mfma_scale_f32_16x16x128_f8f6f4 v[50:53], v[2:9], v[206:213], 0, v188, v188 op_sel_hi:[0,0,0]
	v_mfma_scale_f32_16x16x128_f8f6f4 v[38:41], v[10:17], v[214:221], 0, v188, v188 op_sel_hi:[0,0,0]
	v_mfma_scale_f32_16x16x128_f8f6f4 v[34:37], v[2:9], v[214:221], 0, v188, v188 op_sel_hi:[0,0,0]
	s_setprio 0
	s_barrier
	s_branch .Lmid_1482

.Lmid_1482:
	s_add_i32 s2, 0, 0x18000
	v_add_u32_e32 v0, s2, v183
	s_add_i32 s3, 0, 0x1c000
	ds_read_b128 v[2:5], v0
	ds_read_b128 v[6:9], v0 offset:1024
	ds_read_b128 v[10:13], v0 offset:2048
	ds_read_b128 v[14:17], v0 offset:3072
	v_add_u32_e32 v0, s3, v183
	ds_read_b128 v[18:21], v0
	ds_read_b128 v[22:25], v0 offset:1024
	ds_read_b128 v[26:29], v0 offset:2048
	ds_read_b128 v[30:33], v0 offset:3072
	s_add_u32 s0, s38, 0x40000
	s_addc_u32 s1, s39, 0
	s_mov_b32 m0, s50
	v_lshl_add_u64 v[222:223], s[0:1], 0, v[162:163]
	ds_read_b128 v[190:193], v187 offset:32768
	ds_read_b128 v[194:197], v187 offset:33792
	ds_read_b128 v[198:201], v187 offset:34816
	ds_read_b128 v[202:205], v187 offset:35840
	ds_read_b128 v[206:209], v187 offset:36864
	ds_read_b128 v[210:213], v187 offset:37888
	ds_read_b128 v[214:217], v187 offset:38912
	ds_read_b128 v[218:221], v187 offset:39936
	global_load_lds_dwordx4 v[222:223], off
	v_lshl_add_u64 v[222:223], s[0:1], 0, v[166:167]
	s_mov_b32 m0, s51
	s_nop 0
	global_load_lds_dwordx4 v[222:223], off
	s_waitcnt vmcnt(8)
	s_waitcnt lgkmcnt(0)
	s_barrier
	s_setprio 1
	s_waitcnt lgkmcnt(0)
	v_mfma_scale_f32_16x16x128_f8f6f4 v[158:161], v[2:9], v[190:197], v[158:161], v188, v188 op_sel_hi:[0,0,0]
	v_mfma_scale_f32_16x16x128_f8f6f4 v[154:157], v[10:17], v[190:197], v[154:157], v188, v188 op_sel_hi:[0,0,0]
	v_mfma_scale_f32_16x16x128_f8f6f4 v[142:145], v[2:9], v[198:205], v[142:145], v188, v188 op_sel_hi:[0,0,0]
	v_mfma_scale_f32_16x16x128_f8f6f4 v[138:141], v[10:17], v[198:205], v[138:141], v188, v188 op_sel_hi:[0,0,0]
	v_mfma_scale_f32_16x16x128_f8f6f4 v[126:129], v[2:9], v[206:213], v[126:129], v188, v188 op_sel_hi:[0,0,0]
	v_mfma_scale_f32_16x16x128_f8f6f4 v[122:125], v[10:17], v[206:213], v[122:125], v188, v188 op_sel_hi:[0,0,0]
	v_mfma_scale_f32_16x16x128_f8f6f4 v[110:113], v[2:9], v[214:221], v[110:113], v188, v188 op_sel_hi:[0,0,0]
	v_mfma_scale_f32_16x16x128_f8f6f4 v[106:109], v[10:17], v[214:221], v[106:109], v188, v188 op_sel_hi:[0,0,0]
	s_setprio 0
	s_setprio 1
	v_mfma_scale_f32_16x16x128_f8f6f4 v[150:153], v[18:25], v[190:197], v[150:153], v188, v188 op_sel_hi:[0,0,0]
	v_mfma_scale_f32_16x16x128_f8f6f4 v[146:149], v[26:33], v[190:197], v[146:149], v188, v188 op_sel_hi:[0,0,0]
	v_mfma_scale_f32_16x16x128_f8f6f4 v[134:137], v[18:25], v[198:205], v[134:137], v188, v188 op_sel_hi:[0,0,0]
	v_mfma_scale_f32_16x16x128_f8f6f4 v[130:133], v[26:33], v[198:205], v[130:133], v188, v188 op_sel_hi:[0,0,0]
	v_mfma_scale_f32_16x16x128_f8f6f4 v[118:121], v[18:25], v[206:213], v[118:121], v188, v188 op_sel_hi:[0,0,0]
	v_mfma_scale_f32_16x16x128_f8f6f4 v[114:117], v[26:33], v[206:213], v[114:117], v188, v188 op_sel_hi:[0,0,0]
	v_mfma_scale_f32_16x16x128_f8f6f4 v[102:105], v[18:25], v[214:221], v[102:105], v188, v188 op_sel_hi:[0,0,0]
	v_mfma_scale_f32_16x16x128_f8f6f4 v[98:101], v[26:33], v[214:221], v[98:101], v188, v188 op_sel_hi:[0,0,0]
	s_setprio 0
	s_barrier
	s_add_u32 s0, s36, 0x2000
	s_addc_u32 s1, s37, 0
	s_add_i32 s2, s2, s49
	v_lshl_add_u64 v[222:223], s[0:1], 0, v[164:165]
	s_mov_b32 m0, s2
	ds_read_b128 v[190:193], v187 offset:49152
	ds_read_b128 v[194:197], v187 offset:50176
	ds_read_b128 v[198:201], v187 offset:51200
	ds_read_b128 v[202:205], v187 offset:52224
	ds_read_b128 v[206:209], v187 offset:53248
	ds_read_b128 v[210:213], v187 offset:54272
	ds_read_b128 v[214:217], v187 offset:55296
	ds_read_b128 v[218:221], v187 offset:56320
	global_load_lds_dwordx4 v[222:223], off
	s_add_i32 m0, s2, 0x2000
	v_lshl_add_u64 v[222:223], s[0:1], 0, v[168:169]
	s_add_u32 s0, s36, 0x42000
	s_addc_u32 s1, s37, 0
	s_add_i32 s2, s3, s49
	global_load_lds_dwordx4 v[222:223], off
	v_lshl_add_u64 v[222:223], s[0:1], 0, v[164:165]
	s_mov_b32 m0, s2
	v_lshl_add_u64 v[178:179], v[178:179], 0, s[16:17]
	global_load_lds_dwordx4 v[222:223], off
	v_lshl_add_u64 v[222:223], s[0:1], 0, v[168:169]
	s_add_i32 m0, s2, 0x2000
	s_nop 0
	global_load_lds_dwordx4 v[222:223], off
	s_mov_b32 m0, s53
	s_nop 0
	global_load_lds_dwordx4 v[178:179], off
	v_lshl_add_u64 v[178:179], v[180:181], 0, s[16:17]
	s_mov_b32 m0, s54
	s_nop 0
	global_load_lds_dwordx4 v[178:179], off
	s_waitcnt vmcnt(8)
	s_waitcnt lgkmcnt(0)
	s_barrier
	s_setprio 1
	s_waitcnt lgkmcnt(0)
	v_mfma_scale_f32_16x16x128_f8f6f4 v[94:97], v[2:9], v[190:197], v[94:97], v188, v188 op_sel_hi:[0,0,0]
	v_mfma_scale_f32_16x16x128_f8f6f4 v[90:93], v[10:17], v[190:197], v[90:93], v188, v188 op_sel_hi:[0,0,0]
	v_mfma_scale_f32_16x16x128_f8f6f4 v[78:81], v[2:9], v[198:205], v[78:81], v188, v188 op_sel_hi:[0,0,0]
	v_mfma_scale_f32_16x16x128_f8f6f4 v[74:77], v[10:17], v[198:205], v[74:77], v188, v188 op_sel_hi:[0,0,0]
	v_mfma_scale_f32_16x16x128_f8f6f4 v[62:65], v[2:9], v[206:213], v[62:65], v188, v188 op_sel_hi:[0,0,0]
	v_mfma_scale_f32_16x16x128_f8f6f4 v[58:61], v[10:17], v[206:213], v[58:61], v188, v188 op_sel_hi:[0,0,0]
	v_mfma_scale_f32_16x16x128_f8f6f4 v[46:49], v[2:9], v[214:221], v[46:49], v188, v188 op_sel_hi:[0,0,0]
	v_mfma_scale_f32_16x16x128_f8f6f4 v[42:45], v[10:17], v[214:221], v[42:45], v188, v188 op_sel_hi:[0,0,0]
	s_setprio 0
	s_setprio 1
	v_mfma_scale_f32_16x16x128_f8f6f4 v[86:89], v[18:25], v[190:197], v[86:89], v188, v188 op_sel_hi:[0,0,0]
	v_mfma_scale_f32_16x16x128_f8f6f4 v[82:85], v[26:33], v[190:197], v[82:85], v188, v188 op_sel_hi:[0,0,0]
	v_mfma_scale_f32_16x16x128_f8f6f4 v[70:73], v[18:25], v[198:205], v[70:73], v188, v188 op_sel_hi:[0,0,0]
	v_mfma_scale_f32_16x16x128_f8f6f4 v[66:69], v[26:33], v[198:205], v[66:69], v188, v188 op_sel_hi:[0,0,0]
	v_mfma_scale_f32_16x16x128_f8f6f4 v[54:57], v[18:25], v[206:213], v[54:57], v188, v188 op_sel_hi:[0,0,0]
	v_mfma_scale_f32_16x16x128_f8f6f4 v[50:53], v[26:33], v[206:213], v[50:53], v188, v188 op_sel_hi:[0,0,0]
	v_mfma_scale_f32_16x16x128_f8f6f4 v[38:41], v[18:25], v[214:221], v[38:41], v188, v188 op_sel_hi:[0,0,0]
	v_mfma_scale_f32_16x16x128_f8f6f4 v[34:37], v[26:33], v[214:221], v[34:37], v188, v188 op_sel_hi:[0,0,0]
	s_setprio 0
	s_barrier
	s_add_i32 s67, s67, 2
	s_add_u32 s65, s65, 0x4000
	s_addc_u32 s66, s66, 0
	s_add_u32 s34, s34, 0x100
	s_addc_u32 s35, s35, 0
	s_cmp_gt_u32 s67, 13
	s_cbranch_scc0 .LBB0_1482
	s_and_b64 vcc, exec, s[18:19]
	s_cbranch_vccz .LBB0_1485
	s_barrier
.LBB0_1485:
	s_lshl_b32 s1, s30, 7
	s_ashr_i32 s0, s30, 4
	s_and_b32 s1, s1, 0x780
	v_or_b32_e32 v170, s1, v184
	v_lshl_add_u32 v20, s28, 8, v182
	v_fmamk_f32 v0, v158, 0x3a800000, v224
	v_fmamk_f32 v23, v156, 0x3a800000, v230
	v_fmamk_f32 v18, v154, 0x3a800000, v228
	v_min_f32_e32 v0, 0x40e00000, v0
	v_min_f32_e32 v23, 0x40e00000, v23
	v_min_f32_e32 v18, 0x40e00000, v18
	v_fmamk_f32 v26, v150, 0x3a800000, v232
	v_mul_f32_e32 v28, 0x3fd9db23, v0
	v_mul_f32_e32 v150, 0x3fd9db23, v23
	v_mul_f32_e32 v29, 0x3fd9db23, v18
	v_mul_f32_e32 v28, 0xbfb8aa3b, v28
	v_mul_f32_e32 v150, 0xbfb8aa3b, v150
	v_mul_f32_e32 v29, 0xbfb8aa3b, v29
	v_exp_f32_e32 v28, v28
	v_exp_f32_e32 v150, v150
	v_fmamk_f32 v31, v147, 0x3a800000, v237
	v_exp_f32_e32 v29, v29
	v_fmamk_f32 v21, v155, 0x3a800000, v229
	v_fmamk_f32 v27, v146, 0x3a800000, v236
	v_med3_f32 v26, v26, s59, v189
	v_med3_f32 v31, v31, s59, v189
	v_min_f32_e32 v21, 0x40e00000, v21
	v_med3_f32 v27, v27, s59, v189
	v_add_f32_e32 v26, 1.0, v26
	v_add_f32_e32 v31, 1.0, v31
	v_mul_f32_e32 v33, 0x3fd9db23, v21
	v_add_f32_e32 v27, 1.0, v27
	v_mul_f32_e32 v0, v0, v26
	v_mul_f32_e32 v21, v21, v31
	v_add_f32_e32 v26, 1.0, v28
	v_add_f32_e32 v31, 1.0, v150
	v_fmamk_f32 v147, v148, 0x3a800000, v238
	v_mul_f32_e32 v18, v18, v27
	v_add_f32_e32 v27, 1.0, v29
	v_rcp_f32_e32 v26, v26
	v_rcp_f32_e32 v31, v31
	v_fmamk_f32 v19, v159, 0x3a800000, v225
	v_fmamk_f32 v22, v160, 0x3a800000, v226
	v_fmamk_f32 v24, v161, 0x3a800000, v227
	v_med3_f32 v147, v147, s59, v189
	v_rcp_f32_e32 v27, v27
	v_min_f32_e32 v19, 0x40e00000, v19
	v_min_f32_e32 v22, 0x40e00000, v22
	v_min_f32_e32 v24, 0x40e00000, v24
	v_add_f32_e32 v147, 1.0, v147
	v_fmamk_f32 v25, v157, 0x3a800000, v231
	v_mul_f32_e32 v32, 0x3fd9db23, v19
	v_fmamk_f32 v146, v152, 0x3a800000, v234
	v_mul_f32_e32 v148, 0x3fd9db23, v22
	v_mul_f32_e32 v152, 0x3fd9db23, v24
	v_mul_f32_e32 v23, v23, v147
	v_min_f32_e32 v25, 0x40e00000, v25
	v_mul_f32_e32 v32, 0xbfb8aa3b, v32
	v_mul_f32_e32 v148, 0xbfb8aa3b, v148
	v_mul_f32_e32 v0, v0, v26
	v_mul_f32_e32 v26, v23, v31
	v_mul_f32_e32 v23, 0xbfb8aa3b, v152
	v_mul_f32_e32 v33, 0xbfb8aa3b, v33
	v_exp_f32_e32 v32, v32
	v_exp_f32_e32 v148, v148
	v_mul_f32_e32 v18, v18, v27
	v_exp_f32_e32 v23, v23
	v_mul_f32_e32 v27, 0x3fd9db23, v25
	v_fmamk_f32 v30, v151, 0x3a800000, v233
	v_exp_f32_e32 v33, v33
	v_mul_f32_e32 v27, 0xbfb8aa3b, v27
	v_med3_f32 v30, v30, s59, v189
	v_exp_f32_e32 v27, v27
	v_add_f32_e32 v30, 1.0, v30
	v_mul_f32_e32 v19, v19, v30
	v_add_f32_e32 v28, 1.0, v32
	v_add_f32_e32 v30, 1.0, v148
	v_add_f32_e32 v23, 1.0, v23
	v_fmamk_f32 v151, v153, 0x3a800000, v235
	v_add_f32_e32 v29, 1.0, v33
	v_rcp_f32_e32 v28, v28
	v_rcp_f32_e32 v30, v30
	v_rcp_f32_e32 v23, v23
	v_med3_f32 v146, v146, s59, v189
	v_med3_f32 v151, v151, s59, v189
	v_rcp_f32_e32 v29, v29
	v_add_f32_e32 v27, 1.0, v27
	v_fmamk_f32 v149, v149, 0x3a800000, v239
	v_add_f32_e32 v146, 1.0, v146
	v_add_f32_e32 v151, 1.0, v151
	v_rcp_f32_e32 v27, v27
	v_med3_f32 v149, v149, s59, v189
	v_mul_f32_e32 v22, v22, v146
	v_mul_f32_e32 v24, v24, v151
	v_mul_f32_e32 v19, v19, v28
	v_mul_f32_e32 v22, v22, v30
	v_mul_f32_e32 v23, v24, v23
	v_add_f32_e32 v24, 1.0, v149
	v_mul_f32_e32 v21, v21, v29
	v_mul_f32_e32 v24, v25, v24
	v_mul_f32_e32 v0, 4.0, v0
	v_mul_f32_e32 v19, 4.0, v19
	v_mul_f32_e32 v25, 4.0, v22
	v_mov_b32_e32 v22, v171
	v_mul_f32_e32 v24, v24, v27
	v_mul_f32_e32 v27, 4.0, v23
	v_cvt_pk_fp8_f32 v22, v0, v19
	v_mul_f32_e32 v0, 4.0, v18
	v_mul_f32_e32 v18, 4.0, v21
	v_mov_b32_e32 v23, v171
	v_cvt_pk_fp8_f32 v23, v0, v18
	v_mul_f32_e32 v0, 4.0, v26
	v_mul_f32_e32 v18, 4.0, v24
	v_ashrrev_i32_e32 v21, 31, v20
	v_cvt_pk_fp8_f32 v23, v0, v18 op_sel:[0,0,1]
	v_lshlrev_b64 v[18:19], 11, v[20:21]
	v_fmamk_f32 v21, v138, 0x3a800000, v228
	v_cvt_pk_fp8_f32 v22, v25, v27 op_sel:[0,0,1]
	v_min_f32_e32 v21, 0x40e00000, v21
	v_mul_f32_e32 v25, 0x3fd9db23, v21
	v_lshl_add_u64 v[18:19], s[14:15], 0, v[18:19]
	v_mul_f32_e32 v25, 0xbfb8aa3b, v25
	v_lshl_add_u64 v[18:19], v[18:19], 0, v[170:171]
	v_exp_f32_e32 v25, v25
	global_store_dwordx2 v[18:19], v[22:23], off
	v_fmamk_f32 v22, v134, 0x3a800000, v232
	v_fmamk_f32 v0, v142, 0x3a800000, v224
	v_med3_f32 v22, v22, s59, v189
	v_min_f32_e32 v0, 0x40e00000, v0
	v_add_f32_e32 v22, 1.0, v22
	v_mul_f32_e32 v24, 0x3fd9db23, v0
	v_mul_f32_e32 v0, v0, v22
	v_add_f32_e32 v22, 1.0, v25
	v_fmamk_f32 v23, v130, 0x3a800000, v236
	v_rcp_f32_e32 v22, v22
	v_med3_f32 v23, v23, s59, v189
	v_mul_f32_e32 v24, 0xbfb8aa3b, v24
	v_exp_f32_e32 v24, v24
	v_add_f32_e32 v23, 1.0, v23
	v_mul_f32_e32 v21, v21, v23
	v_mul_f32_e32 v21, v21, v22
	v_fmamk_f32 v22, v143, 0x3a800000, v225
	v_min_f32_e32 v22, 0x40e00000, v22
	v_add_f32_e32 v24, 1.0, v24
	v_fmamk_f32 v23, v139, 0x3a800000, v229
	v_mul_f32_e32 v26, 0x3fd9db23, v22
	v_rcp_f32_e32 v24, v24
	v_min_f32_e32 v23, 0x40e00000, v23
	v_mul_f32_e32 v26, 0xbfb8aa3b, v26
	v_exp_f32_e32 v26, v26
	v_mul_f32_e32 v27, 0x3fd9db23, v23
	v_mul_f32_e32 v27, 0xbfb8aa3b, v27
	v_exp_f32_e32 v27, v27
	v_mul_f32_e32 v0, v0, v24
	v_fmamk_f32 v24, v135, 0x3a800000, v233
	v_med3_f32 v24, v24, s59, v189
	v_add_f32_e32 v26, 1.0, v26
	v_add_f32_e32 v24, 1.0, v24
	v_rcp_f32_e32 v26, v26
	v_mul_f32_e32 v22, v22, v24
	v_add_f32_e32 v24, 1.0, v27
	v_fmamk_f32 v25, v131, 0x3a800000, v237
	v_rcp_f32_e32 v24, v24
	v_med3_f32 v25, v25, s59, v189
	v_mul_f32_e32 v26, v22, v26
	v_add_f32_e32 v22, 1.0, v25
	v_mul_f32_e32 v22, v23, v22
	v_mul_f32_e32 v23, v22, v24
	v_fmamk_f32 v22, v144, 0x3a800000, v226
	v_min_f32_e32 v22, 0x40e00000, v22
	v_fmamk_f32 v24, v140, 0x3a800000, v230
	v_mul_f32_e32 v28, 0x3fd9db23, v22
	v_min_f32_e32 v24, 0x40e00000, v24
	v_mul_f32_e32 v28, 0xbfb8aa3b, v28
	v_exp_f32_e32 v28, v28
	v_mul_f32_e32 v29, 0x3fd9db23, v24
	v_mul_f32_e32 v29, 0xbfb8aa3b, v29
	v_exp_f32_e32 v29, v29
	v_fmamk_f32 v25, v136, 0x3a800000, v234
	v_med3_f32 v25, v25, s59, v189
	v_add_f32_e32 v28, 1.0, v28
	v_add_f32_e32 v25, 1.0, v25
	v_rcp_f32_e32 v28, v28
	v_mul_f32_e32 v22, v22, v25
	v_add_f32_e32 v25, 1.0, v29
	v_fmamk_f32 v27, v132, 0x3a800000, v238
	v_rcp_f32_e32 v25, v25
	v_med3_f32 v27, v27, s59, v189
	v_mul_f32_e32 v28, v22, v28
	v_add_f32_e32 v22, 1.0, v27
	v_mul_f32_e32 v22, v24, v22
	v_mul_f32_e32 v27, v22, v25
	v_fmamk_f32 v22, v145, 0x3a800000, v227
	v_min_f32_e32 v22, 0x40e00000, v22
	v_fmamk_f32 v24, v141, 0x3a800000, v231
	v_mul_f32_e32 v30, 0x3fd9db23, v22
	v_min_f32_e32 v24, 0x40e00000, v24
	v_mul_f32_e32 v30, 0xbfb8aa3b, v30
	v_exp_f32_e32 v30, v30
	v_mul_f32_e32 v31, 0x3fd9db23, v24
	v_mul_f32_e32 v31, 0xbfb8aa3b, v31
	v_exp_f32_e32 v31, v31
	v_fmamk_f32 v25, v137, 0x3a800000, v235
	v_med3_f32 v25, v25, s59, v189
	v_add_f32_e32 v30, 1.0, v30
	v_add_f32_e32 v25, 1.0, v25
	v_rcp_f32_e32 v30, v30
	v_mul_f32_e32 v22, v22, v25
	v_add_f32_e32 v25, 1.0, v31
	v_fmamk_f32 v29, v133, 0x3a800000, v239
	v_rcp_f32_e32 v25, v25
	v_med3_f32 v29, v29, s59, v189
	v_mul_f32_e32 v30, v22, v30
	v_add_f32_e32 v22, 1.0, v29
	v_mul_f32_e32 v22, v24, v22
	v_mul_f32_e32 v29, v22, v25
	v_mul_f32_e32 v0, 4.0, v0
	v_mul_f32_e32 v25, 4.0, v26
	v_mov_b32_e32 v24, v171
	v_cvt_pk_fp8_f32 v24, v0, v25
	v_mul_f32_e32 v0, 4.0, v21
	v_mul_f32_e32 v21, 4.0, v23
	v_mov_b32_e32 v25, v171
	v_cvt_pk_fp8_f32 v25, v0, v21
	v_or_b32_e32 v22, 16, v20
	v_mul_f32_e32 v26, 4.0, v28
	v_mul_f32_e32 v28, 4.0, v30
	v_mul_f32_e32 v0, 4.0, v27
	v_mul_f32_e32 v21, 4.0, v29
	v_cvt_pk_fp8_f32 v24, v26, v28 op_sel:[0,0,1]
	v_cvt_pk_fp8_f32 v25, v0, v21 op_sel:[0,0,1]
	v_ashrrev_i32_e32 v23, 31, v22
	v_lshlrev_b64 v[22:23], 11, v[22:23]
	v_lshl_add_u64 v[22:23], s[14:15], 0, v[22:23]
	v_fmamk_f32 v21, v122, 0x3a800000, v228
	v_lshl_add_u64 v[22:23], v[22:23], 0, v[170:171]
	v_min_f32_e32 v21, 0x40e00000, v21
	global_store_dwordx2 v[22:23], v[24:25], off
	v_mul_f32_e32 v25, 0x3fd9db23, v21
	v_mul_f32_e32 v25, 0xbfb8aa3b, v25
	v_exp_f32_e32 v25, v25
	v_fmamk_f32 v22, v118, 0x3a800000, v232
	v_fmamk_f32 v0, v126, 0x3a800000, v224
	v_med3_f32 v22, v22, s59, v189
	v_min_f32_e32 v0, 0x40e00000, v0
	v_add_f32_e32 v22, 1.0, v22
	v_mul_f32_e32 v24, 0x3fd9db23, v0
	v_mul_f32_e32 v0, v0, v22
	v_add_f32_e32 v22, 1.0, v25
	v_fmamk_f32 v23, v114, 0x3a800000, v236
	v_rcp_f32_e32 v22, v22
	v_med3_f32 v23, v23, s59, v189
	v_mul_f32_e32 v24, 0xbfb8aa3b, v24
	v_exp_f32_e32 v24, v24
	v_add_f32_e32 v23, 1.0, v23
	v_mul_f32_e32 v21, v21, v23
	v_mul_f32_e32 v21, v21, v22
	v_fmamk_f32 v22, v127, 0x3a800000, v225
	v_min_f32_e32 v22, 0x40e00000, v22
	v_add_f32_e32 v24, 1.0, v24
	v_fmamk_f32 v23, v123, 0x3a800000, v229
	v_mul_f32_e32 v26, 0x3fd9db23, v22
	v_rcp_f32_e32 v24, v24
	v_min_f32_e32 v23, 0x40e00000, v23
	v_mul_f32_e32 v26, 0xbfb8aa3b, v26
	v_exp_f32_e32 v26, v26
	v_mul_f32_e32 v27, 0x3fd9db23, v23
	v_mul_f32_e32 v27, 0xbfb8aa3b, v27
	v_exp_f32_e32 v27, v27
	v_mul_f32_e32 v0, v0, v24
	v_fmamk_f32 v24, v119, 0x3a800000, v233
	v_med3_f32 v24, v24, s59, v189
	v_add_f32_e32 v26, 1.0, v26
	v_add_f32_e32 v24, 1.0, v24
	v_rcp_f32_e32 v26, v26
	v_mul_f32_e32 v22, v22, v24
	v_add_f32_e32 v24, 1.0, v27
	v_fmamk_f32 v25, v115, 0x3a800000, v237
	v_rcp_f32_e32 v24, v24
	v_med3_f32 v25, v25, s59, v189
	v_mul_f32_e32 v26, v22, v26
	v_add_f32_e32 v22, 1.0, v25
	v_mul_f32_e32 v22, v23, v22
	v_mul_f32_e32 v23, v22, v24
	v_fmamk_f32 v22, v128, 0x3a800000, v226
	v_min_f32_e32 v22, 0x40e00000, v22
	v_fmamk_f32 v24, v124, 0x3a800000, v230
	v_mul_f32_e32 v28, 0x3fd9db23, v22
	v_min_f32_e32 v24, 0x40e00000, v24
	v_mul_f32_e32 v28, 0xbfb8aa3b, v28
	v_exp_f32_e32 v28, v28
	v_mul_f32_e32 v29, 0x3fd9db23, v24
	v_mul_f32_e32 v29, 0xbfb8aa3b, v29
	v_exp_f32_e32 v29, v29
	v_fmamk_f32 v25, v120, 0x3a800000, v234
	v_med3_f32 v25, v25, s59, v189
	v_add_f32_e32 v28, 1.0, v28
	v_add_f32_e32 v25, 1.0, v25
	v_rcp_f32_e32 v28, v28
	v_mul_f32_e32 v22, v22, v25
	v_add_f32_e32 v25, 1.0, v29
	v_fmamk_f32 v27, v116, 0x3a800000, v238
	v_rcp_f32_e32 v25, v25
	v_med3_f32 v27, v27, s59, v189
	v_mul_f32_e32 v28, v22, v28
	v_add_f32_e32 v22, 1.0, v27
	v_mul_f32_e32 v22, v24, v22
	v_mul_f32_e32 v27, v22, v25
	v_fmamk_f32 v22, v129, 0x3a800000, v227
	v_min_f32_e32 v22, 0x40e00000, v22
	v_fmamk_f32 v24, v125, 0x3a800000, v231
	v_mul_f32_e32 v30, 0x3fd9db23, v22
	v_min_f32_e32 v24, 0x40e00000, v24
	v_mul_f32_e32 v30, 0xbfb8aa3b, v30
	v_exp_f32_e32 v30, v30
	v_mul_f32_e32 v31, 0x3fd9db23, v24
	v_mul_f32_e32 v31, 0xbfb8aa3b, v31
	v_exp_f32_e32 v31, v31
	v_fmamk_f32 v25, v121, 0x3a800000, v235
	v_med3_f32 v25, v25, s59, v189
	v_add_f32_e32 v30, 1.0, v30
	v_add_f32_e32 v25, 1.0, v25
	v_rcp_f32_e32 v30, v30
	v_mul_f32_e32 v22, v22, v25
	v_add_f32_e32 v25, 1.0, v31
	v_fmamk_f32 v29, v117, 0x3a800000, v239
	v_rcp_f32_e32 v25, v25
	v_med3_f32 v29, v29, s59, v189
	v_mul_f32_e32 v30, v22, v30
	v_add_f32_e32 v22, 1.0, v29
	v_mul_f32_e32 v22, v24, v22
	v_mul_f32_e32 v29, v22, v25
	v_mul_f32_e32 v0, 4.0, v0
	v_mul_f32_e32 v25, 4.0, v26
	v_mov_b32_e32 v24, v171
	v_cvt_pk_fp8_f32 v24, v0, v25
	v_mul_f32_e32 v0, 4.0, v21
	v_mul_f32_e32 v21, 4.0, v23
	v_mov_b32_e32 v25, v171
	v_cvt_pk_fp8_f32 v25, v0, v21
	v_or_b32_e32 v22, 32, v20
	v_mul_f32_e32 v26, 4.0, v28
	v_mul_f32_e32 v28, 4.0, v30
	v_mul_f32_e32 v0, 4.0, v27
	v_mul_f32_e32 v21, 4.0, v29
	v_cvt_pk_fp8_f32 v24, v26, v28 op_sel:[0,0,1]
	v_cvt_pk_fp8_f32 v25, v0, v21 op_sel:[0,0,1]
	v_ashrrev_i32_e32 v23, 31, v22
	v_lshlrev_b64 v[22:23], 11, v[22:23]
	v_lshl_add_u64 v[22:23], s[14:15], 0, v[22:23]
	v_fmamk_f32 v21, v106, 0x3a800000, v228
	v_lshl_add_u64 v[22:23], v[22:23], 0, v[170:171]
	v_fmamk_f32 v0, v110, 0x3a800000, v224
	v_min_f32_e32 v21, 0x40e00000, v21
	global_store_dwordx2 v[22:23], v[24:25], off
	v_min_f32_e32 v0, 0x40e00000, v0
	v_mul_f32_e32 v25, 0x3fd9db23, v21
	v_mul_f32_e32 v24, 0x3fd9db23, v0
	v_mul_f32_e32 v25, 0xbfb8aa3b, v25
	v_mul_f32_e32 v24, 0xbfb8aa3b, v24
	v_exp_f32_e32 v25, v25
	v_fmamk_f32 v22, v102, 0x3a800000, v232
	v_exp_f32_e32 v24, v24
	v_med3_f32 v22, v22, s59, v189
	v_fmamk_f32 v23, v98, 0x3a800000, v236
	v_med3_f32 v23, v23, s59, v189
	v_add_f32_e32 v22, 1.0, v22
	v_mul_f32_e32 v0, v0, v22
	v_add_f32_e32 v22, 1.0, v25
	v_add_f32_e32 v23, 1.0, v23
	v_add_f32_e32 v24, 1.0, v24
	v_rcp_f32_e32 v22, v22
	v_mul_f32_e32 v21, v21, v23
	v_fmamk_f32 v23, v107, 0x3a800000, v229
	v_rcp_f32_e32 v24, v24
	v_min_f32_e32 v23, 0x40e00000, v23
	v_mul_f32_e32 v27, 0x3fd9db23, v23
	v_mul_f32_e32 v27, 0xbfb8aa3b, v27
	v_mul_f32_e32 v21, v21, v22
	v_fmamk_f32 v22, v111, 0x3a800000, v225
	v_exp_f32_e32 v27, v27
	v_mul_f32_e32 v0, v0, v24
	v_min_f32_e32 v22, 0x40e00000, v22
	v_fmamk_f32 v24, v103, 0x3a800000, v233
	v_med3_f32 v24, v24, s59, v189
	v_mul_f32_e32 v26, 0x3fd9db23, v22
	v_add_f32_e32 v24, 1.0, v24
	v_mul_f32_e32 v26, 0xbfb8aa3b, v26
	v_exp_f32_e32 v26, v26
	v_mul_f32_e32 v22, v22, v24
	v_add_f32_e32 v24, 1.0, v27
	v_fmamk_f32 v25, v99, 0x3a800000, v237
	v_rcp_f32_e32 v24, v24
	v_med3_f32 v25, v25, s59, v189
	v_add_f32_e32 v25, 1.0, v25
	v_add_f32_e32 v26, 1.0, v26
	v_mul_f32_e32 v23, v23, v25
	v_fmamk_f32 v25, v108, 0x3a800000, v230
	v_rcp_f32_e32 v26, v26
	v_mul_f32_e32 v23, v23, v24
	v_fmamk_f32 v24, v112, 0x3a800000, v226
	v_min_f32_e32 v25, 0x40e00000, v25
	v_min_f32_e32 v24, 0x40e00000, v24
	v_mul_f32_e32 v29, 0x3fd9db23, v25
	v_mul_f32_e32 v28, 0x3fd9db23, v24
	v_mul_f32_e32 v29, 0xbfb8aa3b, v29
	v_mul_f32_e32 v28, 0xbfb8aa3b, v28
	v_exp_f32_e32 v29, v29
	v_mul_f32_e32 v22, v22, v26
	v_fmamk_f32 v26, v104, 0x3a800000, v234
	v_exp_f32_e32 v28, v28
	v_med3_f32 v26, v26, s59, v189
	v_fmamk_f32 v27, v100, 0x3a800000, v238
	v_med3_f32 v27, v27, s59, v189
	v_add_f32_e32 v26, 1.0, v26
	v_mul_f32_e32 v24, v24, v26
	v_add_f32_e32 v26, 1.0, v29
	v_add_f32_e32 v27, 1.0, v27
	v_add_f32_e32 v28, 1.0, v28
	v_rcp_f32_e32 v26, v26
	v_mul_f32_e32 v25, v25, v27
	v_fmamk_f32 v27, v109, 0x3a800000, v231
	v_rcp_f32_e32 v28, v28
	v_min_f32_e32 v27, 0x40e00000, v27
	v_mul_f32_e32 v31, 0x3fd9db23, v27
	v_mul_f32_e32 v31, 0xbfb8aa3b, v31
	v_mul_f32_e32 v25, v25, v26
	v_fmamk_f32 v26, v113, 0x3a800000, v227
	v_exp_f32_e32 v31, v31
	v_mul_f32_e32 v24, v24, v28
	v_min_f32_e32 v26, 0x40e00000, v26
	v_fmamk_f32 v28, v105, 0x3a800000, v235
	v_med3_f32 v28, v28, s59, v189
	v_mul_f32_e32 v30, 0x3fd9db23, v26
	v_add_f32_e32 v28, 1.0, v28
	v_mul_f32_e32 v30, 0xbfb8aa3b, v30
	v_exp_f32_e32 v30, v30
	v_mul_f32_e32 v26, v26, v28
	v_add_f32_e32 v28, 1.0, v31
	v_fmamk_f32 v29, v101, 0x3a800000, v239
	v_rcp_f32_e32 v28, v28
	v_med3_f32 v29, v29, s59, v189
	v_add_f32_e32 v29, 1.0, v29
	v_add_f32_e32 v30, 1.0, v30
	v_mul_f32_e32 v27, v27, v29
	v_rcp_f32_e32 v30, v30
	v_mul_f32_e32 v27, v27, v28
	v_mul_f32_e32 v0, 4.0, v0
	v_mul_f32_e32 v28, 4.0, v22
	v_mov_b32_e32 v22, v171
	v_cvt_pk_fp8_f32 v22, v0, v28
	v_mul_f32_e32 v0, 4.0, v21
	v_mul_f32_e32 v21, 4.0, v23
	v_mov_b32_e32 v23, v171
	v_cvt_pk_fp8_f32 v23, v0, v21
	v_mul_f32_e32 v26, v26, v30
	v_or_b32_e32 v20, 48, v20
	v_mul_f32_e32 v24, 4.0, v24
	v_mul_f32_e32 v26, 4.0, v26
	v_mul_f32_e32 v0, 4.0, v25
	v_mul_f32_e32 v21, 4.0, v27
	v_cvt_pk_fp8_f32 v22, v24, v26 op_sel:[0,0,1]
	v_cvt_pk_fp8_f32 v23, v0, v21 op_sel:[0,0,1]
	v_ashrrev_i32_e32 v21, 31, v20
	v_lshlrev_b64 v[20:21], 11, v[20:21]
	v_lshl_add_u64 v[20:21], s[14:15], 0, v[20:21]
	v_lshl_add_u64 v[20:21], v[20:21], 0, v[170:171]
	global_store_dwordx2 v[20:21], v[22:23], off
	v_fmamk_f32 v20, v90, 0x3a800000, v228
	v_fmamk_f32 v0, v94, 0x3a800000, v224
	v_min_f32_e32 v20, 0x40e00000, v20
	v_min_f32_e32 v0, 0x40e00000, v0
	v_mul_f32_e32 v24, 0x3fd9db23, v20
	v_mul_f32_e32 v23, 0x3fd9db23, v0
	v_mul_f32_e32 v24, 0xbfb8aa3b, v24
	v_mul_f32_e32 v23, 0xbfb8aa3b, v23
	v_exp_f32_e32 v24, v24
	v_fmamk_f32 v21, v86, 0x3a800000, v232
	v_exp_f32_e32 v23, v23
	v_med3_f32 v21, v21, s59, v189
	v_fmamk_f32 v22, v82, 0x3a800000, v236
	v_med3_f32 v22, v22, s59, v189
	v_add_f32_e32 v21, 1.0, v21
	v_mul_f32_e32 v0, v0, v21
	v_add_f32_e32 v21, 1.0, v24
	v_add_f32_e32 v22, 1.0, v22
	v_add_f32_e32 v23, 1.0, v23
	v_rcp_f32_e32 v21, v21
	v_mul_f32_e32 v20, v20, v22
	v_fmamk_f32 v22, v91, 0x3a800000, v229
	v_rcp_f32_e32 v23, v23
	v_min_f32_e32 v22, 0x40e00000, v22
	v_mul_f32_e32 v26, 0x3fd9db23, v22
	v_mul_f32_e32 v26, 0xbfb8aa3b, v26
	v_mul_f32_e32 v21, v20, v21
	v_fmamk_f32 v20, v95, 0x3a800000, v225
	v_exp_f32_e32 v26, v26
	v_mul_f32_e32 v0, v0, v23
	v_min_f32_e32 v20, 0x40e00000, v20
	v_fmamk_f32 v23, v87, 0x3a800000, v233
	v_med3_f32 v23, v23, s59, v189
	v_mul_f32_e32 v25, 0x3fd9db23, v20
	v_add_f32_e32 v23, 1.0, v23
	v_mul_f32_e32 v25, 0xbfb8aa3b, v25
	v_exp_f32_e32 v25, v25
	v_mul_f32_e32 v20, v20, v23
	v_add_f32_e32 v23, 1.0, v26
	v_fmamk_f32 v24, v83, 0x3a800000, v237
	v_rcp_f32_e32 v23, v23
	v_med3_f32 v24, v24, s59, v189
	v_add_f32_e32 v24, 1.0, v24
	v_add_f32_e32 v25, 1.0, v25
	v_mul_f32_e32 v22, v22, v24
	v_fmamk_f32 v24, v92, 0x3a800000, v230
	v_rcp_f32_e32 v25, v25
	v_mul_f32_e32 v22, v22, v23
	v_fmamk_f32 v23, v96, 0x3a800000, v226
	v_min_f32_e32 v24, 0x40e00000, v24
	v_min_f32_e32 v23, 0x40e00000, v23
	v_mul_f32_e32 v28, 0x3fd9db23, v24
	v_mul_f32_e32 v27, 0x3fd9db23, v23
	v_mul_f32_e32 v28, 0xbfb8aa3b, v28
	v_mul_f32_e32 v27, 0xbfb8aa3b, v27
	v_exp_f32_e32 v28, v28
	v_mul_f32_e32 v20, v20, v25
	v_fmamk_f32 v25, v88, 0x3a800000, v234
	v_exp_f32_e32 v27, v27
	v_med3_f32 v25, v25, s59, v189
	v_fmamk_f32 v26, v84, 0x3a800000, v238
	v_med3_f32 v26, v26, s59, v189
	v_add_f32_e32 v25, 1.0, v25
	v_mul_f32_e32 v23, v23, v25
	v_add_f32_e32 v25, 1.0, v28
	v_add_f32_e32 v26, 1.0, v26
	v_add_f32_e32 v27, 1.0, v27
	v_rcp_f32_e32 v25, v25
	v_mul_f32_e32 v24, v24, v26
	v_fmamk_f32 v26, v93, 0x3a800000, v231
	v_rcp_f32_e32 v27, v27
	v_min_f32_e32 v26, 0x40e00000, v26
	v_mul_f32_e32 v30, 0x3fd9db23, v26
	v_mul_f32_e32 v30, 0xbfb8aa3b, v30
	v_mul_f32_e32 v24, v24, v25
	v_fmamk_f32 v25, v97, 0x3a800000, v227
	v_exp_f32_e32 v30, v30
	v_mul_f32_e32 v23, v23, v27
	v_min_f32_e32 v25, 0x40e00000, v25
	v_fmamk_f32 v27, v89, 0x3a800000, v235
	v_med3_f32 v27, v27, s59, v189
	v_mul_f32_e32 v29, 0x3fd9db23, v25
	v_add_f32_e32 v27, 1.0, v27
	v_mul_f32_e32 v29, 0xbfb8aa3b, v29
	v_exp_f32_e32 v29, v29
	v_mul_f32_e32 v25, v25, v27
	v_add_f32_e32 v27, 1.0, v30
	v_fmamk_f32 v28, v85, 0x3a800000, v239
	v_rcp_f32_e32 v27, v27
	v_med3_f32 v28, v28, s59, v189
	v_add_f32_e32 v28, 1.0, v28
	v_add_f32_e32 v29, 1.0, v29
	v_mul_f32_e32 v26, v26, v28
	v_rcp_f32_e32 v29, v29
	v_mul_f32_e32 v26, v26, v27
	v_mul_f32_e32 v0, 4.0, v0
	v_mul_f32_e32 v27, 4.0, v20
	v_mov_b32_e32 v20, v171
	v_cvt_pk_fp8_f32 v20, v0, v27
	v_mul_f32_e32 v0, 4.0, v21
	v_mul_f32_e32 v22, 4.0, v22
	v_mov_b32_e32 v21, v171
	v_cvt_pk_fp8_f32 v21, v0, v22
	v_mul_f32_e32 v25, v25, v29
	v_mul_f32_e32 v23, 4.0, v23
	v_mul_f32_e32 v25, 4.0, v25
	v_mul_f32_e32 v0, 4.0, v24
	v_mul_f32_e32 v22, 4.0, v26
	v_cvt_pk_fp8_f32 v20, v23, v25 op_sel:[0,0,1]
	v_cvt_pk_fp8_f32 v21, v0, v22 op_sel:[0,0,1]
	v_add_co_u32_e32 v22, vcc, s60, v18
	v_fmamk_f32 v0, v78, 0x3a800000, v224
	s_nop 0
	v_addc_co_u32_e32 v23, vcc, 0, v19, vcc
	global_store_dwordx2 v[22:23], v[20:21], off
	v_fmamk_f32 v20, v74, 0x3a800000, v228
	v_min_f32_e32 v20, 0x40e00000, v20
	v_min_f32_e32 v0, 0x40e00000, v0
	v_mul_f32_e32 v24, 0x3fd9db23, v20
	v_mul_f32_e32 v23, 0x3fd9db23, v0
	v_mul_f32_e32 v24, 0xbfb8aa3b, v24
	v_mul_f32_e32 v23, 0xbfb8aa3b, v23
	v_exp_f32_e32 v24, v24
	v_fmamk_f32 v21, v70, 0x3a800000, v232
	v_exp_f32_e32 v23, v23
	v_med3_f32 v21, v21, s59, v189
	v_fmamk_f32 v22, v66, 0x3a800000, v236
	v_med3_f32 v22, v22, s59, v189
	v_add_f32_e32 v21, 1.0, v21
	v_mul_f32_e32 v0, v0, v21
	v_add_f32_e32 v21, 1.0, v24
	v_add_f32_e32 v22, 1.0, v22
	v_add_f32_e32 v23, 1.0, v23
	v_rcp_f32_e32 v21, v21
	v_mul_f32_e32 v20, v20, v22
	v_fmamk_f32 v22, v75, 0x3a800000, v229
	v_rcp_f32_e32 v23, v23
	v_min_f32_e32 v22, 0x40e00000, v22
	v_mul_f32_e32 v26, 0x3fd9db23, v22
	v_mul_f32_e32 v26, 0xbfb8aa3b, v26
	v_mul_f32_e32 v21, v20, v21
	v_fmamk_f32 v20, v79, 0x3a800000, v225
	v_exp_f32_e32 v26, v26
	v_mul_f32_e32 v0, v0, v23
	v_min_f32_e32 v20, 0x40e00000, v20
	v_fmamk_f32 v23, v71, 0x3a800000, v233
	v_med3_f32 v23, v23, s59, v189
	v_mul_f32_e32 v25, 0x3fd9db23, v20
	v_add_f32_e32 v23, 1.0, v23
	v_mul_f32_e32 v25, 0xbfb8aa3b, v25
	v_exp_f32_e32 v25, v25
	v_mul_f32_e32 v20, v20, v23
	v_add_f32_e32 v23, 1.0, v26
	v_fmamk_f32 v24, v67, 0x3a800000, v237
	v_rcp_f32_e32 v23, v23
	v_med3_f32 v24, v24, s59, v189
	v_add_f32_e32 v24, 1.0, v24
	v_add_f32_e32 v25, 1.0, v25
	v_mul_f32_e32 v22, v22, v24
	v_fmamk_f32 v24, v76, 0x3a800000, v230
	v_rcp_f32_e32 v25, v25
	v_mul_f32_e32 v22, v22, v23
	v_fmamk_f32 v23, v80, 0x3a800000, v226
	v_min_f32_e32 v24, 0x40e00000, v24
	v_min_f32_e32 v23, 0x40e00000, v23
	v_mul_f32_e32 v28, 0x3fd9db23, v24
	v_mul_f32_e32 v27, 0x3fd9db23, v23
	v_mul_f32_e32 v28, 0xbfb8aa3b, v28
	v_mul_f32_e32 v27, 0xbfb8aa3b, v27
	v_exp_f32_e32 v28, v28
	v_mul_f32_e32 v20, v20, v25
	v_fmamk_f32 v25, v72, 0x3a800000, v234
	v_exp_f32_e32 v27, v27
	v_med3_f32 v25, v25, s59, v189
	v_fmamk_f32 v26, v68, 0x3a800000, v238
	v_med3_f32 v26, v26, s59, v189
	v_add_f32_e32 v25, 1.0, v25
	v_mul_f32_e32 v23, v23, v25
	v_add_f32_e32 v25, 1.0, v28
	v_add_f32_e32 v26, 1.0, v26
	v_add_f32_e32 v27, 1.0, v27
	v_rcp_f32_e32 v25, v25
	v_mul_f32_e32 v24, v24, v26
	v_fmamk_f32 v26, v77, 0x3a800000, v231
	v_rcp_f32_e32 v27, v27
	v_min_f32_e32 v26, 0x40e00000, v26
	v_mul_f32_e32 v30, 0x3fd9db23, v26
	v_mul_f32_e32 v30, 0xbfb8aa3b, v30
	v_mul_f32_e32 v24, v24, v25
	v_fmamk_f32 v25, v81, 0x3a800000, v227
	v_exp_f32_e32 v30, v30
	v_mul_f32_e32 v23, v23, v27
	v_min_f32_e32 v25, 0x40e00000, v25
	v_fmamk_f32 v27, v73, 0x3a800000, v235
	v_med3_f32 v27, v27, s59, v189
	v_mul_f32_e32 v29, 0x3fd9db23, v25
	v_add_f32_e32 v27, 1.0, v27
	v_mul_f32_e32 v29, 0xbfb8aa3b, v29
	v_exp_f32_e32 v29, v29
	v_mul_f32_e32 v25, v25, v27
	v_add_f32_e32 v27, 1.0, v30
	v_fmamk_f32 v28, v69, 0x3a800000, v239
	v_rcp_f32_e32 v27, v27
	v_med3_f32 v28, v28, s59, v189
	v_add_f32_e32 v28, 1.0, v28
	v_add_f32_e32 v29, 1.0, v29
	v_mul_f32_e32 v26, v26, v28
	v_rcp_f32_e32 v29, v29
	v_mul_f32_e32 v26, v26, v27
	v_mul_f32_e32 v0, 4.0, v0
	v_mul_f32_e32 v27, 4.0, v20
	v_mov_b32_e32 v20, v171
	v_cvt_pk_fp8_f32 v20, v0, v27
	v_mul_f32_e32 v0, 4.0, v21
	v_mul_f32_e32 v22, 4.0, v22
	v_mov_b32_e32 v21, v171
	v_cvt_pk_fp8_f32 v21, v0, v22
	v_mul_f32_e32 v25, v25, v29
	v_mul_f32_e32 v23, 4.0, v23
	v_mul_f32_e32 v25, 4.0, v25
	v_mul_f32_e32 v0, 4.0, v24
	v_mul_f32_e32 v22, 4.0, v26
	v_cvt_pk_fp8_f32 v20, v23, v25 op_sel:[0,0,1]
	v_cvt_pk_fp8_f32 v21, v0, v22 op_sel:[0,0,1]
	v_add_co_u32_e32 v22, vcc, s61, v18
	v_fmamk_f32 v0, v62, 0x3a800000, v224
	s_nop 0
	v_addc_co_u32_e32 v23, vcc, 0, v19, vcc
	global_store_dwordx2 v[22:23], v[20:21], off
	v_fmamk_f32 v20, v58, 0x3a800000, v228
	v_min_f32_e32 v20, 0x40e00000, v20
	v_min_f32_e32 v0, 0x40e00000, v0
	v_mul_f32_e32 v24, 0x3fd9db23, v20
	v_mul_f32_e32 v23, 0x3fd9db23, v0
	v_mul_f32_e32 v24, 0xbfb8aa3b, v24
	v_mul_f32_e32 v23, 0xbfb8aa3b, v23
	v_exp_f32_e32 v24, v24
	v_fmamk_f32 v21, v54, 0x3a800000, v232
	v_exp_f32_e32 v23, v23
	v_med3_f32 v21, v21, s59, v189
	v_fmamk_f32 v22, v50, 0x3a800000, v236
	v_med3_f32 v22, v22, s59, v189
	v_add_f32_e32 v21, 1.0, v21
	v_mul_f32_e32 v0, v0, v21
	v_add_f32_e32 v21, 1.0, v24
	v_add_f32_e32 v22, 1.0, v22
	v_add_f32_e32 v23, 1.0, v23
	v_rcp_f32_e32 v21, v21
	v_mul_f32_e32 v20, v20, v22
	v_fmamk_f32 v22, v59, 0x3a800000, v229
	v_rcp_f32_e32 v23, v23
	v_min_f32_e32 v22, 0x40e00000, v22
	v_mul_f32_e32 v26, 0x3fd9db23, v22
	v_mul_f32_e32 v26, 0xbfb8aa3b, v26
	v_mul_f32_e32 v21, v20, v21
	v_fmamk_f32 v20, v63, 0x3a800000, v225
	v_exp_f32_e32 v26, v26
	v_mul_f32_e32 v0, v0, v23
	v_min_f32_e32 v20, 0x40e00000, v20
	v_fmamk_f32 v23, v55, 0x3a800000, v233
	v_med3_f32 v23, v23, s59, v189
	v_mul_f32_e32 v25, 0x3fd9db23, v20
	v_add_f32_e32 v23, 1.0, v23
	v_mul_f32_e32 v25, 0xbfb8aa3b, v25
	v_exp_f32_e32 v25, v25
	v_mul_f32_e32 v20, v20, v23
	v_add_f32_e32 v23, 1.0, v26
	v_fmamk_f32 v24, v51, 0x3a800000, v237
	v_rcp_f32_e32 v23, v23
	v_med3_f32 v24, v24, s59, v189
	v_add_f32_e32 v24, 1.0, v24
	v_add_f32_e32 v25, 1.0, v25
	v_mul_f32_e32 v22, v22, v24
	v_fmamk_f32 v24, v60, 0x3a800000, v230
	v_rcp_f32_e32 v25, v25
	v_mul_f32_e32 v22, v22, v23
	v_fmamk_f32 v23, v64, 0x3a800000, v226
	v_min_f32_e32 v24, 0x40e00000, v24
	v_min_f32_e32 v23, 0x40e00000, v23
	v_mul_f32_e32 v28, 0x3fd9db23, v24
	v_mul_f32_e32 v27, 0x3fd9db23, v23
	v_mul_f32_e32 v28, 0xbfb8aa3b, v28
	v_mul_f32_e32 v27, 0xbfb8aa3b, v27
	v_exp_f32_e32 v28, v28
	v_mul_f32_e32 v20, v20, v25
	v_fmamk_f32 v25, v56, 0x3a800000, v234
	v_exp_f32_e32 v27, v27
	v_med3_f32 v25, v25, s59, v189
	v_fmamk_f32 v26, v52, 0x3a800000, v238
	v_med3_f32 v26, v26, s59, v189
	v_add_f32_e32 v25, 1.0, v25
	v_mul_f32_e32 v23, v23, v25
	v_add_f32_e32 v25, 1.0, v28
	v_add_f32_e32 v26, 1.0, v26
	v_add_f32_e32 v27, 1.0, v27
	v_rcp_f32_e32 v25, v25
	v_mul_f32_e32 v24, v24, v26
	v_fmamk_f32 v26, v61, 0x3a800000, v231
	v_rcp_f32_e32 v27, v27
	v_min_f32_e32 v26, 0x40e00000, v26
	v_mul_f32_e32 v30, 0x3fd9db23, v26
	v_mul_f32_e32 v30, 0xbfb8aa3b, v30
	v_mul_f32_e32 v24, v24, v25
	v_fmamk_f32 v25, v65, 0x3a800000, v227
	v_exp_f32_e32 v30, v30
	v_mul_f32_e32 v23, v23, v27
	v_min_f32_e32 v25, 0x40e00000, v25
	v_fmamk_f32 v27, v57, 0x3a800000, v235
	v_med3_f32 v27, v27, s59, v189
	v_mul_f32_e32 v29, 0x3fd9db23, v25
	v_add_f32_e32 v27, 1.0, v27
	v_mul_f32_e32 v29, 0xbfb8aa3b, v29
	v_exp_f32_e32 v29, v29
	v_mul_f32_e32 v25, v25, v27
	v_add_f32_e32 v27, 1.0, v30
	v_fmamk_f32 v28, v53, 0x3a800000, v239
	v_rcp_f32_e32 v27, v27
	v_med3_f32 v28, v28, s59, v189
	v_add_f32_e32 v28, 1.0, v28
	v_add_f32_e32 v29, 1.0, v29
	v_mul_f32_e32 v26, v26, v28
	v_rcp_f32_e32 v29, v29
	v_mul_f32_e32 v26, v26, v27
	v_mul_f32_e32 v0, 4.0, v0
	v_mul_f32_e32 v27, 4.0, v20
	v_mov_b32_e32 v20, v171
	v_cvt_pk_fp8_f32 v20, v0, v27
	v_mul_f32_e32 v0, 4.0, v21
	v_mul_f32_e32 v22, 4.0, v22
	v_mov_b32_e32 v21, v171
	v_cvt_pk_fp8_f32 v21, v0, v22
	v_mul_f32_e32 v25, v25, v29
	v_mul_f32_e32 v23, 4.0, v23
	v_mul_f32_e32 v25, 4.0, v25
	v_mul_f32_e32 v0, 4.0, v24
	v_mul_f32_e32 v22, 4.0, v26
	v_cvt_pk_fp8_f32 v20, v23, v25 op_sel:[0,0,1]
	v_cvt_pk_fp8_f32 v21, v0, v22 op_sel:[0,0,1]
	v_add_co_u32_e32 v22, vcc, s62, v18
	v_fmamk_f32 v2, v42, 0x3a800000, v228
	s_nop 0
	v_addc_co_u32_e32 v23, vcc, 0, v19, vcc
	v_min_f32_e32 v2, 0x40e00000, v2
	global_store_dwordx2 v[22:23], v[20:21], off
	v_mul_f32_e32 v20, 0x3fd9db23, v2
	v_mul_f32_e32 v20, 0xbfb8aa3b, v20
	v_exp_f32_e32 v20, v20
	v_fmamk_f32 v0, v46, 0x3a800000, v224
	v_fmamk_f32 v10, v38, 0x3a800000, v232
	v_med3_f32 v10, v10, s59, v189
	v_min_f32_e32 v0, 0x40e00000, v0
	v_add_f32_e32 v10, 1.0, v10
	v_mul_f32_e32 v14, 0x3fd9db23, v0
	v_mul_f32_e32 v0, v0, v10
	v_add_f32_e32 v10, 1.0, v20
	v_fmamk_f32 v6, v34, 0x3a800000, v236
	v_rcp_f32_e32 v10, v10
	v_med3_f32 v6, v6, s59, v189
	v_add_f32_e32 v6, 1.0, v6
	v_mul_f32_e32 v14, 0xbfb8aa3b, v14
	v_mul_f32_e32 v2, v2, v6
	v_exp_f32_e32 v14, v14
	v_mul_f32_e32 v6, v2, v10
	v_fmamk_f32 v2, v47, 0x3a800000, v225
	v_min_f32_e32 v2, 0x40e00000, v2
	v_mul_f32_e32 v11, 0x3fd9db23, v2
	v_mul_f32_e32 v11, 0xbfb8aa3b, v11
	v_add_f32_e32 v14, 1.0, v14
	v_exp_f32_e32 v11, v11
	v_rcp_f32_e32 v14, v14
	v_fmamk_f32 v3, v43, 0x3a800000, v229
	v_min_f32_e32 v3, 0x40e00000, v3
	v_fmamk_f32 v7, v35, 0x3a800000, v237
	v_add_f32_e32 v11, 1.0, v11
	v_mul_f32_e32 v0, v0, v14
	v_fmamk_f32 v10, v39, 0x3a800000, v233
	v_med3_f32 v7, v7, s59, v189
	v_mul_f32_e32 v14, 0x3fd9db23, v3
	v_rcp_f32_e32 v11, v11
	v_med3_f32 v10, v10, s59, v189
	v_mul_f32_e32 v14, 0xbfb8aa3b, v14
	v_add_f32_e32 v7, 1.0, v7
	v_add_f32_e32 v10, 1.0, v10
	v_exp_f32_e32 v14, v14
	v_mul_f32_e32 v3, v3, v7
	v_fmamk_f32 v7, v48, 0x3a800000, v226
	v_mul_f32_e32 v2, v2, v10
	v_min_f32_e32 v7, 0x40e00000, v7
	v_mul_f32_e32 v2, v2, v11
	v_mul_f32_e32 v11, 0x3fd9db23, v7
	v_mul_f32_e32 v11, 0xbfb8aa3b, v11
	v_add_f32_e32 v10, 1.0, v14
	v_fmamk_f32 v4, v44, 0x3a800000, v230
	v_exp_f32_e32 v11, v11
	v_rcp_f32_e32 v10, v10
	v_min_f32_e32 v4, 0x40e00000, v4
	v_mul_f32_e32 v12, 0x3fd9db23, v4
	v_mul_f32_e32 v12, 0xbfb8aa3b, v12
	v_exp_f32_e32 v12, v12
	v_add_f32_e32 v11, 1.0, v11
	v_mul_f32_e32 v3, v3, v10
	v_fmamk_f32 v10, v40, 0x3a800000, v234
	v_fmamk_f32 v8, v36, 0x3a800000, v238
	v_rcp_f32_e32 v11, v11
	v_med3_f32 v10, v10, s59, v189
	v_med3_f32 v8, v8, s59, v189
	v_add_f32_e32 v10, 1.0, v10
	v_add_f32_e32 v8, 1.0, v8
	v_fmamk_f32 v13, v49, 0x3a800000, v227
	v_fmamk_f32 v5, v45, 0x3a800000, v231
	v_mul_f32_e32 v7, v7, v10
	v_add_f32_e32 v10, 1.0, v12
	v_mul_f32_e32 v4, v4, v8
	v_min_f32_e32 v8, 0x40e00000, v13
	v_min_f32_e32 v5, 0x40e00000, v5
	v_rcp_f32_e32 v10, v10
	v_mul_f32_e32 v7, v7, v11
	v_mul_f32_e32 v11, 0x3fd9db23, v8
	v_mul_f32_e32 v12, 0x3fd9db23, v5
	v_mul_f32_e32 v11, 0xbfb8aa3b, v11
	v_mul_f32_e32 v12, 0xbfb8aa3b, v12
	v_exp_f32_e32 v11, v11
	v_exp_f32_e32 v12, v12
	v_fmamk_f32 v17, v41, 0x3a800000, v235
	v_mul_f32_e32 v4, v4, v10
	v_med3_f32 v10, v17, s59, v189
	v_fmamk_f32 v9, v37, 0x3a800000, v239
	v_med3_f32 v9, v9, s59, v189
	v_add_f32_e32 v10, 1.0, v10
	v_add_f32_e32 v11, 1.0, v11
	v_mul_f32_e32 v8, v8, v10
	v_add_f32_e32 v10, 1.0, v12
	v_add_f32_e32 v9, 1.0, v9
	v_rcp_f32_e32 v11, v11
	v_rcp_f32_e32 v10, v10
	v_mul_f32_e32 v5, v5, v9
	v_mul_f32_e32 v0, 4.0, v0
	v_mul_f32_e32 v9, 4.0, v2
	v_mov_b32_e32 v2, v171
	v_cvt_pk_fp8_f32 v2, v0, v9
	v_mul_f32_e32 v0, 4.0, v6
	v_mul_f32_e32 v6, 4.0, v3
	v_mov_b32_e32 v3, v171
	v_cvt_pk_fp8_f32 v3, v0, v6
	v_mul_f32_e32 v8, v8, v11
	v_mul_f32_e32 v5, v5, v10
	v_mul_f32_e32 v7, 4.0, v7
	v_mul_f32_e32 v8, 4.0, v8
	v_mul_f32_e32 v0, 4.0, v4
	v_mul_f32_e32 v4, 4.0, v5
	v_cvt_pk_fp8_f32 v2, v7, v8 op_sel:[0,0,1]
	v_cvt_pk_fp8_f32 v3, v0, v4 op_sel:[0,0,1]
	v_add_co_u32_e32 v4, vcc, 0x58000, v18
	s_nop 1
	v_addc_co_u32_e32 v5, vcc, 0, v19, vcc
	s_andn2_b64 vcc, exec, s[4:5]
	s_mov_b64 s[4:5], -1
	global_store_dwordx2 v[4:5], v[2:3], off
	s_cbranch_vccnz .LBB0_1470
	s_andn2_b64 vcc, exec, s[12:13]
	s_cbranch_vccnz .LBB0_1469
	s_barrier
	s_branch .LBB0_1469

.LBB0_1576:
	s_lshl_b32 s1, s38, 8
	s_ashr_i32 s0, s38, 3
	s_and_b32 s1, s1, 0x700
	v_or_b32_e32 v240, s1, v183
	s_ashr_i32 s1, s0, 31
	s_lshl_b64 s[0:1], s[0:1], 13
	s_add_u32 s2, s6, s0
	s_addc_u32 s3, s7, s1
	v_lshlrev_b32_e32 v240, 2, v240
	global_load_dwordx4 v[224:227], v240, s[2:3]
	global_load_dwordx4 v[228:231], v240, s[2:3] offset:16
	global_load_dwordx4 v[232:235], v240, s[2:3] offset:512
	global_load_dwordx4 v[236:239], v240, s[2:3] offset:528
	s_ashr_i32 s27, s26, 31
	s_lshl_b64 s[0:1], s[26:27], 19
	s_add_u32 s30, s49, s0
	s_addc_u32 s31, s50, s1
	s_and_b64 s[0:1], s[4:5], exec
	s_cselect_b32 s27, s31, s43
	s_cselect_b32 s39, s30, s42
	s_ashr_i32 s29, s28, 31
	s_lshl_b64 s[0:1], s[28:29], 19
	s_add_u32 s34, s51, s0
	s_addc_u32 s35, s52, s1
	s_and_b64 s[0:1], s[4:5], exec
	s_cselect_b32 s29, s35, s41
	s_cselect_b32 s68, s34, s40
	s_add_u32 s69, s40, 0x4000
	s_addc_u32 s70, s41, 0
	s_add_u32 s40, s42, 0x40080
	s_addc_u32 s41, s43, 0
	s_mov_b32 s71, -2
	ds_read_b128 v[26:29], v184
	ds_read_b128 v[30:33], v184 offset:1024
	ds_read_b128 v[18:21], v184 offset:2048
	ds_read_b128 v[22:25], v184 offset:3072
	ds_read_b128 v[10:13], v185
	ds_read_b128 v[14:17], v185 offset:1024
	ds_read_b128 v[2:5], v185 offset:2048
	ds_read_b128 v[6:9], v185 offset:3072
	s_add_u32 s0, s40, 0xfffc0080
	s_addc_u32 s1, s41, -1
	s_cmp_eq_u32 s71, 12
	s_cselect_b32 s45, s27, s1
	s_cselect_b32 s44, s39, s0
	s_cselect_b32 s43, s29, s70
	s_cselect_b32 s42, s68, s69
	v_lshl_add_u64 v[178:179], s[40:41], 0, v[172:173]
	s_add_i32 m0, s37, 0xc000
	ds_read_b128 v[188:191], v186
	ds_read_b128 v[192:195], v186 offset:1024
	ds_read_b128 v[196:199], v186 offset:2048
	ds_read_b128 v[200:203], v186 offset:3072
	ds_read_b128 v[204:207], v186 offset:4096
	ds_read_b128 v[208:211], v186 offset:5120
	ds_read_b128 v[212:215], v186 offset:6144
	ds_read_b128 v[216:219], v186 offset:7168
	global_load_lds_dwordx4 v[178:179], off
	v_lshl_add_u64 v[178:179], s[40:41], 0, v[174:175]
	s_add_i32 m0, s37, 0xe000
	s_nop 0
	global_load_lds_dwordx4 v[178:179], off
	s_waitcnt vmcnt(8)
	s_waitcnt lgkmcnt(0)
	s_barrier
	s_setprio 1
	s_waitcnt lgkmcnt(0)
	v_mfma_scale_f32_16x16x128_f8f6f4 v[158:161], v[26:33], v[188:195], 0, v187, v187 op_sel_hi:[0,0,0]
	v_mfma_scale_f32_16x16x128_f8f6f4 v[154:157], v[18:25], v[188:195], 0, v187, v187 op_sel_hi:[0,0,0]
	v_mfma_scale_f32_16x16x128_f8f6f4 v[150:153], v[26:33], v[196:203], 0, v187, v187 op_sel_hi:[0,0,0]
	v_mfma_scale_f32_16x16x128_f8f6f4 v[146:149], v[18:25], v[196:203], 0, v187, v187 op_sel_hi:[0,0,0]
	v_mfma_scale_f32_16x16x128_f8f6f4 v[142:145], v[26:33], v[204:211], 0, v187, v187 op_sel_hi:[0,0,0]
	v_mfma_scale_f32_16x16x128_f8f6f4 v[138:141], v[18:25], v[204:211], 0, v187, v187 op_sel_hi:[0,0,0]
	v_mfma_scale_f32_16x16x128_f8f6f4 v[134:137], v[26:33], v[212:219], 0, v187, v187 op_sel_hi:[0,0,0]
	v_mfma_scale_f32_16x16x128_f8f6f4 v[130:133], v[18:25], v[212:219], 0, v187, v187 op_sel_hi:[0,0,0]
	s_setprio 0
	s_setprio 1
	v_mfma_scale_f32_16x16x128_f8f6f4 v[102:105], v[10:17], v[188:195], 0, v187, v187 op_sel_hi:[0,0,0]
	v_mfma_scale_f32_16x16x128_f8f6f4 v[98:101], v[2:9], v[188:195], 0, v187, v187 op_sel_hi:[0,0,0]
	v_mfma_scale_f32_16x16x128_f8f6f4 v[86:89], v[10:17], v[196:203], 0, v187, v187 op_sel_hi:[0,0,0]
	v_mfma_scale_f32_16x16x128_f8f6f4 v[82:85], v[2:9], v[196:203], 0, v187, v187 op_sel_hi:[0,0,0]
	v_mfma_scale_f32_16x16x128_f8f6f4 v[78:81], v[10:17], v[204:211], 0, v187, v187 op_sel_hi:[0,0,0]
	v_mfma_scale_f32_16x16x128_f8f6f4 v[74:77], v[2:9], v[204:211], 0, v187, v187 op_sel_hi:[0,0,0]
	v_mfma_scale_f32_16x16x128_f8f6f4 v[70:73], v[10:17], v[212:219], 0, v187, v187 op_sel_hi:[0,0,0]
	v_mfma_scale_f32_16x16x128_f8f6f4 v[66:69], v[2:9], v[212:219], 0, v187, v187 op_sel_hi:[0,0,0]
	s_setprio 0
	s_barrier
	s_add_i32 s0, s62, s53
	v_lshl_add_u64 v[178:179], s[42:43], 0, v[164:165]
	s_mov_b32 m0, s0
	ds_read_b128 v[188:191], v186 offset:16384
	ds_read_b128 v[192:195], v186 offset:17408
	ds_read_b128 v[196:199], v186 offset:18432
	ds_read_b128 v[200:203], v186 offset:19456
	ds_read_b128 v[204:207], v186 offset:20480
	ds_read_b128 v[208:211], v186 offset:21504
	ds_read_b128 v[212:215], v186 offset:22528
	ds_read_b128 v[216:219], v186 offset:23552
	global_load_lds_dwordx4 v[178:179], off
	s_add_i32 m0, s0, 0x2000
	s_add_u32 s0, s42, 0x40000
	v_lshl_add_u64 v[178:179], s[42:43], 0, v[168:169]
	s_addc_u32 s1, s43, 0
	s_add_i32 s2, s63, s53
	global_load_lds_dwordx4 v[178:179], off
	v_lshl_add_u64 v[178:179], s[0:1], 0, v[164:165]
	s_mov_b32 m0, s2
	v_lshl_add_u64 v[180:181], s[44:45], 0, v[166:167]
	global_load_lds_dwordx4 v[178:179], off
	v_lshl_add_u64 v[178:179], s[0:1], 0, v[168:169]
	s_add_i32 m0, s2, 0x2000
	s_nop 0
	global_load_lds_dwordx4 v[178:179], off
	v_lshl_add_u64 v[178:179], s[44:45], 0, v[162:163]
	s_mov_b32 m0, s37
	s_nop 0
	global_load_lds_dwordx4 v[178:179], off
	s_mov_b32 m0, s54
	s_nop 0
	global_load_lds_dwordx4 v[180:181], off
	s_waitcnt vmcnt(8)
	s_waitcnt lgkmcnt(0)
	s_barrier
	s_setprio 1
	s_waitcnt lgkmcnt(0)
	v_mfma_scale_f32_16x16x128_f8f6f4 v[126:129], v[26:33], v[188:195], 0, v187, v187 op_sel_hi:[0,0,0]
	v_mfma_scale_f32_16x16x128_f8f6f4 v[122:125], v[18:25], v[188:195], 0, v187, v187 op_sel_hi:[0,0,0]
	v_mfma_scale_f32_16x16x128_f8f6f4 v[118:121], v[26:33], v[196:203], 0, v187, v187 op_sel_hi:[0,0,0]
	v_mfma_scale_f32_16x16x128_f8f6f4 v[114:117], v[18:25], v[196:203], 0, v187, v187 op_sel_hi:[0,0,0]
	v_mfma_scale_f32_16x16x128_f8f6f4 v[110:113], v[26:33], v[204:211], 0, v187, v187 op_sel_hi:[0,0,0]
	v_mfma_scale_f32_16x16x128_f8f6f4 v[106:109], v[18:25], v[204:211], 0, v187, v187 op_sel_hi:[0,0,0]
	v_mfma_scale_f32_16x16x128_f8f6f4 v[94:97], v[26:33], v[212:219], 0, v187, v187 op_sel_hi:[0,0,0]
	v_mfma_scale_f32_16x16x128_f8f6f4 v[90:93], v[18:25], v[212:219], 0, v187, v187 op_sel_hi:[0,0,0]
	s_setprio 0
	s_setprio 1
	v_mfma_scale_f32_16x16x128_f8f6f4 v[62:65], v[10:17], v[188:195], 0, v187, v187 op_sel_hi:[0,0,0]
	v_mfma_scale_f32_16x16x128_f8f6f4 v[58:61], v[2:9], v[188:195], 0, v187, v187 op_sel_hi:[0,0,0]
	v_mfma_scale_f32_16x16x128_f8f6f4 v[54:57], v[10:17], v[196:203], 0, v187, v187 op_sel_hi:[0,0,0]
	v_mfma_scale_f32_16x16x128_f8f6f4 v[50:53], v[2:9], v[196:203], 0, v187, v187 op_sel_hi:[0,0,0]
	v_mfma_scale_f32_16x16x128_f8f6f4 v[46:49], v[10:17], v[204:211], 0, v187, v187 op_sel_hi:[0,0,0]
	v_mfma_scale_f32_16x16x128_f8f6f4 v[42:45], v[2:9], v[204:211], 0, v187, v187 op_sel_hi:[0,0,0]
	v_mfma_scale_f32_16x16x128_f8f6f4 v[38:41], v[10:17], v[212:219], 0, v187, v187 op_sel_hi:[0,0,0]
	v_mfma_scale_f32_16x16x128_f8f6f4 v[34:37], v[2:9], v[212:219], 0, v187, v187 op_sel_hi:[0,0,0]
	s_setprio 0
	s_barrier
	s_branch .Lmid_1577

.Lmid_1577:
	s_add_i32 s2, 0, 0x18000
	v_add_u32_e32 v0, s2, v182
	s_add_i32 s3, 0, 0x1c000
	ds_read_b128 v[2:5], v0
	ds_read_b128 v[6:9], v0 offset:1024
	ds_read_b128 v[10:13], v0 offset:2048
	ds_read_b128 v[14:17], v0 offset:3072
	v_add_u32_e32 v0, s3, v182
	ds_read_b128 v[18:21], v0
	ds_read_b128 v[22:25], v0 offset:1024
	ds_read_b128 v[26:29], v0 offset:2048
	ds_read_b128 v[30:33], v0 offset:3072
	s_add_u32 s0, s44, 0x40000
	s_addc_u32 s1, s45, 0
	s_mov_b32 m0, s55
	v_lshl_add_u64 v[220:221], s[0:1], 0, v[162:163]
	ds_read_b128 v[188:191], v186 offset:32768
	ds_read_b128 v[192:195], v186 offset:33792
	ds_read_b128 v[196:199], v186 offset:34816
	ds_read_b128 v[200:203], v186 offset:35840
	ds_read_b128 v[204:207], v186 offset:36864
	ds_read_b128 v[208:211], v186 offset:37888
	ds_read_b128 v[212:215], v186 offset:38912
	ds_read_b128 v[216:219], v186 offset:39936
	global_load_lds_dwordx4 v[220:221], off
	v_lshl_add_u64 v[220:221], s[0:1], 0, v[166:167]
	s_mov_b32 m0, s56
	s_nop 0
	global_load_lds_dwordx4 v[220:221], off
	s_waitcnt vmcnt(8)
	s_waitcnt lgkmcnt(0)
	s_barrier
	s_setprio 1
	s_waitcnt lgkmcnt(0)
	v_mfma_scale_f32_16x16x128_f8f6f4 v[158:161], v[2:9], v[188:195], v[158:161], v187, v187 op_sel_hi:[0,0,0]
	v_mfma_scale_f32_16x16x128_f8f6f4 v[154:157], v[10:17], v[188:195], v[154:157], v187, v187 op_sel_hi:[0,0,0]
	v_mfma_scale_f32_16x16x128_f8f6f4 v[150:153], v[2:9], v[196:203], v[150:153], v187, v187 op_sel_hi:[0,0,0]
	v_mfma_scale_f32_16x16x128_f8f6f4 v[146:149], v[10:17], v[196:203], v[146:149], v187, v187 op_sel_hi:[0,0,0]
	v_mfma_scale_f32_16x16x128_f8f6f4 v[142:145], v[2:9], v[204:211], v[142:145], v187, v187 op_sel_hi:[0,0,0]
	v_mfma_scale_f32_16x16x128_f8f6f4 v[138:141], v[10:17], v[204:211], v[138:141], v187, v187 op_sel_hi:[0,0,0]
	v_mfma_scale_f32_16x16x128_f8f6f4 v[134:137], v[2:9], v[212:219], v[134:137], v187, v187 op_sel_hi:[0,0,0]
	v_mfma_scale_f32_16x16x128_f8f6f4 v[130:133], v[10:17], v[212:219], v[130:133], v187, v187 op_sel_hi:[0,0,0]
	s_setprio 0
	s_setprio 1
	v_mfma_scale_f32_16x16x128_f8f6f4 v[102:105], v[18:25], v[188:195], v[102:105], v187, v187 op_sel_hi:[0,0,0]
	v_mfma_scale_f32_16x16x128_f8f6f4 v[98:101], v[26:33], v[188:195], v[98:101], v187, v187 op_sel_hi:[0,0,0]
	v_mfma_scale_f32_16x16x128_f8f6f4 v[86:89], v[18:25], v[196:203], v[86:89], v187, v187 op_sel_hi:[0,0,0]
	v_mfma_scale_f32_16x16x128_f8f6f4 v[82:85], v[26:33], v[196:203], v[82:85], v187, v187 op_sel_hi:[0,0,0]
	v_mfma_scale_f32_16x16x128_f8f6f4 v[78:81], v[18:25], v[204:211], v[78:81], v187, v187 op_sel_hi:[0,0,0]
	v_mfma_scale_f32_16x16x128_f8f6f4 v[74:77], v[26:33], v[204:211], v[74:77], v187, v187 op_sel_hi:[0,0,0]
	v_mfma_scale_f32_16x16x128_f8f6f4 v[70:73], v[18:25], v[212:219], v[70:73], v187, v187 op_sel_hi:[0,0,0]
	v_mfma_scale_f32_16x16x128_f8f6f4 v[66:69], v[26:33], v[212:219], v[66:69], v187, v187 op_sel_hi:[0,0,0]
	s_setprio 0
	s_barrier
	s_add_u32 s0, s42, 0x2000
	s_addc_u32 s1, s43, 0
	s_add_i32 s2, s2, s53
	v_lshl_add_u64 v[220:221], s[0:1], 0, v[164:165]
	s_mov_b32 m0, s2
	ds_read_b128 v[188:191], v186 offset:49152
	ds_read_b128 v[192:195], v186 offset:50176
	ds_read_b128 v[196:199], v186 offset:51200
	ds_read_b128 v[200:203], v186 offset:52224
	ds_read_b128 v[204:207], v186 offset:53248
	ds_read_b128 v[208:211], v186 offset:54272
	ds_read_b128 v[212:215], v186 offset:55296
	ds_read_b128 v[216:219], v186 offset:56320
	global_load_lds_dwordx4 v[220:221], off
	s_add_i32 m0, s2, 0x2000
	v_lshl_add_u64 v[220:221], s[0:1], 0, v[168:169]
	s_add_u32 s0, s42, 0x42000
	s_addc_u32 s1, s43, 0
	s_add_i32 s2, s3, s53
	global_load_lds_dwordx4 v[220:221], off
	v_lshl_add_u64 v[220:221], s[0:1], 0, v[164:165]
	s_mov_b32 m0, s2
	v_lshl_add_u64 v[178:179], v[178:179], 0, s[14:15]
	global_load_lds_dwordx4 v[220:221], off
	v_lshl_add_u64 v[220:221], s[0:1], 0, v[168:169]
	s_add_i32 m0, s2, 0x2000
	s_nop 0
	global_load_lds_dwordx4 v[220:221], off
	s_mov_b32 m0, s58
	s_nop 0
	global_load_lds_dwordx4 v[178:179], off
	v_lshl_add_u64 v[178:179], v[180:181], 0, s[14:15]
	s_mov_b32 m0, s59
	s_nop 0
	global_load_lds_dwordx4 v[178:179], off
	s_waitcnt vmcnt(8)
	s_waitcnt lgkmcnt(0)
	s_barrier
	s_setprio 1
	s_waitcnt lgkmcnt(0)
	v_mfma_scale_f32_16x16x128_f8f6f4 v[126:129], v[2:9], v[188:195], v[126:129], v187, v187 op_sel_hi:[0,0,0]
	v_mfma_scale_f32_16x16x128_f8f6f4 v[122:125], v[10:17], v[188:195], v[122:125], v187, v187 op_sel_hi:[0,0,0]
	v_mfma_scale_f32_16x16x128_f8f6f4 v[118:121], v[2:9], v[196:203], v[118:121], v187, v187 op_sel_hi:[0,0,0]
	v_mfma_scale_f32_16x16x128_f8f6f4 v[114:117], v[10:17], v[196:203], v[114:117], v187, v187 op_sel_hi:[0,0,0]
	v_mfma_scale_f32_16x16x128_f8f6f4 v[110:113], v[2:9], v[204:211], v[110:113], v187, v187 op_sel_hi:[0,0,0]
	v_mfma_scale_f32_16x16x128_f8f6f4 v[106:109], v[10:17], v[204:211], v[106:109], v187, v187 op_sel_hi:[0,0,0]
	v_mfma_scale_f32_16x16x128_f8f6f4 v[94:97], v[2:9], v[212:219], v[94:97], v187, v187 op_sel_hi:[0,0,0]
	v_mfma_scale_f32_16x16x128_f8f6f4 v[90:93], v[10:17], v[212:219], v[90:93], v187, v187 op_sel_hi:[0,0,0]
	s_setprio 0
	s_setprio 1
	v_mfma_scale_f32_16x16x128_f8f6f4 v[62:65], v[18:25], v[188:195], v[62:65], v187, v187 op_sel_hi:[0,0,0]
	v_mfma_scale_f32_16x16x128_f8f6f4 v[58:61], v[26:33], v[188:195], v[58:61], v187, v187 op_sel_hi:[0,0,0]
	v_mfma_scale_f32_16x16x128_f8f6f4 v[54:57], v[18:25], v[196:203], v[54:57], v187, v187 op_sel_hi:[0,0,0]
	v_mfma_scale_f32_16x16x128_f8f6f4 v[50:53], v[26:33], v[196:203], v[50:53], v187, v187 op_sel_hi:[0,0,0]
	v_mfma_scale_f32_16x16x128_f8f6f4 v[46:49], v[18:25], v[204:211], v[46:49], v187, v187 op_sel_hi:[0,0,0]
	v_mfma_scale_f32_16x16x128_f8f6f4 v[42:45], v[26:33], v[204:211], v[42:45], v187, v187 op_sel_hi:[0,0,0]
	v_mfma_scale_f32_16x16x128_f8f6f4 v[38:41], v[18:25], v[212:219], v[38:41], v187, v187 op_sel_hi:[0,0,0]
	v_mfma_scale_f32_16x16x128_f8f6f4 v[34:37], v[26:33], v[212:219], v[34:37], v187, v187 op_sel_hi:[0,0,0]
	s_setprio 0
	s_barrier
	s_add_i32 s71, s71, 2
	s_add_u32 s69, s69, 0x4000
	s_addc_u32 s70, s70, 0
	s_add_u32 s40, s40, 0x100
	s_addc_u32 s41, s41, 0
	s_cmp_gt_u32 s71, 13
	s_cbranch_scc0 .LBB0_1577
	s_and_b64 vcc, exec, s[16:17]
	s_cbranch_vccz .LBB0_1580
	s_barrier
.LBB0_1580:
	s_lshl_b32 s1, s38, 8
	s_ashr_i32 s0, s38, 3
	s_and_b32 s1, s1, 0x700
	v_or_b32_e32 v170, s1, v183
	v_mov_b32_e32 v16, v171
	v_mov_b32_e32 v17, v171
	v_mov_b32_e32 v18, v171
	v_mov_b32_e32 v19, v171
	v_mov_b32_e32 v20, v171
	v_mov_b32_e32 v21, v171
	v_lshl_add_u32 v10, s36, 8, v1
	v_ashrrev_i32_e32 v11, 31, v10
	v_or_b32_e32 v12, 16, v10
	v_or_b32_e32 v14, 32, v10
	v_or_b32_e32 v24, 48, v10
	v_lshlrev_b64 v[10:11], 11, v[10:11]
	v_ashrrev_i32_e32 v13, 31, v12
	v_ashrrev_i32_e32 v15, 31, v14
	v_lshl_add_u64 v[10:11], s[12:13], 0, v[10:11]
	v_lshlrev_b64 v[12:13], 11, v[12:13]
	v_lshlrev_b64 v[14:15], 11, v[14:15]
	v_lshl_add_u64 v[10:11], v[10:11], 0, v[170:171]
	v_lshl_add_u64 v[12:13], s[12:13], 0, v[12:13]
	v_lshl_add_u64 v[14:15], s[12:13], 0, v[14:15]
	v_mov_b32_e32 v22, v171
	v_lshl_add_u64 v[12:13], v[12:13], 0, v[170:171]
	v_lshl_add_u64 v[14:15], v[14:15], 0, v[170:171]
	v_pk_fma_f32 v[28:29], v[158:159], s[18:19], v[224:225] op_sel_hi:[1,0,1]
	v_pk_fma_f32 v[32:33], v[154:155], s[18:19], v[228:229] op_sel_hi:[1,0,1]
	v_pk_fma_f32 v[150:151], v[150:151], s[18:19], v[224:225] op_sel_hi:[1,0,1]
	v_pk_fma_f32 v[146:147], v[146:147], s[18:19], v[228:229] op_sel_hi:[1,0,1]
	v_mul_f32_e32 v23, 0x41800000, v28
	v_mul_f32_e32 v25, 0x41800000, v29
	v_mul_f32_e32 v28, 0x41800000, v32
	v_mul_f32_e32 v29, 0x41800000, v33
	v_pk_fma_f32 v[142:143], v[142:143], s[18:19], v[224:225] op_sel_hi:[1,0,1]
	v_pk_fma_f32 v[138:139], v[138:139], s[18:19], v[228:229] op_sel_hi:[1,0,1]
	v_mul_f32_e32 v32, 0x41800000, v150
	v_mul_f32_e32 v33, 0x41800000, v151
	v_mul_f32_e32 v146, 0x41800000, v146
	v_mul_f32_e32 v147, 0x41800000, v147
	v_cvt_pk_fp8_f32 v16, v23, v25
	v_cvt_pk_fp8_f32 v17, v28, v29
	v_mul_f32_e32 v142, 0x41800000, v142
	v_mul_f32_e32 v143, 0x41800000, v143
	v_mul_f32_e32 v138, 0x41800000, v138
	v_mul_f32_e32 v139, 0x41800000, v139
	v_cvt_pk_fp8_f32 v18, v32, v33
	v_cvt_pk_fp8_f32 v19, v146, v147
	v_pk_fma_f32 v[26:27], v[160:161], s[18:19], v[226:227] op_sel_hi:[1,0,1]
	v_pk_fma_f32 v[30:31], v[156:157], s[18:19], v[230:231] op_sel_hi:[1,0,1]
	v_cvt_pk_fp8_f32 v20, v142, v143
	v_cvt_pk_fp8_f32 v21, v138, v139
	v_pk_fma_f32 v[152:153], v[152:153], s[18:19], v[226:227] op_sel_hi:[1,0,1]
	v_pk_fma_f32 v[148:149], v[148:149], s[18:19], v[230:231] op_sel_hi:[1,0,1]
	v_mul_f32_e32 v26, 0x41800000, v26
	v_mul_f32_e32 v27, 0x41800000, v27
	v_mul_f32_e32 v30, 0x41800000, v30
	v_mul_f32_e32 v31, 0x41800000, v31
	v_pk_fma_f32 v[144:145], v[144:145], s[18:19], v[226:227] op_sel_hi:[1,0,1]
	v_pk_fma_f32 v[140:141], v[140:141], s[18:19], v[230:231] op_sel_hi:[1,0,1]
	v_mul_f32_e32 v150, 0x41800000, v152
	v_mul_f32_e32 v151, 0x41800000, v153
	v_mul_f32_e32 v148, 0x41800000, v148
	v_mul_f32_e32 v149, 0x41800000, v149
	v_cvt_pk_fp8_f32 v16, v26, v27 op_sel:[0,0,1]
	v_cvt_pk_fp8_f32 v17, v30, v31 op_sel:[0,0,1]
	v_mul_f32_e32 v144, 0x41800000, v144
	v_mul_f32_e32 v145, 0x41800000, v145
	v_mul_f32_e32 v140, 0x41800000, v140
	v_mul_f32_e32 v141, 0x41800000, v141
	v_cvt_pk_fp8_f32 v18, v150, v151 op_sel:[0,0,1]
	v_cvt_pk_fp8_f32 v19, v148, v149 op_sel:[0,0,1]
	v_cvt_pk_fp8_f32 v20, v144, v145 op_sel:[0,0,1]
	v_cvt_pk_fp8_f32 v21, v140, v141 op_sel:[0,0,1]
	v_pk_fma_f32 v[134:135], v[134:135], s[18:19], v[224:225] op_sel_hi:[1,0,1]
	v_pk_fma_f32 v[130:131], v[130:131], s[18:19], v[228:229] op_sel_hi:[1,0,1]
	v_mul_f32_e32 v134, 0x41800000, v134
	v_mul_f32_e32 v135, 0x41800000, v135
	v_mul_f32_e32 v130, 0x41800000, v130
	global_store_dwordx2 v[10:11], v[16:17], off
	global_store_dwordx2 v[12:13], v[18:19], off
	global_store_dwordx2 v[14:15], v[20:21], off
	v_mul_f32_e32 v16, 0x41800000, v131
	v_mov_b32_e32 v23, v171
	v_cvt_pk_fp8_f32 v22, v134, v135
	v_cvt_pk_fp8_f32 v23, v130, v16
	v_pk_fma_f32 v[136:137], v[136:137], s[18:19], v[226:227] op_sel_hi:[1,0,1]
	v_pk_fma_f32 v[132:133], v[132:133], s[18:19], v[230:231] op_sel_hi:[1,0,1]
	v_mul_f32_e32 v136, 0x41800000, v136
	v_mul_f32_e32 v137, 0x41800000, v137
	v_mul_f32_e32 v16, 0x41800000, v132
	v_mul_f32_e32 v17, 0x41800000, v133
	v_ashrrev_i32_e32 v25, 31, v24
	v_pk_fma_f32 v[18:19], v[128:129], s[18:19], v[226:227] op_sel_hi:[1,0,1]
	v_pk_fma_f32 v[20:21], v[126:127], s[18:19], v[224:225] op_sel_hi:[1,0,1]
	v_cvt_pk_fp8_f32 v22, v136, v137 op_sel:[0,0,1]
	v_cvt_pk_fp8_f32 v23, v16, v17 op_sel:[0,0,1]
	v_lshlrev_b64 v[16:17], 11, v[24:25]
	v_pk_fma_f32 v[24:25], v[122:123], s[18:19], v[228:229] op_sel_hi:[1,0,1]
	v_mul_f32_e32 v20, 0x41800000, v20
	v_mul_f32_e32 v21, 0x41800000, v21
	v_mul_f32_e32 v26, 0x41800000, v18
	v_mov_b32_e32 v18, v171
	v_mul_f32_e32 v27, 0x41800000, v19
	v_cvt_pk_fp8_f32 v18, v20, v21
	v_mul_f32_e32 v20, 0x41800000, v24
	v_mul_f32_e32 v21, 0x41800000, v25
	v_mov_b32_e32 v19, v171
	v_lshl_add_u64 v[16:17], s[12:13], 0, v[16:17]
	v_cvt_pk_fp8_f32 v19, v20, v21
	v_lshl_add_u64 v[16:17], v[16:17], 0, v[170:171]
	global_store_dwordx2 v[16:17], v[22:23], off
	v_pk_fma_f32 v[22:23], v[124:125], s[18:19], v[230:231] op_sel_hi:[1,0,1]
	v_cvt_pk_fp8_f32 v18, v26, v27 op_sel:[0,0,1]
	v_mul_f32_e32 v20, 0x41800000, v22
	v_mul_f32_e32 v21, 0x41800000, v23
	v_cvt_pk_fp8_f32 v19, v20, v21 op_sel:[0,0,1]
	v_add_co_u32_e32 v20, vcc, s64, v10
	v_pk_fma_f32 v[24:25], v[114:115], s[18:19], v[228:229] op_sel_hi:[1,0,1]
	s_nop 0
	v_addc_co_u32_e32 v21, vcc, 0, v11, vcc
	global_store_dwordx2 v[20:21], v[18:19], off
	v_pk_fma_f32 v[18:19], v[120:121], s[18:19], v[226:227] op_sel_hi:[1,0,1]
	v_pk_fma_f32 v[20:21], v[118:119], s[18:19], v[224:225] op_sel_hi:[1,0,1]
	v_mul_f32_e32 v26, 0x41800000, v18
	v_mul_f32_e32 v20, 0x41800000, v20
	v_mul_f32_e32 v21, 0x41800000, v21
	v_mov_b32_e32 v18, v171
	v_mul_f32_e32 v27, 0x41800000, v19
	v_cvt_pk_fp8_f32 v18, v20, v21
	v_mul_f32_e32 v20, 0x41800000, v24
	v_mul_f32_e32 v21, 0x41800000, v25
	v_mov_b32_e32 v19, v171
	v_cvt_pk_fp8_f32 v19, v20, v21
	v_pk_fma_f32 v[22:23], v[116:117], s[18:19], v[230:231] op_sel_hi:[1,0,1]
	v_cvt_pk_fp8_f32 v18, v26, v27 op_sel:[0,0,1]
	v_mul_f32_e32 v20, 0x41800000, v22
	v_mul_f32_e32 v21, 0x41800000, v23
	v_cvt_pk_fp8_f32 v19, v20, v21 op_sel:[0,0,1]
	v_add_co_u32_e32 v20, vcc, s65, v10
	v_pk_fma_f32 v[24:25], v[106:107], s[18:19], v[228:229] op_sel_hi:[1,0,1]
	s_nop 0
	v_addc_co_u32_e32 v21, vcc, 0, v11, vcc
	global_store_dwordx2 v[20:21], v[18:19], off
	v_pk_fma_f32 v[18:19], v[112:113], s[18:19], v[226:227] op_sel_hi:[1,0,1]
	v_pk_fma_f32 v[20:21], v[110:111], s[18:19], v[224:225] op_sel_hi:[1,0,1]
	v_mul_f32_e32 v26, 0x41800000, v18
	v_mul_f32_e32 v20, 0x41800000, v20
	v_mul_f32_e32 v21, 0x41800000, v21
	v_mov_b32_e32 v18, v171
	v_mul_f32_e32 v27, 0x41800000, v19
	v_cvt_pk_fp8_f32 v18, v20, v21
	v_mul_f32_e32 v20, 0x41800000, v24
	v_mul_f32_e32 v21, 0x41800000, v25
	v_mov_b32_e32 v19, v171
	v_cvt_pk_fp8_f32 v19, v20, v21
	v_pk_fma_f32 v[22:23], v[108:109], s[18:19], v[230:231] op_sel_hi:[1,0,1]
	v_cvt_pk_fp8_f32 v18, v26, v27 op_sel:[0,0,1]
	v_mul_f32_e32 v20, 0x41800000, v22
	v_mul_f32_e32 v21, 0x41800000, v23
	v_cvt_pk_fp8_f32 v19, v20, v21 op_sel:[0,0,1]
	v_add_co_u32_e32 v20, vcc, s66, v10
	v_pk_fma_f32 v[6:7], v[94:95], s[18:19], v[224:225] op_sel_hi:[1,0,1]
	s_nop 0
	v_addc_co_u32_e32 v21, vcc, 0, v11, vcc
	global_store_dwordx2 v[20:21], v[18:19], off
	v_pk_fma_f32 v[2:3], v[90:91], s[18:19], v[228:229] op_sel_hi:[1,0,1]
	v_mul_f32_e32 v18, 0x41800000, v6
	v_mul_f32_e32 v7, 0x41800000, v7
	v_mov_b32_e32 v6, v171
	v_cvt_pk_fp8_f32 v6, v18, v7
	v_mul_f32_e32 v2, 0x41800000, v2
	v_mul_f32_e32 v3, 0x41800000, v3
	v_mov_b32_e32 v7, v171
	v_cvt_pk_fp8_f32 v7, v2, v3
	v_pk_fma_f32 v[8:9], v[96:97], s[18:19], v[226:227] op_sel_hi:[1,0,1]
	v_pk_fma_f32 v[4:5], v[92:93], s[18:19], v[230:231] op_sel_hi:[1,0,1]
	v_mul_f32_e32 v8, 0x41800000, v8
	v_mul_f32_e32 v9, 0x41800000, v9
	v_mul_f32_e32 v2, 0x41800000, v4
	v_mul_f32_e32 v3, 0x41800000, v5
	v_cvt_pk_fp8_f32 v6, v8, v9 op_sel:[0,0,1]
	v_cvt_pk_fp8_f32 v7, v2, v3 op_sel:[0,0,1]
	v_add_co_u32_e32 v2, vcc, s67, v10
	v_lshl_add_u64 v[18:19], v[10:11], 0, s[8:9]
	s_nop 0
	v_addc_co_u32_e32 v3, vcc, 0, v11, vcc
	global_store_dwordx2 v[2:3], v[6:7], off
	s_nop 0
	v_lshl_add_u64 v[20:21], v[10:11], 0, s[20:21]
	v_lshl_add_u64 v[22:23], v[10:11], 0, s[22:23]
	v_lshl_add_u64 v[24:25], v[10:11], 0, s[24:25]
	s_andn2_b64 vcc, exec, s[4:5]
	s_mov_b64 s[4:5], -1
	v_pk_fma_f32 v[26:27], v[104:105], s[18:19], v[234:235] op_sel_hi:[1,0,1]
	v_pk_fma_f32 v[28:29], v[102:103], s[18:19], v[232:233] op_sel_hi:[1,0,1]
	v_pk_fma_f32 v[32:33], v[98:99], s[18:19], v[236:237] op_sel_hi:[1,0,1]
	v_mul_f32_e32 v0, 0x41800000, v28
	v_mul_f32_e32 v28, 0x41800000, v29
	v_mul_f32_e32 v29, 0x41800000, v26
	v_mov_b32_e32 v26, v171
	v_mul_f32_e32 v90, 0x41800000, v27
	v_cvt_pk_fp8_f32 v26, v0, v28
	v_mul_f32_e32 v0, 0x41800000, v32
	v_mul_f32_e32 v28, 0x41800000, v33
	v_mov_b32_e32 v27, v171
	v_cvt_pk_fp8_f32 v27, v0, v28
	v_pk_fma_f32 v[30:31], v[100:101], s[18:19], v[238:239] op_sel_hi:[1,0,1]
	v_cvt_pk_fp8_f32 v26, v29, v90 op_sel:[0,0,1]
	v_mul_f32_e32 v0, 0x41800000, v30
	v_mul_f32_e32 v28, 0x41800000, v31
	v_cvt_pk_fp8_f32 v27, v0, v28 op_sel:[0,0,1]
	v_pk_fma_f32 v[28:29], v[88:89], s[18:19], v[234:235] op_sel_hi:[1,0,1]
	v_pk_fma_f32 v[30:31], v[86:87], s[18:19], v[232:233] op_sel_hi:[1,0,1]
	v_pk_fma_f32 v[82:83], v[82:83], s[18:19], v[236:237] op_sel_hi:[1,0,1]
	v_mul_f32_e32 v0, 0x41800000, v30
	v_mul_f32_e32 v30, 0x41800000, v31
	v_mul_f32_e32 v31, 0x41800000, v28
	v_mov_b32_e32 v28, v171
	v_pk_fma_f32 v[32:33], v[84:85], s[18:19], v[238:239] op_sel_hi:[1,0,1]
	v_mul_f32_e32 v84, 0x41800000, v29
	v_cvt_pk_fp8_f32 v28, v0, v30
	v_mul_f32_e32 v0, 0x41800000, v82
	v_mul_f32_e32 v30, 0x41800000, v83
	v_mov_b32_e32 v29, v171
	v_cvt_pk_fp8_f32 v29, v0, v30
	v_mul_f32_e32 v0, 0x41800000, v32
	v_mul_f32_e32 v30, 0x41800000, v33
	v_cvt_pk_fp8_f32 v28, v31, v84 op_sel:[0,0,1]
	v_cvt_pk_fp8_f32 v29, v0, v30 op_sel:[0,0,1]
	v_pk_fma_f32 v[30:31], v[80:81], s[18:19], v[234:235] op_sel_hi:[1,0,1]
	v_pk_fma_f32 v[32:33], v[78:79], s[18:19], v[232:233] op_sel_hi:[1,0,1]
	v_pk_fma_f32 v[74:75], v[74:75], s[18:19], v[236:237] op_sel_hi:[1,0,1]
	v_mul_f32_e32 v0, 0x41800000, v32
	v_mul_f32_e32 v32, 0x41800000, v33
	v_mul_f32_e32 v33, 0x41800000, v30
	v_mov_b32_e32 v30, v171
	v_mul_f32_e32 v78, 0x41800000, v31
	v_cvt_pk_fp8_f32 v30, v0, v32
	v_mul_f32_e32 v0, 0x41800000, v74
	v_mul_f32_e32 v32, 0x41800000, v75
	v_mov_b32_e32 v31, v171
	v_cvt_pk_fp8_f32 v31, v0, v32
	v_pk_fma_f32 v[76:77], v[76:77], s[18:19], v[238:239] op_sel_hi:[1,0,1]
	v_cvt_pk_fp8_f32 v30, v33, v78 op_sel:[0,0,1]
	v_mul_f32_e32 v0, 0x41800000, v76
	v_mul_f32_e32 v32, 0x41800000, v77
	v_cvt_pk_fp8_f32 v31, v0, v32 op_sel:[0,0,1]
	v_pk_fma_f32 v[32:33], v[72:73], s[18:19], v[234:235] op_sel_hi:[1,0,1]
	v_pk_fma_f32 v[70:71], v[70:71], s[18:19], v[232:233] op_sel_hi:[1,0,1]
	v_pk_fma_f32 v[66:67], v[66:67], s[18:19], v[236:237] op_sel_hi:[1,0,1]
	v_mul_f32_e32 v0, 0x41800000, v70
	v_mul_f32_e32 v70, 0x41800000, v71
	v_mul_f32_e32 v71, 0x41800000, v32
	v_mov_b32_e32 v32, v171
	v_mul_f32_e32 v72, 0x41800000, v33
	v_cvt_pk_fp8_f32 v32, v0, v70
	v_mul_f32_e32 v0, 0x41800000, v66
	v_mul_f32_e32 v66, 0x41800000, v67
	v_mov_b32_e32 v33, v171
	v_cvt_pk_fp8_f32 v33, v0, v66
	v_pk_fma_f32 v[68:69], v[68:69], s[18:19], v[238:239] op_sel_hi:[1,0,1]
	v_cvt_pk_fp8_f32 v32, v71, v72 op_sel:[0,0,1]
	v_mul_f32_e32 v0, 0x41800000, v68
	v_mul_f32_e32 v66, 0x41800000, v69
	v_cvt_pk_fp8_f32 v33, v0, v66 op_sel:[0,0,1]
	global_store_dwordx2 v[10:11], v[26:27], off offset:128
	global_store_dwordx2 v[12:13], v[28:29], off offset:128
	global_store_dwordx2 v[14:15], v[30:31], off offset:128
	global_store_dwordx2 v[16:17], v[32:33], off offset:128
	v_pk_fma_f32 v[10:11], v[64:65], s[18:19], v[234:235] op_sel_hi:[1,0,1]
	v_pk_fma_f32 v[12:13], v[62:63], s[18:19], v[232:233] op_sel_hi:[1,0,1]
	v_pk_fma_f32 v[16:17], v[58:59], s[18:19], v[236:237] op_sel_hi:[1,0,1]
	v_mul_f32_e32 v0, 0x41800000, v12
	v_mul_f32_e32 v12, 0x41800000, v13
	v_mul_f32_e32 v13, 0x41800000, v10
	v_mov_b32_e32 v10, v171
	v_mul_f32_e32 v26, 0x41800000, v11
	v_cvt_pk_fp8_f32 v10, v0, v12
	v_mul_f32_e32 v0, 0x41800000, v16
	v_mul_f32_e32 v12, 0x41800000, v17
	v_mov_b32_e32 v11, v171
	v_cvt_pk_fp8_f32 v11, v0, v12
	v_pk_fma_f32 v[14:15], v[60:61], s[18:19], v[238:239] op_sel_hi:[1,0,1]
	v_cvt_pk_fp8_f32 v10, v13, v26 op_sel:[0,0,1]
	v_mul_f32_e32 v0, 0x41800000, v14
	v_mul_f32_e32 v12, 0x41800000, v15
	v_cvt_pk_fp8_f32 v11, v0, v12 op_sel:[0,0,1]
	v_pk_fma_f32 v[12:13], v[56:57], s[18:19], v[234:235] op_sel_hi:[1,0,1]
	v_pk_fma_f32 v[14:15], v[54:55], s[18:19], v[232:233] op_sel_hi:[1,0,1]
	v_pk_fma_f32 v[26:27], v[50:51], s[18:19], v[236:237] op_sel_hi:[1,0,1]
	v_mul_f32_e32 v0, 0x41800000, v14
	v_mul_f32_e32 v14, 0x41800000, v15
	v_mul_f32_e32 v15, 0x41800000, v12
	v_mov_b32_e32 v12, v171
	v_mul_f32_e32 v28, 0x41800000, v13
	v_cvt_pk_fp8_f32 v12, v0, v14
	v_mul_f32_e32 v0, 0x41800000, v26
	v_mul_f32_e32 v14, 0x41800000, v27
	v_mov_b32_e32 v13, v171
	v_cvt_pk_fp8_f32 v13, v0, v14
	v_pk_fma_f32 v[16:17], v[52:53], s[18:19], v[238:239] op_sel_hi:[1,0,1]
	v_cvt_pk_fp8_f32 v12, v15, v28 op_sel:[0,0,1]
	v_mul_f32_e32 v0, 0x41800000, v16
	v_mul_f32_e32 v14, 0x41800000, v17
	v_cvt_pk_fp8_f32 v13, v0, v14 op_sel:[0,0,1]
	v_pk_fma_f32 v[14:15], v[48:49], s[18:19], v[234:235] op_sel_hi:[1,0,1]
	v_pk_fma_f32 v[16:17], v[46:47], s[18:19], v[232:233] op_sel_hi:[1,0,1]
	v_pk_fma_f32 v[28:29], v[42:43], s[18:19], v[236:237] op_sel_hi:[1,0,1]
	v_mul_f32_e32 v0, 0x41800000, v16
	v_mul_f32_e32 v16, 0x41800000, v17
	v_mul_f32_e32 v17, 0x41800000, v14
	v_mov_b32_e32 v14, v171
	v_mul_f32_e32 v30, 0x41800000, v15
	v_cvt_pk_fp8_f32 v14, v0, v16
	v_mul_f32_e32 v0, 0x41800000, v28
	v_mul_f32_e32 v16, 0x41800000, v29
	v_mov_b32_e32 v15, v171
	v_cvt_pk_fp8_f32 v15, v0, v16
	v_pk_fma_f32 v[26:27], v[44:45], s[18:19], v[238:239] op_sel_hi:[1,0,1]
	v_pk_fma_f32 v[2:3], v[38:39], s[18:19], v[232:233] op_sel_hi:[1,0,1]
	v_mul_f32_e32 v0, 0x41800000, v26
	v_mul_f32_e32 v16, 0x41800000, v27
	v_cvt_pk_fp8_f32 v15, v0, v16 op_sel:[0,0,1]
	v_pk_fma_f32 v[6:7], v[34:35], s[18:19], v[236:237] op_sel_hi:[1,0,1]
	v_mul_f32_e32 v0, 0x41800000, v2
	v_mul_f32_e32 v3, 0x41800000, v3
	v_mov_b32_e32 v2, v171
	v_cvt_pk_fp8_f32 v2, v0, v3
	v_mul_f32_e32 v0, 0x41800000, v6
	v_mul_f32_e32 v6, 0x41800000, v7
	v_mov_b32_e32 v3, v171
	v_cvt_pk_fp8_f32 v3, v0, v6
	v_pk_fma_f32 v[4:5], v[40:41], s[18:19], v[234:235] op_sel_hi:[1,0,1]
	v_pk_fma_f32 v[8:9], v[36:37], s[18:19], v[238:239] op_sel_hi:[1,0,1]
	v_mul_f32_e32 v4, 0x41800000, v4
	v_mul_f32_e32 v5, 0x41800000, v5
	v_cvt_pk_fp8_f32 v14, v17, v30 op_sel:[0,0,1]
	v_cvt_pk_fp8_f32 v2, v4, v5 op_sel:[0,0,1]
	v_mul_f32_e32 v0, 0x41800000, v8
	v_mul_f32_e32 v4, 0x41800000, v9
	v_cvt_pk_fp8_f32 v3, v0, v4 op_sel:[0,0,1]
	global_store_dwordx2 v[18:19], v[10:11], off offset:128
	global_store_dwordx2 v[20:21], v[12:13], off offset:128
	global_store_dwordx2 v[22:23], v[14:15], off offset:128
	global_store_dwordx2 v[24:25], v[2:3], off offset:128
	s_cbranch_vccnz .LBB0_1565
	s_andn2_b64 vcc, exec, s[10:11]
	s_cbranch_vccnz .LBB0_1564
	s_barrier
	s_branch .LBB0_1564
